# pair sweep: no refills past the last row, DMA prologue issued before the h2 computation, token A's x1 row kept in registers, token B's reload under A's output
# speedup vs baseline: 1.0698x; 1.0022x over previous
; #define LAS __attribute__((address_space(3)))
; #define P11_CX(J, ASC0, ASC1) do { const unsigned o0_ = (unsigned)__shfl_xor((int)k0, (J)), o1_ = (unsigned)__shfl_xor((int)k1, (J)); const bool lowl_ = (lane & (J)) == 0; \
;         k0 = (lowl_ == (ASC0)) ? (k0 < o0_ ? k0 : o0_) : (k0 > o0_ ? k0 : o0_); k1 = (lowl_ == (ASC1)) ? (k1 < o1_ ? k1 : o1_) : (k1 > o1_ ? k1 : o1_); } while (0)
; DI void peer_token(LAS unsigned char* ring, const bf16* x1row, float inv2, const float* nffn, const int* ex, const float* pg, const unsigned char* U6, const unsigned char* V6,
;                    const float* usc, const float* vsc, float* orow, int lane) {
;     unsigned k0 = ((unsigned)__hip_atomic_load(ex + lane, __ATOMIC_RELAXED, __HIP_MEMORY_SCOPE_AGENT) << 7) | (unsigned)lane;
;     unsigned k1 = ((unsigned)__hip_atomic_load(ex + 64 + lane, __ATOMIC_RELAXED, __HIP_MEMORY_SCOPE_AGENT) << 7) | (unsigned)(64 + lane);
;     ...
; #pragma unroll
;     for (int kk = 2; kk <= 32; kk <<= 1) { const bool asc = (lane & kk) == 0;
; #pragma unroll
;         for (int j = kk >> 1; j >= 1; j >>= 1) P11_CX(j, asc, asc); }
; #pragma unroll
;     for (int j = 32; j >= 1; j >>= 1) P11_CX(j, true, false);
;     { const unsigned lo_ = k0 < k1 ? k0 : k1, hi_ = k0 < k1 ? k1 : k0; k0 = lo_; k1 = hi_; }
; #pragma unroll
;     for (int j = 32; j >= 1; j >>= 1) P11_CX(j, true, true);
; __global__ void __launch_bounds__(NTHREADS, 2) fwd(Args args) {
;     ...
;             for (int j = 0; j < 4; ++j) { const int t = tb * 32 + wave * 4 + j;
;                 peer_token(lds + wave * (4 * RSLOT), XB + (size_t)t * DM, inv2[t], norm_ffn, experts + (size_t)t * 128, pgates + (size_t)t * 128, U8, V8, usc, vsc, out + (size_t)t * DM, lane); }
.LBB0_901:
	s_lshl_b32 s46, s76, 1
	s_add_i32 s46, s46, s97
	s_ashr_i32 s47, s46, 31
	s_lshl_b64 s[44:45], s[46:47], 12
	s_lshl_b64 s[74:75], s[46:47], 2
	s_add_u32 s74, s64, s74
	s_addc_u32 s75, s65, s75
	s_lshl_b64 s[78:79], s[46:47], 9
	v_lshl_add_u64 v[2:3], v[78:79], 0, s[78:79]
	s_lshl_b64 s[46:47], s[46:47], 13
	v_lshl_add_u64 v[16:17], v[68:69], 0, s[46:47]
	s_mov_b64 s[46:47], 0x1000
	v_lshl_add_u64 v[18:19], v[16:17], 0, s[46:47]
	s_mov_b64 s[46:47], 0x2000
	v_lshl_add_u64 v[144:145], v[16:17], 0, s[46:47]
	s_mov_b64 s[46:47], 0x3000
	v_lshl_add_u64 v[6:7], v[16:17], 0, s[46:47]
	global_load_dwordx2 v[96:97], v67, s[74:75]
	global_load_dword v112, v[2:3], off sc1
	global_load_dword v113, v[2:3], off offset:256 sc1
	global_load_dword v242, v[2:3], off offset:512 sc1
	global_load_dword v243, v[2:3], off offset:768 sc1
	global_load_dwordx2 v[146:147], v[16:17], off
	global_load_dwordx2 v[148:149], v[16:17], off offset:512
	global_load_dwordx2 v[150:151], v[16:17], off offset:1024
	global_load_dwordx2 v[152:153], v[16:17], off offset:1536
	global_load_dwordx2 v[154:155], v[16:17], off offset:2048
	global_load_dwordx2 v[156:157], v[16:17], off offset:2560
	global_load_dwordx2 v[158:159], v[16:17], off offset:3072
	global_load_dwordx2 v[160:161], v[16:17], off offset:3584
	global_load_dwordx2 v[162:163], v[18:19], off
	global_load_dwordx2 v[164:165], v[18:19], off offset:512
	global_load_dwordx2 v[166:167], v[18:19], off offset:1024
	global_load_dwordx2 v[168:169], v[18:19], off offset:1536
	global_load_dwordx2 v[170:171], v[18:19], off offset:2048
	global_load_dwordx2 v[172:173], v[18:19], off offset:2560
	global_load_dwordx2 v[174:175], v[18:19], off offset:3072
	global_load_dwordx2 v[176:177], v[18:19], off offset:3584
	global_load_dwordx2 v[178:179], v[144:145], off
	global_load_dwordx2 v[180:181], v[144:145], off offset:512
	global_load_dwordx2 v[182:183], v[144:145], off offset:1024
	global_load_dwordx2 v[184:185], v[144:145], off offset:1536
	global_load_dwordx2 v[186:187], v[144:145], off offset:2048
	global_load_dwordx2 v[188:189], v[144:145], off offset:2560
	global_load_dwordx2 v[190:191], v[144:145], off offset:3072
	global_load_dwordx2 v[192:193], v[144:145], off offset:3584
	global_load_dwordx2 v[194:195], v[6:7], off
	global_load_dwordx2 v[196:197], v[6:7], off offset:512
	global_load_dwordx2 v[198:199], v[6:7], off offset:1024
	global_load_dwordx2 v[200:201], v[6:7], off offset:1536
	global_load_dwordx2 v[202:203], v[6:7], off offset:2048
	global_load_dwordx2 v[204:205], v[6:7], off offset:2560
	global_load_dwordx2 v[206:207], v[6:7], off offset:3072
	global_load_dwordx2 v[208:209], v[6:7], off offset:3584
	global_load_dwordx4 v[98:101], v66, s[60:61]
	global_load_dwordx4 v[102:105], v66, s[60:61] offset:1024
	global_load_dwordx4 v[126:129], v66, s[60:61] offset:2048
	global_load_dwordx4 v[130:133], v66, s[60:61] offset:3072
	s_add_u32 s46, s60, 0x1000
	s_addc_u32 s47, s61, 0
	global_load_dwordx4 v[136:139], v66, s[46:47]
	global_load_dwordx4 v[140:143], v66, s[46:47] offset:1024
	global_load_dwordx4 v[8:11], v66, s[46:47] offset:2048
	global_load_dwordx4 v[12:15], v66, s[46:47] offset:3072
	s_add_u32 s46, s60, 0x2000
	s_addc_u32 s47, s61, 0
	global_load_dwordx4 v[210:213], v66, s[46:47]
	global_load_dwordx4 v[214:217], v66, s[46:47] offset:1024
	global_load_dwordx4 v[218:221], v66, s[46:47] offset:2048
	global_load_dwordx4 v[222:225], v66, s[46:47] offset:3072
	s_add_u32 s46, s60, 0x3000
	s_addc_u32 s47, s61, 0
	global_load_dwordx4 v[226:229], v66, s[46:47]
	global_load_dwordx4 v[230:233], v66, s[46:47] offset:1024
	global_load_dwordx4 v[234:237], v66, s[46:47] offset:2048
	global_load_dwordx4 v[238:241], v66, s[46:47] offset:3072
	s_mov_b32 m0, s33
	s_waitcnt vmcnt(48)
	v_lshl_or_b32 v112, v112, 8, v1
	v_lshl_or_b32 v113, v113, 8, v114
	v_or_b32_e32 v6, 0x80, v1
	v_lshl_or_b32 v242, v242, 8, v6
	v_or_b32_e32 v6, 0xc0, v1
	v_lshl_or_b32 v243, v243, 8, v6
	ds_bpermute_b32 v2, v106, v112
	ds_bpermute_b32 v3, v106, v113
	ds_bpermute_b32 v4, v106, v242
	ds_bpermute_b32 v5, v106, v243
	v_and_b32_e32 v6, 3, v118
	v_cmp_eq_u32_e64 s[78:79], 0, v6
	v_cmp_eq_u32_e32 vcc, 3, v6
	s_or_b64 s[74:75], s[78:79], vcc
	s_waitcnt lgkmcnt(3)
	v_min_u32_e32 v6, v112, v2
	v_max_u32_e32 v112, v112, v2
	v_cndmask_b32_e64 v112, v112, v6, s[74:75]
	s_waitcnt lgkmcnt(2)
	v_min_u32_e32 v6, v113, v3
	v_max_u32_e32 v113, v113, v3
	v_cndmask_b32_e64 v113, v113, v6, s[74:75]
	s_waitcnt lgkmcnt(1)
	v_min_u32_e32 v6, v242, v4
	v_max_u32_e32 v242, v242, v4
	v_cndmask_b32_e64 v242, v242, v6, s[74:75]
	s_waitcnt lgkmcnt(0)
	v_min_u32_e32 v6, v243, v5
	v_max_u32_e32 v243, v243, v5
	v_cndmask_b32_e64 v243, v243, v6, s[74:75]
	ds_bpermute_b32 v2, v107, v112
	ds_bpermute_b32 v3, v107, v113
	ds_bpermute_b32 v4, v107, v242
	ds_bpermute_b32 v5, v107, v243
	v_and_b32_e32 v6, 6, v118
	v_cmp_eq_u32_e64 s[78:79], 0, v6
	v_cmp_eq_u32_e32 vcc, 6, v6
	s_or_b64 s[74:75], s[78:79], vcc
	s_waitcnt lgkmcnt(3)
	v_min_u32_e32 v6, v112, v2
	v_max_u32_e32 v112, v112, v2
	v_cndmask_b32_e64 v112, v112, v6, s[74:75]
	s_waitcnt lgkmcnt(2)
	v_min_u32_e32 v6, v113, v3
	v_max_u32_e32 v113, v113, v3
	v_cndmask_b32_e64 v113, v113, v6, s[74:75]
	s_waitcnt lgkmcnt(1)
	v_min_u32_e32 v6, v242, v4
	v_max_u32_e32 v242, v242, v4
	v_cndmask_b32_e64 v242, v242, v6, s[74:75]
	s_waitcnt lgkmcnt(0)
	v_min_u32_e32 v6, v243, v5
	v_max_u32_e32 v243, v243, v5
	v_cndmask_b32_e64 v243, v243, v6, s[74:75]
	ds_bpermute_b32 v2, v106, v112
	ds_bpermute_b32 v3, v106, v113
	ds_bpermute_b32 v4, v106, v242
	ds_bpermute_b32 v5, v106, v243
	v_and_b32_e32 v6, 5, v118
	v_cmp_eq_u32_e64 s[78:79], 0, v6
	v_cmp_eq_u32_e32 vcc, 5, v6
	s_or_b64 s[74:75], s[78:79], vcc
	s_waitcnt lgkmcnt(3)
; #define P11_CX(J, ASC0, ASC1) do { const unsigned o0_ = (unsigned)__shfl_xor((int)k0, (J)), o1_ = (unsigned)__shfl_xor((int)k1, (J)); const bool lowl_ = (lane & (J)) == 0; \
;         k0 = (lowl_ == (ASC0)) ? (k0 < o0_ ? k0 : o0_) : (k0 > o0_ ? k0 : o0_); k1 = (lowl_ == (ASC1)) ? (k1 < o1_ ? k1 : o1_) : (k1 > o1_ ? k1 : o1_); } while (0)
; DI void peer_token(LAS unsigned char* ring, const bf16* x1row, float inv2, const float* nffn, const int* ex, const float* pg, const unsigned char* U6, const unsigned char* V6,
;                    const float* usc, const float* vsc, float* orow, int lane) {
;     ...
; #pragma unroll
;     for (int kk = 2; kk <= 32; kk <<= 1) { const bool asc = (lane & kk) == 0;
; #pragma unroll
;         for (int j = kk >> 1; j >= 1; j >>= 1) P11_CX(j, asc, asc); }
; #pragma unroll
;     for (int j = 32; j >= 1; j >>= 1) P11_CX(j, true, false);
;     { const unsigned lo_ = k0 < k1 ? k0 : k1, hi_ = k0 < k1 ? k1 : k0; k0 = lo_; k1 = hi_; }
; #pragma unroll
;     for (int j = 32; j >= 1; j >>= 1) P11_CX(j, true, true);
	v_min_u32_e32 v6, v112, v2
	v_max_u32_e32 v112, v112, v2
	v_cndmask_b32_e64 v112, v112, v6, s[74:75]
	s_waitcnt lgkmcnt(2)
	v_min_u32_e32 v6, v113, v3
	v_max_u32_e32 v113, v113, v3
	v_cndmask_b32_e64 v113, v113, v6, s[74:75]
	s_waitcnt lgkmcnt(1)
	v_min_u32_e32 v6, v242, v4
	v_max_u32_e32 v242, v242, v4
	v_cndmask_b32_e64 v242, v242, v6, s[74:75]
	s_waitcnt lgkmcnt(0)
	v_min_u32_e32 v6, v243, v5
	v_max_u32_e32 v243, v243, v5
	v_cndmask_b32_e64 v243, v243, v6, s[74:75]
	ds_bpermute_b32 v2, v108, v112
	ds_bpermute_b32 v3, v108, v113
	ds_bpermute_b32 v4, v108, v242
	ds_bpermute_b32 v5, v108, v243
	v_and_b32_e32 v6, 12, v118
	v_cmp_eq_u32_e64 s[78:79], 0, v6
	v_cmp_eq_u32_e32 vcc, 12, v6
	s_or_b64 s[74:75], s[78:79], vcc
	s_waitcnt lgkmcnt(3)
	v_min_u32_e32 v6, v112, v2
	v_max_u32_e32 v112, v112, v2
	v_cndmask_b32_e64 v112, v112, v6, s[74:75]
	s_waitcnt lgkmcnt(2)
	v_min_u32_e32 v6, v113, v3
	v_max_u32_e32 v113, v113, v3
	v_cndmask_b32_e64 v113, v113, v6, s[74:75]
	s_waitcnt lgkmcnt(1)
	v_min_u32_e32 v6, v242, v4
	v_max_u32_e32 v242, v242, v4
	v_cndmask_b32_e64 v242, v242, v6, s[74:75]
	s_waitcnt lgkmcnt(0)
	v_min_u32_e32 v6, v243, v5
	v_max_u32_e32 v243, v243, v5
	v_cndmask_b32_e64 v243, v243, v6, s[74:75]
	ds_bpermute_b32 v2, v107, v112
	ds_bpermute_b32 v3, v107, v113
	ds_bpermute_b32 v4, v107, v242
	ds_bpermute_b32 v5, v107, v243
	v_and_b32_e32 v6, 10, v118
	v_cmp_eq_u32_e64 s[78:79], 0, v6
	v_cmp_eq_u32_e32 vcc, 10, v6
	s_or_b64 s[74:75], s[78:79], vcc
	s_waitcnt lgkmcnt(3)
	v_min_u32_e32 v6, v112, v2
	v_max_u32_e32 v112, v112, v2
	v_cndmask_b32_e64 v112, v112, v6, s[74:75]
	s_waitcnt lgkmcnt(2)
	v_min_u32_e32 v6, v113, v3
	v_max_u32_e32 v113, v113, v3
	v_cndmask_b32_e64 v113, v113, v6, s[74:75]
	s_waitcnt lgkmcnt(1)
	v_min_u32_e32 v6, v242, v4
	v_max_u32_e32 v242, v242, v4
	v_cndmask_b32_e64 v242, v242, v6, s[74:75]
	s_waitcnt lgkmcnt(0)
	v_min_u32_e32 v6, v243, v5
	v_max_u32_e32 v243, v243, v5
	v_cndmask_b32_e64 v243, v243, v6, s[74:75]
	ds_bpermute_b32 v2, v106, v112
	ds_bpermute_b32 v3, v106, v113
	ds_bpermute_b32 v4, v106, v242
	ds_bpermute_b32 v5, v106, v243
	v_and_b32_e32 v6, 9, v118
	v_cmp_eq_u32_e64 s[78:79], 0, v6
	v_cmp_eq_u32_e32 vcc, 9, v6
	s_or_b64 s[74:75], s[78:79], vcc
	s_waitcnt lgkmcnt(3)
	v_min_u32_e32 v6, v112, v2
	v_max_u32_e32 v112, v112, v2
	v_cndmask_b32_e64 v112, v112, v6, s[74:75]
	s_waitcnt lgkmcnt(2)
	v_min_u32_e32 v6, v113, v3
	v_max_u32_e32 v113, v113, v3
	v_cndmask_b32_e64 v113, v113, v6, s[74:75]
	s_waitcnt lgkmcnt(1)
	v_min_u32_e32 v6, v242, v4
	v_max_u32_e32 v242, v242, v4
	v_cndmask_b32_e64 v242, v242, v6, s[74:75]
	s_waitcnt lgkmcnt(0)
	v_min_u32_e32 v6, v243, v5
	v_max_u32_e32 v243, v243, v5
	v_cndmask_b32_e64 v243, v243, v6, s[74:75]
	ds_bpermute_b32 v2, v109, v112
	ds_bpermute_b32 v3, v109, v113
	ds_bpermute_b32 v4, v109, v242
	ds_bpermute_b32 v5, v109, v243
	v_and_b32_e32 v6, 24, v118
	v_cmp_eq_u32_e64 s[78:79], 0, v6
	v_cmp_eq_u32_e32 vcc, 24, v6
	s_or_b64 s[74:75], s[78:79], vcc
	s_waitcnt lgkmcnt(3)
	v_min_u32_e32 v6, v112, v2
	v_max_u32_e32 v112, v112, v2
	v_cndmask_b32_e64 v112, v112, v6, s[74:75]
	s_waitcnt lgkmcnt(2)
	v_min_u32_e32 v6, v113, v3
	v_max_u32_e32 v113, v113, v3
	v_cndmask_b32_e64 v113, v113, v6, s[74:75]
	s_waitcnt lgkmcnt(1)
	v_min_u32_e32 v6, v242, v4
	v_max_u32_e32 v242, v242, v4
	v_cndmask_b32_e64 v242, v242, v6, s[74:75]
	s_waitcnt lgkmcnt(0)
	v_min_u32_e32 v6, v243, v5
	v_max_u32_e32 v243, v243, v5
	v_cndmask_b32_e64 v243, v243, v6, s[74:75]
	ds_bpermute_b32 v2, v108, v112
	ds_bpermute_b32 v3, v108, v113
	ds_bpermute_b32 v4, v108, v242
	ds_bpermute_b32 v5, v108, v243
	v_and_b32_e32 v6, 20, v118
	v_cmp_eq_u32_e64 s[78:79], 0, v6
	v_cmp_eq_u32_e32 vcc, 20, v6
	s_or_b64 s[74:75], s[78:79], vcc
	s_waitcnt lgkmcnt(3)
	v_min_u32_e32 v6, v112, v2
	v_max_u32_e32 v112, v112, v2
	v_cndmask_b32_e64 v112, v112, v6, s[74:75]
	s_waitcnt lgkmcnt(2)
	v_min_u32_e32 v6, v113, v3
	v_max_u32_e32 v113, v113, v3
	v_cndmask_b32_e64 v113, v113, v6, s[74:75]
	s_waitcnt lgkmcnt(1)
	v_min_u32_e32 v6, v242, v4
	v_max_u32_e32 v242, v242, v4
	v_cndmask_b32_e64 v242, v242, v6, s[74:75]
	s_waitcnt lgkmcnt(0)
	v_min_u32_e32 v6, v243, v5
	v_max_u32_e32 v243, v243, v5
	v_cndmask_b32_e64 v243, v243, v6, s[74:75]
	ds_bpermute_b32 v2, v107, v112
	ds_bpermute_b32 v3, v107, v113
	ds_bpermute_b32 v4, v107, v242
	ds_bpermute_b32 v5, v107, v243
	v_and_b32_e32 v6, 18, v118
	v_cmp_eq_u32_e64 s[78:79], 0, v6
	v_cmp_eq_u32_e32 vcc, 18, v6
	s_or_b64 s[74:75], s[78:79], vcc
	s_waitcnt lgkmcnt(3)
	v_min_u32_e32 v6, v112, v2
	v_max_u32_e32 v112, v112, v2
	v_cndmask_b32_e64 v112, v112, v6, s[74:75]
	s_waitcnt lgkmcnt(2)
	v_min_u32_e32 v6, v113, v3
	v_max_u32_e32 v113, v113, v3
	v_cndmask_b32_e64 v113, v113, v6, s[74:75]
	s_waitcnt lgkmcnt(1)
	v_min_u32_e32 v6, v242, v4
	v_max_u32_e32 v242, v242, v4
	v_cndmask_b32_e64 v242, v242, v6, s[74:75]
	s_waitcnt lgkmcnt(0)
	v_min_u32_e32 v6, v243, v5
	v_max_u32_e32 v243, v243, v5
	v_cndmask_b32_e64 v243, v243, v6, s[74:75]
	ds_bpermute_b32 v2, v106, v112
	ds_bpermute_b32 v3, v106, v113
	ds_bpermute_b32 v4, v106, v242
	ds_bpermute_b32 v5, v106, v243
	v_and_b32_e32 v6, 17, v118
	v_cmp_eq_u32_e64 s[78:79], 0, v6
	v_cmp_eq_u32_e32 vcc, 17, v6
	s_or_b64 s[74:75], s[78:79], vcc
	s_waitcnt lgkmcnt(3)
	v_min_u32_e32 v6, v112, v2
	v_max_u32_e32 v112, v112, v2
	v_cndmask_b32_e64 v112, v112, v6, s[74:75]
	s_waitcnt lgkmcnt(2)
	v_min_u32_e32 v6, v113, v3
	v_max_u32_e32 v113, v113, v3
	v_cndmask_b32_e64 v113, v113, v6, s[74:75]
	s_waitcnt lgkmcnt(1)
	v_min_u32_e32 v6, v242, v4
	v_max_u32_e32 v242, v242, v4
	v_cndmask_b32_e64 v242, v242, v6, s[74:75]
	s_waitcnt lgkmcnt(0)
; #define P11_CX(J, ASC0, ASC1) do { const unsigned o0_ = (unsigned)__shfl_xor((int)k0, (J)), o1_ = (unsigned)__shfl_xor((int)k1, (J)); const bool lowl_ = (lane & (J)) == 0; \
;         k0 = (lowl_ == (ASC0)) ? (k0 < o0_ ? k0 : o0_) : (k0 > o0_ ? k0 : o0_); k1 = (lowl_ == (ASC1)) ? (k1 < o1_ ? k1 : o1_) : (k1 > o1_ ? k1 : o1_); } while (0)
; DI void peer_token(LAS unsigned char* ring, const bf16* x1row, float inv2, const float* nffn, const int* ex, const float* pg, const unsigned char* U6, const unsigned char* V6,
;                    const float* usc, const float* vsc, float* orow, int lane) {
;     ...
; #pragma unroll
;     for (int kk = 2; kk <= 32; kk <<= 1) { const bool asc = (lane & kk) == 0;
; #pragma unroll
;         for (int j = kk >> 1; j >= 1; j >>= 1) P11_CX(j, asc, asc); }
; #pragma unroll
;     for (int j = 32; j >= 1; j >>= 1) P11_CX(j, true, false);
;     { const unsigned lo_ = k0 < k1 ? k0 : k1, hi_ = k0 < k1 ? k1 : k0; k0 = lo_; k1 = hi_; }
; #pragma unroll
;     for (int j = 32; j >= 1; j >>= 1) P11_CX(j, true, true);
	v_min_u32_e32 v6, v243, v5
	v_max_u32_e32 v243, v243, v5
	v_cndmask_b32_e64 v243, v243, v6, s[74:75]
	ds_bpermute_b32 v2, v110, v112
	ds_bpermute_b32 v3, v110, v113
	ds_bpermute_b32 v4, v110, v242
	ds_bpermute_b32 v5, v110, v243
	v_and_b32_e32 v6, 48, v118
	v_cmp_eq_u32_e64 s[78:79], 0, v6
	v_cmp_eq_u32_e32 vcc, 48, v6
	s_or_b64 s[74:75], s[78:79], vcc
	s_waitcnt lgkmcnt(3)
	v_min_u32_e32 v6, v112, v2
	v_max_u32_e32 v112, v112, v2
	v_cndmask_b32_e64 v112, v112, v6, s[74:75]
	s_waitcnt lgkmcnt(2)
	v_min_u32_e32 v6, v113, v3
	v_max_u32_e32 v113, v113, v3
	v_cndmask_b32_e64 v113, v113, v6, s[74:75]
	s_waitcnt lgkmcnt(1)
	v_min_u32_e32 v6, v242, v4
	v_max_u32_e32 v242, v242, v4
	v_cndmask_b32_e64 v242, v242, v6, s[74:75]
	s_waitcnt lgkmcnt(0)
	v_min_u32_e32 v6, v243, v5
	v_max_u32_e32 v243, v243, v5
	v_cndmask_b32_e64 v243, v243, v6, s[74:75]
	ds_bpermute_b32 v2, v109, v112
	ds_bpermute_b32 v3, v109, v113
	ds_bpermute_b32 v4, v109, v242
	ds_bpermute_b32 v5, v109, v243
	v_and_b32_e32 v6, 40, v118
	v_cmp_eq_u32_e64 s[78:79], 0, v6
	v_cmp_eq_u32_e32 vcc, 40, v6
	s_or_b64 s[74:75], s[78:79], vcc
	s_waitcnt lgkmcnt(3)
	v_min_u32_e32 v6, v112, v2
	v_max_u32_e32 v112, v112, v2
	v_cndmask_b32_e64 v112, v112, v6, s[74:75]
	s_waitcnt lgkmcnt(2)
	v_min_u32_e32 v6, v113, v3
	v_max_u32_e32 v113, v113, v3
	v_cndmask_b32_e64 v113, v113, v6, s[74:75]
	s_waitcnt lgkmcnt(1)
	v_min_u32_e32 v6, v242, v4
	v_max_u32_e32 v242, v242, v4
	v_cndmask_b32_e64 v242, v242, v6, s[74:75]
	s_waitcnt lgkmcnt(0)
	v_min_u32_e32 v6, v243, v5
	v_max_u32_e32 v243, v243, v5
	v_cndmask_b32_e64 v243, v243, v6, s[74:75]
	ds_bpermute_b32 v2, v108, v112
	ds_bpermute_b32 v3, v108, v113
	ds_bpermute_b32 v4, v108, v242
	ds_bpermute_b32 v5, v108, v243
	v_and_b32_e32 v6, 36, v118
	v_cmp_eq_u32_e64 s[78:79], 0, v6
	v_cmp_eq_u32_e32 vcc, 36, v6
	s_or_b64 s[74:75], s[78:79], vcc
	s_waitcnt lgkmcnt(3)
	v_min_u32_e32 v6, v112, v2
	v_max_u32_e32 v112, v112, v2
	v_cndmask_b32_e64 v112, v112, v6, s[74:75]
	s_waitcnt lgkmcnt(2)
	v_min_u32_e32 v6, v113, v3
	v_max_u32_e32 v113, v113, v3
	v_cndmask_b32_e64 v113, v113, v6, s[74:75]
	s_waitcnt lgkmcnt(1)
	v_min_u32_e32 v6, v242, v4
	v_max_u32_e32 v242, v242, v4
	v_cndmask_b32_e64 v242, v242, v6, s[74:75]
	s_waitcnt lgkmcnt(0)
	v_min_u32_e32 v6, v243, v5
	v_max_u32_e32 v243, v243, v5
	v_cndmask_b32_e64 v243, v243, v6, s[74:75]
	ds_bpermute_b32 v2, v107, v112
	ds_bpermute_b32 v3, v107, v113
	ds_bpermute_b32 v4, v107, v242
	ds_bpermute_b32 v5, v107, v243
	v_and_b32_e32 v6, 34, v118
	v_cmp_eq_u32_e64 s[78:79], 0, v6
	v_cmp_eq_u32_e32 vcc, 34, v6
	s_or_b64 s[74:75], s[78:79], vcc
	s_waitcnt lgkmcnt(3)
	v_min_u32_e32 v6, v112, v2
	v_max_u32_e32 v112, v112, v2
	v_cndmask_b32_e64 v112, v112, v6, s[74:75]
	s_waitcnt lgkmcnt(2)
	v_min_u32_e32 v6, v113, v3
	v_max_u32_e32 v113, v113, v3
	v_cndmask_b32_e64 v113, v113, v6, s[74:75]
	s_waitcnt lgkmcnt(1)
	v_min_u32_e32 v6, v242, v4
	v_max_u32_e32 v242, v242, v4
	v_cndmask_b32_e64 v242, v242, v6, s[74:75]
	s_waitcnt lgkmcnt(0)
	v_min_u32_e32 v6, v243, v5
	v_max_u32_e32 v243, v243, v5
	v_cndmask_b32_e64 v243, v243, v6, s[74:75]
	ds_bpermute_b32 v2, v106, v112
	ds_bpermute_b32 v3, v106, v113
	ds_bpermute_b32 v4, v106, v242
	ds_bpermute_b32 v5, v106, v243
	v_and_b32_e32 v6, 33, v118
	v_cmp_eq_u32_e64 s[78:79], 0, v6
	v_cmp_eq_u32_e32 vcc, 33, v6
	s_or_b64 s[74:75], s[78:79], vcc
	s_waitcnt lgkmcnt(3)
	v_min_u32_e32 v6, v112, v2
	v_max_u32_e32 v112, v112, v2
	v_cndmask_b32_e64 v112, v112, v6, s[74:75]
	s_waitcnt lgkmcnt(2)
	v_min_u32_e32 v6, v113, v3
	v_max_u32_e32 v113, v113, v3
	v_cndmask_b32_e64 v113, v113, v6, s[74:75]
	s_waitcnt lgkmcnt(1)
	v_min_u32_e32 v6, v242, v4
	v_max_u32_e32 v242, v242, v4
	v_cndmask_b32_e64 v242, v242, v6, s[74:75]
	s_waitcnt lgkmcnt(0)
	v_min_u32_e32 v6, v243, v5
	v_max_u32_e32 v243, v243, v5
	v_cndmask_b32_e64 v243, v243, v6, s[74:75]
	ds_bpermute_b32 v2, v111, v112
	ds_bpermute_b32 v3, v111, v113
	ds_bpermute_b32 v4, v111, v242
	ds_bpermute_b32 v5, v111, v243
	v_and_b32_e32 v6, 32, v118
	v_cmp_eq_u32_e64 s[74:75], 0, v6
	s_nop 1
	s_not_b64 s[46:47], s[74:75]
	s_waitcnt lgkmcnt(3)
	v_min_u32_e32 v6, v112, v2
	v_max_u32_e32 v112, v112, v2
	v_cndmask_b32_e64 v112, v112, v6, s[74:75]
	s_waitcnt lgkmcnt(2)
	v_min_u32_e32 v6, v113, v3
	v_max_u32_e32 v113, v113, v3
	v_cndmask_b32_e64 v113, v113, v6, s[46:47]
	s_waitcnt lgkmcnt(1)
	v_min_u32_e32 v6, v242, v4
	v_max_u32_e32 v242, v242, v4
	v_cndmask_b32_e64 v242, v242, v6, s[74:75]
	s_waitcnt lgkmcnt(0)
	v_min_u32_e32 v6, v243, v5
	v_max_u32_e32 v243, v243, v5
	v_cndmask_b32_e64 v243, v243, v6, s[46:47]
	ds_bpermute_b32 v2, v110, v112
	ds_bpermute_b32 v3, v110, v113
	ds_bpermute_b32 v4, v110, v242
	ds_bpermute_b32 v5, v110, v243
	v_and_b32_e32 v6, 16, v118
	v_cmp_eq_u32_e64 s[74:75], 0, v6
	s_nop 1
	s_not_b64 s[46:47], s[74:75]
	s_waitcnt lgkmcnt(3)
	v_min_u32_e32 v6, v112, v2
	v_max_u32_e32 v112, v112, v2
	v_cndmask_b32_e64 v112, v112, v6, s[74:75]
	s_waitcnt lgkmcnt(2)
	v_min_u32_e32 v6, v113, v3
	v_max_u32_e32 v113, v113, v3
	v_cndmask_b32_e64 v113, v113, v6, s[46:47]
	s_waitcnt lgkmcnt(1)
	v_min_u32_e32 v6, v242, v4
	v_max_u32_e32 v242, v242, v4
	v_cndmask_b32_e64 v242, v242, v6, s[74:75]
	s_waitcnt lgkmcnt(0)
	v_min_u32_e32 v6, v243, v5
	v_max_u32_e32 v243, v243, v5
	v_cndmask_b32_e64 v243, v243, v6, s[46:47]
	ds_bpermute_b32 v2, v109, v112
	ds_bpermute_b32 v3, v109, v113
	ds_bpermute_b32 v4, v109, v242
	ds_bpermute_b32 v5, v109, v243
	v_and_b32_e32 v6, 8, v118
	v_cmp_eq_u32_e64 s[74:75], 0, v6
	s_nop 1
	s_not_b64 s[46:47], s[74:75]
	s_waitcnt lgkmcnt(3)
	v_min_u32_e32 v6, v112, v2
	v_max_u32_e32 v112, v112, v2
	v_cndmask_b32_e64 v112, v112, v6, s[74:75]
	s_waitcnt lgkmcnt(2)
; #define P11_CX(J, ASC0, ASC1) do { const unsigned o0_ = (unsigned)__shfl_xor((int)k0, (J)), o1_ = (unsigned)__shfl_xor((int)k1, (J)); const bool lowl_ = (lane & (J)) == 0; \
;         k0 = (lowl_ == (ASC0)) ? (k0 < o0_ ? k0 : o0_) : (k0 > o0_ ? k0 : o0_); k1 = (lowl_ == (ASC1)) ? (k1 < o1_ ? k1 : o1_) : (k1 > o1_ ? k1 : o1_); } while (0)
; DI void peer_token(LAS unsigned char* ring, const bf16* x1row, float inv2, const float* nffn, const int* ex, const float* pg, const unsigned char* U6, const unsigned char* V6,
;                    const float* usc, const float* vsc, float* orow, int lane) {
;     ...
; #pragma unroll
;     for (int kk = 2; kk <= 32; kk <<= 1) { const bool asc = (lane & kk) == 0;
; #pragma unroll
;         for (int j = kk >> 1; j >= 1; j >>= 1) P11_CX(j, asc, asc); }
; #pragma unroll
;     for (int j = 32; j >= 1; j >>= 1) P11_CX(j, true, false);
;     { const unsigned lo_ = k0 < k1 ? k0 : k1, hi_ = k0 < k1 ? k1 : k0; k0 = lo_; k1 = hi_; }
; #pragma unroll
;     for (int j = 32; j >= 1; j >>= 1) P11_CX(j, true, true);
	v_min_u32_e32 v6, v113, v3
	v_max_u32_e32 v113, v113, v3
	v_cndmask_b32_e64 v113, v113, v6, s[46:47]
	s_waitcnt lgkmcnt(1)
	v_min_u32_e32 v6, v242, v4
	v_max_u32_e32 v242, v242, v4
	v_cndmask_b32_e64 v242, v242, v6, s[74:75]
	s_waitcnt lgkmcnt(0)
	v_min_u32_e32 v6, v243, v5
	v_max_u32_e32 v243, v243, v5
	v_cndmask_b32_e64 v243, v243, v6, s[46:47]
	ds_bpermute_b32 v2, v108, v112
	ds_bpermute_b32 v3, v108, v113
	ds_bpermute_b32 v4, v108, v242
	ds_bpermute_b32 v5, v108, v243
	v_and_b32_e32 v6, 4, v118
	v_cmp_eq_u32_e64 s[74:75], 0, v6
	s_nop 1
	s_not_b64 s[46:47], s[74:75]
	s_waitcnt lgkmcnt(3)
	v_min_u32_e32 v6, v112, v2
	v_max_u32_e32 v112, v112, v2
	v_cndmask_b32_e64 v112, v112, v6, s[74:75]
	s_waitcnt lgkmcnt(2)
	v_min_u32_e32 v6, v113, v3
	v_max_u32_e32 v113, v113, v3
	v_cndmask_b32_e64 v113, v113, v6, s[46:47]
	s_waitcnt lgkmcnt(1)
	v_min_u32_e32 v6, v242, v4
	v_max_u32_e32 v242, v242, v4
	v_cndmask_b32_e64 v242, v242, v6, s[74:75]
	s_waitcnt lgkmcnt(0)
	v_min_u32_e32 v6, v243, v5
	v_max_u32_e32 v243, v243, v5
	v_cndmask_b32_e64 v243, v243, v6, s[46:47]
	ds_bpermute_b32 v2, v107, v112
	ds_bpermute_b32 v3, v107, v113
	ds_bpermute_b32 v4, v107, v242
	ds_bpermute_b32 v5, v107, v243
	v_and_b32_e32 v6, 2, v118
	v_cmp_eq_u32_e64 s[74:75], 0, v6
	s_nop 1
	s_not_b64 s[46:47], s[74:75]
	s_waitcnt lgkmcnt(3)
	v_min_u32_e32 v6, v112, v2
	v_max_u32_e32 v112, v112, v2
	v_cndmask_b32_e64 v112, v112, v6, s[74:75]
	s_waitcnt lgkmcnt(2)
	v_min_u32_e32 v6, v113, v3
	v_max_u32_e32 v113, v113, v3
	v_cndmask_b32_e64 v113, v113, v6, s[46:47]
	s_waitcnt lgkmcnt(1)
	v_min_u32_e32 v6, v242, v4
	v_max_u32_e32 v242, v242, v4
	v_cndmask_b32_e64 v242, v242, v6, s[74:75]
	s_waitcnt lgkmcnt(0)
	v_min_u32_e32 v6, v243, v5
	v_max_u32_e32 v243, v243, v5
	v_cndmask_b32_e64 v243, v243, v6, s[46:47]
	ds_bpermute_b32 v2, v106, v112
	ds_bpermute_b32 v3, v106, v113
	ds_bpermute_b32 v4, v106, v242
	ds_bpermute_b32 v5, v106, v243
	v_and_b32_e32 v6, 1, v118
	v_cmp_eq_u32_e64 s[74:75], 0, v6
	s_nop 1
	s_not_b64 s[46:47], s[74:75]
	s_waitcnt lgkmcnt(3)
	v_min_u32_e32 v6, v112, v2
	v_max_u32_e32 v112, v112, v2
	v_cndmask_b32_e64 v112, v112, v6, s[74:75]
	s_waitcnt lgkmcnt(2)
	v_min_u32_e32 v6, v113, v3
	v_max_u32_e32 v113, v113, v3
	v_cndmask_b32_e64 v113, v113, v6, s[46:47]
	s_waitcnt lgkmcnt(1)
	v_min_u32_e32 v6, v242, v4
	v_max_u32_e32 v242, v242, v4
	v_cndmask_b32_e64 v242, v242, v6, s[74:75]
	s_waitcnt lgkmcnt(0)
	v_min_u32_e32 v6, v243, v5
	v_max_u32_e32 v243, v243, v5
	v_cndmask_b32_e64 v243, v243, v6, s[46:47]
	v_min_u32_e32 v6, v112, v113
	v_max_u32_e32 v2, v112, v113
	v_mov_b32_e32 v112, v6
	v_mov_b32_e32 v113, v2
	v_min_u32_e32 v6, v242, v243
	v_max_u32_e32 v2, v242, v243
	v_mov_b32_e32 v242, v2
	v_mov_b32_e32 v243, v6
	ds_bpermute_b32 v2, v111, v112
	ds_bpermute_b32 v3, v111, v113
	ds_bpermute_b32 v4, v111, v242
	ds_bpermute_b32 v5, v111, v243
	v_and_b32_e32 v6, 32, v118
	v_cmp_eq_u32_e64 s[74:75], 0, v6
	s_nop 1
	s_not_b64 s[46:47], s[74:75]
	s_waitcnt lgkmcnt(3)
	v_min_u32_e32 v6, v112, v2
	v_max_u32_e32 v112, v112, v2
	v_cndmask_b32_e64 v112, v112, v6, s[74:75]
	s_waitcnt lgkmcnt(2)
	v_min_u32_e32 v6, v113, v3
	v_max_u32_e32 v113, v113, v3
	v_cndmask_b32_e64 v113, v113, v6, s[74:75]
	s_waitcnt lgkmcnt(1)
	v_min_u32_e32 v6, v242, v4
	v_max_u32_e32 v242, v242, v4
	v_cndmask_b32_e64 v242, v242, v6, s[46:47]
	s_waitcnt lgkmcnt(0)
	v_min_u32_e32 v6, v243, v5
	v_max_u32_e32 v243, v243, v5
	v_cndmask_b32_e64 v243, v243, v6, s[46:47]
	ds_bpermute_b32 v2, v110, v112
	ds_bpermute_b32 v3, v110, v113
	ds_bpermute_b32 v4, v110, v242
	ds_bpermute_b32 v5, v110, v243
	v_and_b32_e32 v6, 16, v118
	v_cmp_eq_u32_e64 s[74:75], 0, v6
	s_nop 1
	s_not_b64 s[46:47], s[74:75]
	s_waitcnt lgkmcnt(3)
	v_min_u32_e32 v6, v112, v2
	v_max_u32_e32 v112, v112, v2
	v_cndmask_b32_e64 v112, v112, v6, s[74:75]
	s_waitcnt lgkmcnt(2)
	v_min_u32_e32 v6, v113, v3
	v_max_u32_e32 v113, v113, v3
	v_cndmask_b32_e64 v113, v113, v6, s[74:75]
	s_waitcnt lgkmcnt(1)
	v_min_u32_e32 v6, v242, v4
	v_max_u32_e32 v242, v242, v4
	v_cndmask_b32_e64 v242, v242, v6, s[46:47]
	s_waitcnt lgkmcnt(0)
	v_min_u32_e32 v6, v243, v5
	v_max_u32_e32 v243, v243, v5
	v_cndmask_b32_e64 v243, v243, v6, s[46:47]
	ds_bpermute_b32 v2, v109, v112
	ds_bpermute_b32 v3, v109, v113
	ds_bpermute_b32 v4, v109, v242
	ds_bpermute_b32 v5, v109, v243
	v_and_b32_e32 v6, 8, v118
	v_cmp_eq_u32_e64 s[74:75], 0, v6
	s_nop 1
	s_not_b64 s[46:47], s[74:75]
	s_waitcnt lgkmcnt(3)
	v_min_u32_e32 v6, v112, v2
	v_max_u32_e32 v112, v112, v2
	v_cndmask_b32_e64 v112, v112, v6, s[74:75]
	s_waitcnt lgkmcnt(2)
	v_min_u32_e32 v6, v113, v3
	v_max_u32_e32 v113, v113, v3
	v_cndmask_b32_e64 v113, v113, v6, s[74:75]
	s_waitcnt lgkmcnt(1)
	v_min_u32_e32 v6, v242, v4
	v_max_u32_e32 v242, v242, v4
	v_cndmask_b32_e64 v242, v242, v6, s[46:47]
	s_waitcnt lgkmcnt(0)
	v_min_u32_e32 v6, v243, v5
	v_max_u32_e32 v243, v243, v5
	v_cndmask_b32_e64 v243, v243, v6, s[46:47]
	ds_bpermute_b32 v2, v108, v112
	ds_bpermute_b32 v3, v108, v113
	ds_bpermute_b32 v4, v108, v242
	ds_bpermute_b32 v5, v108, v243
	v_and_b32_e32 v6, 4, v118
	v_cmp_eq_u32_e64 s[74:75], 0, v6
	s_nop 1
	s_not_b64 s[46:47], s[74:75]
	s_waitcnt lgkmcnt(3)
	v_min_u32_e32 v6, v112, v2
	v_max_u32_e32 v112, v112, v2
	v_cndmask_b32_e64 v112, v112, v6, s[74:75]
	s_waitcnt lgkmcnt(2)
	v_min_u32_e32 v6, v113, v3
	v_max_u32_e32 v113, v113, v3
	v_cndmask_b32_e64 v113, v113, v6, s[74:75]
	s_waitcnt lgkmcnt(1)
	v_min_u32_e32 v6, v242, v4
	v_max_u32_e32 v242, v242, v4
	v_cndmask_b32_e64 v242, v242, v6, s[46:47]
	s_waitcnt lgkmcnt(0)
; #define P11_CX(J, ASC0, ASC1) do { const unsigned o0_ = (unsigned)__shfl_xor((int)k0, (J)), o1_ = (unsigned)__shfl_xor((int)k1, (J)); const bool lowl_ = (lane & (J)) == 0; \
;         k0 = (lowl_ == (ASC0)) ? (k0 < o0_ ? k0 : o0_) : (k0 > o0_ ? k0 : o0_); k1 = (lowl_ == (ASC1)) ? (k1 < o1_ ? k1 : o1_) : (k1 > o1_ ? k1 : o1_); } while (0)
; DI void peer_token(LAS unsigned char* ring, const bf16* x1row, float inv2, const float* nffn, const int* ex, const float* pg, const unsigned char* U6, const unsigned char* V6,
;                    const float* usc, const float* vsc, float* orow, int lane) {
;     ...
; #pragma unroll
;     for (int kk = 2; kk <= 32; kk <<= 1) { const bool asc = (lane & kk) == 0;
; #pragma unroll
;         for (int j = kk >> 1; j >= 1; j >>= 1) P11_CX(j, asc, asc); }
; #pragma unroll
;     for (int j = 32; j >= 1; j >>= 1) P11_CX(j, true, false);
;     { const unsigned lo_ = k0 < k1 ? k0 : k1, hi_ = k0 < k1 ? k1 : k0; k0 = lo_; k1 = hi_; }
; #pragma unroll
;     for (int j = 32; j >= 1; j >>= 1) P11_CX(j, true, true);
	v_min_u32_e32 v6, v243, v5
	v_max_u32_e32 v243, v243, v5
	v_cndmask_b32_e64 v243, v243, v6, s[46:47]
	ds_bpermute_b32 v2, v107, v112
	ds_bpermute_b32 v3, v107, v113
	ds_bpermute_b32 v4, v107, v242
	ds_bpermute_b32 v5, v107, v243
	v_and_b32_e32 v6, 2, v118
	v_cmp_eq_u32_e64 s[74:75], 0, v6
	s_nop 1
	s_not_b64 s[46:47], s[74:75]
	s_waitcnt lgkmcnt(3)
	v_min_u32_e32 v6, v112, v2
	v_max_u32_e32 v112, v112, v2
	v_cndmask_b32_e64 v112, v112, v6, s[74:75]
	s_waitcnt lgkmcnt(2)
	v_min_u32_e32 v6, v113, v3
	v_max_u32_e32 v113, v113, v3
	v_cndmask_b32_e64 v113, v113, v6, s[74:75]
	s_waitcnt lgkmcnt(1)
	v_min_u32_e32 v6, v242, v4
	v_max_u32_e32 v242, v242, v4
	v_cndmask_b32_e64 v242, v242, v6, s[46:47]
	s_waitcnt lgkmcnt(0)
	v_min_u32_e32 v6, v243, v5
	v_max_u32_e32 v243, v243, v5
	v_cndmask_b32_e64 v243, v243, v6, s[46:47]
	ds_bpermute_b32 v2, v106, v112
	ds_bpermute_b32 v3, v106, v113
	ds_bpermute_b32 v4, v106, v242
	ds_bpermute_b32 v5, v106, v243
	v_and_b32_e32 v6, 1, v118
	v_cmp_eq_u32_e64 s[74:75], 0, v6
	s_nop 1
	s_not_b64 s[46:47], s[74:75]
	s_waitcnt lgkmcnt(3)
	v_min_u32_e32 v6, v112, v2
	v_max_u32_e32 v112, v112, v2
	v_cndmask_b32_e64 v112, v112, v6, s[74:75]
	s_waitcnt lgkmcnt(2)
	v_min_u32_e32 v6, v113, v3
	v_max_u32_e32 v113, v113, v3
	v_cndmask_b32_e64 v113, v113, v6, s[74:75]
	s_waitcnt lgkmcnt(1)
	v_min_u32_e32 v6, v242, v4
	v_max_u32_e32 v242, v242, v4
	v_cndmask_b32_e64 v242, v242, v6, s[46:47]
	s_waitcnt lgkmcnt(0)
	v_min_u32_e32 v6, v243, v5
	v_max_u32_e32 v243, v243, v5
	v_cndmask_b32_e64 v243, v243, v6, s[46:47]
	v_min_u32_e32 v6, v112, v242
	v_max_u32_e32 v2, v112, v242
	v_mov_b32_e32 v112, v6
	v_mov_b32_e32 v242, v2
	v_min_u32_e32 v6, v113, v243
	v_max_u32_e32 v2, v113, v243
	v_mov_b32_e32 v113, v6
	v_mov_b32_e32 v243, v2
	v_min_u32_e32 v6, v112, v113
	v_max_u32_e32 v2, v112, v113
	v_mov_b32_e32 v112, v6
	v_mov_b32_e32 v113, v2
	v_min_u32_e32 v6, v242, v243
	v_max_u32_e32 v2, v242, v243
	v_mov_b32_e32 v242, v6
	v_mov_b32_e32 v243, v2
	ds_bpermute_b32 v2, v111, v112
	ds_bpermute_b32 v3, v111, v113
	ds_bpermute_b32 v4, v111, v242
	ds_bpermute_b32 v5, v111, v243
	v_and_b32_e32 v6, 32, v118
	v_cmp_eq_u32_e64 s[74:75], 0, v6
	s_nop 1
	s_not_b64 s[46:47], s[74:75]
	s_waitcnt lgkmcnt(3)
	v_min_u32_e32 v6, v112, v2
	v_max_u32_e32 v112, v112, v2
	v_cndmask_b32_e64 v112, v112, v6, s[74:75]
	s_waitcnt lgkmcnt(2)
	v_min_u32_e32 v6, v113, v3
	v_max_u32_e32 v113, v113, v3
	v_cndmask_b32_e64 v113, v113, v6, s[74:75]
	s_waitcnt lgkmcnt(1)
	v_min_u32_e32 v6, v242, v4
	v_max_u32_e32 v242, v242, v4
	v_cndmask_b32_e64 v242, v242, v6, s[74:75]
	s_waitcnt lgkmcnt(0)
	v_min_u32_e32 v6, v243, v5
	v_max_u32_e32 v243, v243, v5
	v_cndmask_b32_e64 v243, v243, v6, s[74:75]
	ds_bpermute_b32 v2, v110, v112
	ds_bpermute_b32 v3, v110, v113
	ds_bpermute_b32 v4, v110, v242
	ds_bpermute_b32 v5, v110, v243
	v_and_b32_e32 v6, 16, v118
	v_cmp_eq_u32_e64 s[74:75], 0, v6
	s_nop 1
	s_not_b64 s[46:47], s[74:75]
	s_waitcnt lgkmcnt(3)
	v_min_u32_e32 v6, v112, v2
	v_max_u32_e32 v112, v112, v2
	v_cndmask_b32_e64 v112, v112, v6, s[74:75]
	s_waitcnt lgkmcnt(2)
	v_min_u32_e32 v6, v113, v3
	v_max_u32_e32 v113, v113, v3
	v_cndmask_b32_e64 v113, v113, v6, s[74:75]
	s_waitcnt lgkmcnt(1)
	v_min_u32_e32 v6, v242, v4
	v_max_u32_e32 v242, v242, v4
	v_cndmask_b32_e64 v242, v242, v6, s[74:75]
	s_waitcnt lgkmcnt(0)
	v_min_u32_e32 v6, v243, v5
	v_max_u32_e32 v243, v243, v5
	v_cndmask_b32_e64 v243, v243, v6, s[74:75]
	ds_bpermute_b32 v2, v109, v112
	ds_bpermute_b32 v3, v109, v113
	ds_bpermute_b32 v4, v109, v242
	ds_bpermute_b32 v5, v109, v243
	v_and_b32_e32 v6, 8, v118
	v_cmp_eq_u32_e64 s[74:75], 0, v6
	s_nop 1
	s_not_b64 s[46:47], s[74:75]
	s_waitcnt lgkmcnt(3)
	v_min_u32_e32 v6, v112, v2
	v_max_u32_e32 v112, v112, v2
	v_cndmask_b32_e64 v112, v112, v6, s[74:75]
	s_waitcnt lgkmcnt(2)
	v_min_u32_e32 v6, v113, v3
	v_max_u32_e32 v113, v113, v3
	v_cndmask_b32_e64 v113, v113, v6, s[74:75]
	s_waitcnt lgkmcnt(1)
	v_min_u32_e32 v6, v242, v4
	v_max_u32_e32 v242, v242, v4
	v_cndmask_b32_e64 v242, v242, v6, s[74:75]
	s_waitcnt lgkmcnt(0)
	v_min_u32_e32 v6, v243, v5
	v_max_u32_e32 v243, v243, v5
	v_cndmask_b32_e64 v243, v243, v6, s[74:75]
	ds_bpermute_b32 v2, v108, v112
	ds_bpermute_b32 v3, v108, v113
	ds_bpermute_b32 v4, v108, v242
	ds_bpermute_b32 v5, v108, v243
	v_and_b32_e32 v6, 4, v118
	v_cmp_eq_u32_e64 s[74:75], 0, v6
	s_nop 1
	s_not_b64 s[46:47], s[74:75]
	s_waitcnt lgkmcnt(3)
	v_min_u32_e32 v6, v112, v2
	v_max_u32_e32 v112, v112, v2
	v_cndmask_b32_e64 v112, v112, v6, s[74:75]
	s_waitcnt lgkmcnt(2)
	v_min_u32_e32 v6, v113, v3
	v_max_u32_e32 v113, v113, v3
	v_cndmask_b32_e64 v113, v113, v6, s[74:75]
	s_waitcnt lgkmcnt(1)
	v_min_u32_e32 v6, v242, v4
	v_max_u32_e32 v242, v242, v4
	v_cndmask_b32_e64 v242, v242, v6, s[74:75]
	s_waitcnt lgkmcnt(0)
	v_min_u32_e32 v6, v243, v5
	v_max_u32_e32 v243, v243, v5
	v_cndmask_b32_e64 v243, v243, v6, s[74:75]
	ds_bpermute_b32 v2, v107, v112
	ds_bpermute_b32 v3, v107, v113
	ds_bpermute_b32 v4, v107, v242
	ds_bpermute_b32 v5, v107, v243
	v_and_b32_e32 v6, 2, v118
	v_cmp_eq_u32_e64 s[74:75], 0, v6
	s_nop 1
	s_not_b64 s[46:47], s[74:75]
	s_waitcnt lgkmcnt(3)
	v_min_u32_e32 v6, v112, v2
	v_max_u32_e32 v112, v112, v2
	v_cndmask_b32_e64 v112, v112, v6, s[74:75]
	s_waitcnt lgkmcnt(2)
	v_min_u32_e32 v6, v113, v3
	v_max_u32_e32 v113, v113, v3
	v_cndmask_b32_e64 v113, v113, v6, s[74:75]
	s_waitcnt lgkmcnt(1)
	v_min_u32_e32 v6, v242, v4
	v_max_u32_e32 v242, v242, v4
	v_cndmask_b32_e64 v242, v242, v6, s[74:75]
	s_waitcnt lgkmcnt(0)
; #define P11_DMA(gsrc, ldst, NP) do { _Pragma("unroll") for (int _i = 0; _i < (NP); ++_i) \
;     __builtin_amdgcn_global_load_lds((const unsigned*)((gsrc) + _i * 1024), (LAS unsigned*)((ldst) + _i * 1024), 16, 0, 0); } while (0)
; #define P11_CX(J, ASC0, ASC1) do { const unsigned o0_ = (unsigned)__shfl_xor((int)k0, (J)), o1_ = (unsigned)__shfl_xor((int)k1, (J)); const bool lowl_ = (lane & (J)) == 0; \
;         k0 = (lowl_ == (ASC0)) ? (k0 < o0_ ? k0 : o0_) : (k0 > o0_ ? k0 : o0_); k1 = (lowl_ == (ASC1)) ? (k1 < o1_ ? k1 : o1_) : (k1 > o1_ ? k1 : o1_); } while (0)
; DI void peer_token(LAS unsigned char* ring, const bf16* x1row, float inv2, const float* nffn, const int* ex, const float* pg, const unsigned char* U6, const unsigned char* V6,
;                    const float* usc, const float* vsc, float* orow, int lane) {
;     ...
;     for (int j = 32; j >= 1; j >>= 1) P11_CX(j, true, true);
;     ...
;     const int e_lo = (int)(k0 >> 7), e_hi = (int)(k1 >> 7);
;     const float us_lo = usc[e_lo], us_hi = usc[e_hi];
;     const float gv_lo = __hip_atomic_load(pg + (k0 & 127u), __ATOMIC_RELAXED, __HIP_MEMORY_SCOPE_AGENT) * vsc[e_lo], gv_hi = __hip_atomic_load(pg + (k1 & 127u), __ATOMIC_RELAXED, __HIP_MEMORY_SCOPE_AGENT) * vsc[e_hi];
;     f32x2 h2[32], y[32];
;     asm volatile("" : "+s"(nffn));
; #pragma unroll
;     for (int i = 0; i < 16; ++i) {
;         const v2u aw = *(const v2u*)(x1row + i * 256 + lane * 4); const f32x4 g = *(const f32x4*)(nffn + i * 256 + lane * 4);
;         h2[2 * i] = (f32x2){bflo(aw.x) * inv2 * g.x, bfhi(aw.x) * inv2 * g.y}; h2[2 * i + 1] = (f32x2){bflo(aw.y) * inv2 * g.z, bfhi(aw.y) * inv2 * g.w};
;     }
; #pragma unroll
;     for (int i = 0; i < 32; ++i) y[i] = (f32x2){0.f, 0.f};
;     asm volatile("s_waitcnt vmcnt(0)" ::: "memory");
;     const unsigned char* ul = U6 + lane * 16; const unsigned char* vl = V6 + lane * 16;
;     {
; #pragma unroll
;         for (int j = 0; j < 8; ++j) { const int ej = __builtin_amdgcn_readlane(e_lo, j); P11_DMA(ul + (size_t)ej * ROW4, ring + j * ROW4, 2); }
	v_min_u32_e32 v6, v243, v5
	v_max_u32_e32 v243, v243, v5
	v_cndmask_b32_e64 v243, v243, v6, s[74:75]
	ds_bpermute_b32 v2, v106, v112
	ds_bpermute_b32 v3, v106, v113
	ds_bpermute_b32 v4, v106, v242
	ds_bpermute_b32 v5, v106, v243
	v_and_b32_e32 v6, 1, v118
	v_cmp_eq_u32_e64 s[74:75], 0, v6
	s_nop 1
	s_not_b64 s[46:47], s[74:75]
	s_waitcnt lgkmcnt(3)
	v_min_u32_e32 v6, v112, v2
	v_max_u32_e32 v112, v112, v2
	v_cndmask_b32_e64 v112, v112, v6, s[74:75]
	s_waitcnt lgkmcnt(2)
	v_min_u32_e32 v6, v113, v3
	v_max_u32_e32 v113, v113, v3
	v_cndmask_b32_e64 v113, v113, v6, s[74:75]
	s_waitcnt lgkmcnt(1)
	v_min_u32_e32 v6, v242, v4
	v_max_u32_e32 v242, v242, v4
	v_cndmask_b32_e64 v242, v242, v6, s[74:75]
	s_waitcnt lgkmcnt(0)
	v_min_u32_e32 v6, v243, v5
	v_max_u32_e32 v243, v243, v5
	v_cndmask_b32_e64 v243, v243, v6, s[74:75]
	v_and_b32_e32 v6, 0x80, v112
	v_cmp_ne_u32_e64 s[100:101], 0, v6
	v_and_b32_e32 v6, 0x80, v113
	v_cmp_ne_u32_e64 s[50:51], 0, v6
	v_and_b32_e32 v6, 0x80, v242
	v_cmp_ne_u32_e64 s[82:83], 0, v6
	v_and_b32_e32 v6, 0x80, v243
	v_cmp_ne_u32_e64 s[70:71], 0, v6
	s_lshl_b32 s46, s76, 1
	s_add_i32 s46, s46, s97
	s_ashr_i32 s47, s46, 31
	s_lshl_b64 s[78:79], s[46:47], 9
	s_add_u32 s74, s56, s78
	s_addc_u32 s75, s57, s79
	v_lshrrev_b32_e32 v2, 6, v112
	v_and_b32_e32 v2, -4, v2
	v_and_b32_e32 v16, 0xff, v112
	v_lshlrev_b32_e32 v16, 2, v16
	v_lshrrev_b32_e32 v3, 6, v113
	v_and_b32_e32 v3, -4, v3
	v_and_b32_e32 v17, 0xff, v113
	v_lshlrev_b32_e32 v17, 2, v17
	v_lshrrev_b32_e32 v4, 6, v242
	v_and_b32_e32 v4, -4, v4
	v_and_b32_e32 v18, 0xff, v242
	v_lshlrev_b32_e32 v18, 2, v18
	v_lshrrev_b32_e32 v5, 6, v243
	v_and_b32_e32 v5, -4, v5
	v_and_b32_e32 v19, 0xff, v243
	v_lshlrev_b32_e32 v19, 2, v19
	global_load_dword v121, v2, s[52:53]
	global_load_dword v124, v16, s[74:75] sc1
	global_load_dword v115, v2, s[54:55]
	global_load_dword v119, v3, s[52:53]
	global_load_dword v122, v17, s[74:75] sc1
	global_load_dword v116, v3, s[54:55]
	global_load_dword v244, v4, s[52:53]
	global_load_dword v246, v18, s[74:75] sc1
	global_load_dword v71, v4, s[54:55]
	global_load_dword v245, v5, s[52:53]
	global_load_dword v247, v19, s[74:75] sc1
	global_load_dword v135, v5, s[54:55]
	v_readlane_b32 s74, v112, 0
	s_lshr_b32 s74, s74, 8
	s_lshl_b32 s74, s74, 11
	s_mov_b32 s75, 0
	v_lshl_add_u64 v[2:3], v[72:73], 0, s[74:75]
	s_mov_b32 m0, s33
	s_nop 0
	global_load_lds_dwordx4 v[2:3], off
	global_load_lds_dwordx4 v[2:3], off offset:1024
	v_readlane_b32 s74, v112, 1
	s_lshr_b32 s74, s74, 8
	s_lshl_b32 s74, s74, 11
	s_mov_b32 s75, 0
	v_lshl_add_u64 v[2:3], v[72:73], 0, s[74:75]
	s_add_i32 m0, s33, 0x800
	s_nop 0
	global_load_lds_dwordx4 v[2:3], off
	global_load_lds_dwordx4 v[2:3], off offset:1024
	v_readlane_b32 s74, v112, 2
	s_lshr_b32 s74, s74, 8
	s_lshl_b32 s74, s74, 11
	s_mov_b32 s75, 0
	v_lshl_add_u64 v[2:3], v[72:73], 0, s[74:75]
	s_add_i32 m0, s33, 0x1000
	s_nop 0
	global_load_lds_dwordx4 v[2:3], off
	global_load_lds_dwordx4 v[2:3], off offset:1024
	v_readlane_b32 s74, v112, 3
	s_lshr_b32 s74, s74, 8
	s_lshl_b32 s74, s74, 11
	s_mov_b32 s75, 0
	v_lshl_add_u64 v[2:3], v[72:73], 0, s[74:75]
	s_add_i32 m0, s33, 0x1800
	s_nop 0
	global_load_lds_dwordx4 v[2:3], off
	global_load_lds_dwordx4 v[2:3], off offset:1024
	v_readlane_b32 s74, v112, 4
	s_lshr_b32 s74, s74, 8
	s_lshl_b32 s74, s74, 11
	s_mov_b32 s75, 0
	v_lshl_add_u64 v[2:3], v[72:73], 0, s[74:75]
	s_add_i32 m0, s33, 0x2000
	s_nop 0
	global_load_lds_dwordx4 v[2:3], off
	global_load_lds_dwordx4 v[2:3], off offset:1024
	v_readlane_b32 s74, v112, 5
	s_lshr_b32 s74, s74, 8
	s_lshl_b32 s74, s74, 11
	s_mov_b32 s75, 0
	v_lshl_add_u64 v[2:3], v[72:73], 0, s[74:75]
	s_add_i32 m0, s33, 0x2800
	s_nop 0
	global_load_lds_dwordx4 v[2:3], off
	global_load_lds_dwordx4 v[2:3], off offset:1024
	v_readlane_b32 s74, v112, 6
	s_lshr_b32 s74, s74, 8
	s_lshl_b32 s74, s74, 11
	s_mov_b32 s75, 0
	v_lshl_add_u64 v[2:3], v[72:73], 0, s[74:75]
	s_add_i32 m0, s33, 0x3000
	s_nop 0
	global_load_lds_dwordx4 v[2:3], off
	global_load_lds_dwordx4 v[2:3], off offset:1024
	v_readlane_b32 s74, v112, 7
	s_lshr_b32 s74, s74, 8
	s_lshl_b32 s74, s74, 11
	s_mov_b32 s75, 0
	v_lshl_add_u64 v[2:3], v[72:73], 0, s[74:75]
	s_add_i32 m0, s33, 0x3800
	s_nop 0
	global_load_lds_dwordx4 v[2:3], off
	global_load_lds_dwordx4 v[2:3], off offset:1024
	s_waitcnt vmcnt(28)
; DI void peer_token(LAS unsigned char* ring, const bf16* x1row, float inv2, const float* nffn, const int* ex, const float* pg, const unsigned char* U6, const unsigned char* V6,
;                    const float* usc, const float* vsc, float* orow, int lane) {
;     ...
;     f32x2 h2[32], y[32];
;     asm volatile("" : "+s"(nffn));
; #pragma unroll
;     for (int i = 0; i < 16; ++i) {
;         const v2u aw = *(const v2u*)(x1row + i * 256 + lane * 4); const f32x4 g = *(const f32x4*)(nffn + i * 256 + lane * 4);
;         h2[2 * i] = (f32x2){bflo(aw.x) * inv2 * g.x, bfhi(aw.x) * inv2 * g.y}; h2[2 * i + 1] = (f32x2){bflo(aw.y) * inv2 * g.z, bfhi(aw.y) * inv2 * g.w};
;     }
; #pragma unroll
;     for (int i = 0; i < 32; ++i) y[i] = (f32x2){0.f, 0.f};
	v_mov_b32_e32 v134, v97
	v_lshlrev_b32_e32 v2, 16, v146
	v_and_b32_e32 v3, 0xffff0000, v146
	v_lshlrev_b32_e32 v4, 16, v147
	v_and_b32_e32 v5, 0xffff0000, v147
	v_pk_mul_f32 v[2:3], v[96:97], v[2:3] op_sel_hi:[0,1]
	v_pk_mul_f32 v[4:5], v[96:97], v[4:5] op_sel_hi:[0,1]
	v_pk_mul_f32 v[20:21], v[98:99], v[2:3]
	v_pk_mul_f32 v[22:23], v[100:101], v[4:5]
	v_lshlrev_b32_e32 v16, 16, v148
	v_and_b32_e32 v17, 0xffff0000, v148
	v_lshlrev_b32_e32 v18, 16, v149
	v_and_b32_e32 v19, 0xffff0000, v149
	v_pk_mul_f32 v[16:17], v[96:97], v[16:17] op_sel_hi:[0,1]
	v_pk_mul_f32 v[18:19], v[96:97], v[18:19] op_sel_hi:[0,1]
	v_pk_mul_f32 v[24:25], v[102:103], v[16:17]
	v_pk_mul_f32 v[26:27], v[104:105], v[18:19]
	v_lshlrev_b32_e32 v2, 16, v150
	v_and_b32_e32 v3, 0xffff0000, v150
	v_lshlrev_b32_e32 v4, 16, v151
	v_and_b32_e32 v5, 0xffff0000, v151
	v_pk_mul_f32 v[2:3], v[96:97], v[2:3] op_sel_hi:[0,1]
	v_pk_mul_f32 v[4:5], v[96:97], v[4:5] op_sel_hi:[0,1]
	v_pk_mul_f32 v[28:29], v[126:127], v[2:3]
	v_pk_mul_f32 v[30:31], v[128:129], v[4:5]
	v_lshlrev_b32_e32 v16, 16, v152
	v_and_b32_e32 v17, 0xffff0000, v152
	v_lshlrev_b32_e32 v18, 16, v153
	v_and_b32_e32 v19, 0xffff0000, v153
	v_pk_mul_f32 v[16:17], v[96:97], v[16:17] op_sel_hi:[0,1]
	v_pk_mul_f32 v[18:19], v[96:97], v[18:19] op_sel_hi:[0,1]
	v_pk_mul_f32 v[32:33], v[130:131], v[16:17]
	v_pk_mul_f32 v[34:35], v[132:133], v[18:19]
	v_lshlrev_b32_e32 v2, 16, v154
	v_and_b32_e32 v3, 0xffff0000, v154
	v_lshlrev_b32_e32 v4, 16, v155
	v_and_b32_e32 v5, 0xffff0000, v155
	v_pk_mul_f32 v[2:3], v[96:97], v[2:3] op_sel_hi:[0,1]
	v_pk_mul_f32 v[4:5], v[96:97], v[4:5] op_sel_hi:[0,1]
	v_pk_mul_f32 v[36:37], v[136:137], v[2:3]
	v_pk_mul_f32 v[38:39], v[138:139], v[4:5]
	v_lshlrev_b32_e32 v16, 16, v156
	v_and_b32_e32 v17, 0xffff0000, v156
	v_lshlrev_b32_e32 v18, 16, v157
	v_and_b32_e32 v19, 0xffff0000, v157
	v_pk_mul_f32 v[16:17], v[96:97], v[16:17] op_sel_hi:[0,1]
	v_pk_mul_f32 v[18:19], v[96:97], v[18:19] op_sel_hi:[0,1]
	v_pk_mul_f32 v[40:41], v[140:141], v[16:17]
	v_pk_mul_f32 v[42:43], v[142:143], v[18:19]
	v_lshlrev_b32_e32 v2, 16, v158
	v_and_b32_e32 v3, 0xffff0000, v158
	v_lshlrev_b32_e32 v4, 16, v159
	v_and_b32_e32 v5, 0xffff0000, v159
	v_pk_mul_f32 v[2:3], v[96:97], v[2:3] op_sel_hi:[0,1]
	v_pk_mul_f32 v[4:5], v[96:97], v[4:5] op_sel_hi:[0,1]
	v_pk_mul_f32 v[44:45], v[8:9], v[2:3]
	v_pk_mul_f32 v[46:47], v[10:11], v[4:5]
	v_lshlrev_b32_e32 v16, 16, v160
	v_and_b32_e32 v17, 0xffff0000, v160
	v_lshlrev_b32_e32 v18, 16, v161
	v_and_b32_e32 v19, 0xffff0000, v161
	v_pk_mul_f32 v[16:17], v[96:97], v[16:17] op_sel_hi:[0,1]
	v_pk_mul_f32 v[18:19], v[96:97], v[18:19] op_sel_hi:[0,1]
	v_pk_mul_f32 v[48:49], v[12:13], v[16:17]
	v_pk_mul_f32 v[50:51], v[14:15], v[18:19]
	v_lshlrev_b32_e32 v2, 16, v162
	v_and_b32_e32 v3, 0xffff0000, v162
	v_lshlrev_b32_e32 v4, 16, v163
	v_and_b32_e32 v5, 0xffff0000, v163
	v_pk_mul_f32 v[2:3], v[96:97], v[2:3] op_sel_hi:[0,1]
	v_pk_mul_f32 v[4:5], v[96:97], v[4:5] op_sel_hi:[0,1]
	v_pk_mul_f32 v[52:53], v[210:211], v[2:3]
	v_pk_mul_f32 v[54:55], v[212:213], v[4:5]
	v_lshlrev_b32_e32 v16, 16, v164
	v_and_b32_e32 v17, 0xffff0000, v164
	v_lshlrev_b32_e32 v18, 16, v165
	v_and_b32_e32 v19, 0xffff0000, v165
	v_pk_mul_f32 v[16:17], v[96:97], v[16:17] op_sel_hi:[0,1]
	v_pk_mul_f32 v[18:19], v[96:97], v[18:19] op_sel_hi:[0,1]
	v_pk_mul_f32 v[56:57], v[214:215], v[16:17]
	v_pk_mul_f32 v[58:59], v[216:217], v[18:19]
	v_lshlrev_b32_e32 v2, 16, v166
	v_and_b32_e32 v3, 0xffff0000, v166
	v_lshlrev_b32_e32 v4, 16, v167
	v_and_b32_e32 v5, 0xffff0000, v167
	v_pk_mul_f32 v[2:3], v[96:97], v[2:3] op_sel_hi:[0,1]
	v_pk_mul_f32 v[4:5], v[96:97], v[4:5] op_sel_hi:[0,1]
	v_pk_mul_f32 v[60:61], v[218:219], v[2:3]
	v_pk_mul_f32 v[62:63], v[220:221], v[4:5]
	v_lshlrev_b32_e32 v16, 16, v168
	v_and_b32_e32 v17, 0xffff0000, v168
	v_lshlrev_b32_e32 v18, 16, v169
	v_and_b32_e32 v19, 0xffff0000, v169
	v_pk_mul_f32 v[16:17], v[96:97], v[16:17] op_sel_hi:[0,1]
	v_pk_mul_f32 v[18:19], v[96:97], v[18:19] op_sel_hi:[0,1]
	v_pk_mul_f32 v[64:65], v[222:223], v[16:17]
	v_pk_mul_f32 v[80:81], v[224:225], v[18:19]
	v_lshlrev_b32_e32 v2, 16, v170
	v_and_b32_e32 v3, 0xffff0000, v170
	v_lshlrev_b32_e32 v4, 16, v171
	v_and_b32_e32 v5, 0xffff0000, v171
	v_pk_mul_f32 v[2:3], v[96:97], v[2:3] op_sel_hi:[0,1]
	v_pk_mul_f32 v[4:5], v[96:97], v[4:5] op_sel_hi:[0,1]
	v_pk_mul_f32 v[82:83], v[226:227], v[2:3]
	v_pk_mul_f32 v[84:85], v[228:229], v[4:5]
	v_lshlrev_b32_e32 v16, 16, v172
	v_and_b32_e32 v17, 0xffff0000, v172
	v_lshlrev_b32_e32 v18, 16, v173
	v_and_b32_e32 v19, 0xffff0000, v173
	v_pk_mul_f32 v[16:17], v[96:97], v[16:17] op_sel_hi:[0,1]
	v_pk_mul_f32 v[18:19], v[96:97], v[18:19] op_sel_hi:[0,1]
	v_pk_mul_f32 v[86:87], v[230:231], v[16:17]
	v_pk_mul_f32 v[88:89], v[232:233], v[18:19]
	v_lshlrev_b32_e32 v2, 16, v174
	v_and_b32_e32 v3, 0xffff0000, v174
	v_lshlrev_b32_e32 v4, 16, v175
	v_and_b32_e32 v5, 0xffff0000, v175
	v_pk_mul_f32 v[2:3], v[96:97], v[2:3] op_sel_hi:[0,1]
	v_pk_mul_f32 v[4:5], v[96:97], v[4:5] op_sel_hi:[0,1]
	v_pk_mul_f32 v[90:91], v[234:235], v[2:3]
	v_pk_mul_f32 v[92:93], v[236:237], v[4:5]
	v_lshlrev_b32_e32 v16, 16, v176
	v_and_b32_e32 v17, 0xffff0000, v176
	v_lshlrev_b32_e32 v18, 16, v177
	v_and_b32_e32 v19, 0xffff0000, v177
	v_pk_mul_f32 v[16:17], v[96:97], v[16:17] op_sel_hi:[0,1]
	v_pk_mul_f32 v[18:19], v[96:97], v[18:19] op_sel_hi:[0,1]
	v_pk_mul_f32 v[94:95], v[238:239], v[16:17]
	v_pk_mul_f32 v[96:97], v[240:241], v[18:19]
	v_lshlrev_b32_e32 v16, 16, v208
	v_and_b32_e32 v17, 0xffff0000, v208
	v_lshlrev_b32_e32 v18, 16, v209
	v_and_b32_e32 v19, 0xffff0000, v209
	v_pk_mul_f32 v[16:17], v[134:135], v[16:17] op_sel_hi:[0,1]
; #define P11_DMA(gsrc, ldst, NP) do { _Pragma("unroll") for (int _i = 0; _i < (NP); ++_i) \
;     __builtin_amdgcn_global_load_lds((const unsigned*)((gsrc) + _i * 1024), (LAS unsigned*)((ldst) + _i * 1024), 16, 0, 0); } while (0)
; DI void peer_token(LAS unsigned char* ring, const bf16* x1row, float inv2, const float* nffn, const int* ex, const float* pg, const unsigned char* U6, const unsigned char* V6,
;                    const float* usc, const float* vsc, float* orow, int lane) {
;     ...
;     for (int i = 0; i < 16; ++i) {
;         const v2u aw = *(const v2u*)(x1row + i * 256 + lane * 4); const f32x4 g = *(const f32x4*)(nffn + i * 256 + lane * 4);
;         h2[2 * i] = (f32x2){bflo(aw.x) * inv2 * g.x, bfhi(aw.x) * inv2 * g.y}; h2[2 * i + 1] = (f32x2){bflo(aw.y) * inv2 * g.z, bfhi(aw.y) * inv2 * g.w};
;     }
; #pragma unroll
;     for (int i = 0; i < 32; ++i) y[i] = (f32x2){0.f, 0.f};
;     asm volatile("s_waitcnt vmcnt(0)" ::: "memory");
;     const unsigned char* ul = U6 + lane * 16; const unsigned char* vl = V6 + lane * 16;
;     {
; #pragma unroll
;         for (int j = 0; j < 8; ++j) { const int ej = __builtin_amdgcn_readlane(e_lo, j); P11_DMA(ul + (size_t)ej * ROW4, ring + j * ROW4, 2); }
	v_pk_mul_f32 v[18:19], v[134:135], v[18:19] op_sel_hi:[0,1]
	v_pk_mul_f32 v[238:239], v[238:239], v[16:17]
	v_pk_mul_f32 v[240:241], v[240:241], v[18:19]
	v_lshlrev_b32_e32 v2, 16, v206
	v_and_b32_e32 v3, 0xffff0000, v206
	v_lshlrev_b32_e32 v4, 16, v207
	v_and_b32_e32 v5, 0xffff0000, v207
	v_pk_mul_f32 v[2:3], v[134:135], v[2:3] op_sel_hi:[0,1]
	v_pk_mul_f32 v[4:5], v[134:135], v[4:5] op_sel_hi:[0,1]
	v_pk_mul_f32 v[234:235], v[234:235], v[2:3]
	v_pk_mul_f32 v[236:237], v[236:237], v[4:5]
	v_lshlrev_b32_e32 v16, 16, v204
	v_and_b32_e32 v17, 0xffff0000, v204
	v_lshlrev_b32_e32 v18, 16, v205
	v_and_b32_e32 v19, 0xffff0000, v205
	v_pk_mul_f32 v[16:17], v[134:135], v[16:17] op_sel_hi:[0,1]
	v_pk_mul_f32 v[18:19], v[134:135], v[18:19] op_sel_hi:[0,1]
	v_pk_mul_f32 v[230:231], v[230:231], v[16:17]
	v_pk_mul_f32 v[232:233], v[232:233], v[18:19]
	v_lshlrev_b32_e32 v2, 16, v202
	v_and_b32_e32 v3, 0xffff0000, v202
	v_lshlrev_b32_e32 v4, 16, v203
	v_and_b32_e32 v5, 0xffff0000, v203
	v_pk_mul_f32 v[2:3], v[134:135], v[2:3] op_sel_hi:[0,1]
	v_pk_mul_f32 v[4:5], v[134:135], v[4:5] op_sel_hi:[0,1]
	v_pk_mul_f32 v[226:227], v[226:227], v[2:3]
	v_pk_mul_f32 v[228:229], v[228:229], v[4:5]
	v_lshlrev_b32_e32 v16, 16, v200
	v_and_b32_e32 v17, 0xffff0000, v200
	v_lshlrev_b32_e32 v18, 16, v201
	v_and_b32_e32 v19, 0xffff0000, v201
	v_pk_mul_f32 v[16:17], v[134:135], v[16:17] op_sel_hi:[0,1]
	v_pk_mul_f32 v[18:19], v[134:135], v[18:19] op_sel_hi:[0,1]
	v_pk_mul_f32 v[222:223], v[222:223], v[16:17]
	v_pk_mul_f32 v[224:225], v[224:225], v[18:19]
	v_lshlrev_b32_e32 v2, 16, v198
	v_and_b32_e32 v3, 0xffff0000, v198
	v_lshlrev_b32_e32 v4, 16, v199
	v_and_b32_e32 v5, 0xffff0000, v199
	v_pk_mul_f32 v[2:3], v[134:135], v[2:3] op_sel_hi:[0,1]
	v_pk_mul_f32 v[4:5], v[134:135], v[4:5] op_sel_hi:[0,1]
	v_pk_mul_f32 v[218:219], v[218:219], v[2:3]
	v_pk_mul_f32 v[220:221], v[220:221], v[4:5]
	v_lshlrev_b32_e32 v16, 16, v196
	v_and_b32_e32 v17, 0xffff0000, v196
	v_lshlrev_b32_e32 v18, 16, v197
	v_and_b32_e32 v19, 0xffff0000, v197
	v_pk_mul_f32 v[16:17], v[134:135], v[16:17] op_sel_hi:[0,1]
	v_pk_mul_f32 v[18:19], v[134:135], v[18:19] op_sel_hi:[0,1]
	v_pk_mul_f32 v[214:215], v[214:215], v[16:17]
	v_pk_mul_f32 v[216:217], v[216:217], v[18:19]
	v_lshlrev_b32_e32 v2, 16, v194
	v_and_b32_e32 v3, 0xffff0000, v194
	v_lshlrev_b32_e32 v4, 16, v195
	v_and_b32_e32 v5, 0xffff0000, v195
	v_pk_mul_f32 v[2:3], v[134:135], v[2:3] op_sel_hi:[0,1]
	v_pk_mul_f32 v[4:5], v[134:135], v[4:5] op_sel_hi:[0,1]
	v_pk_mul_f32 v[210:211], v[210:211], v[2:3]
	v_pk_mul_f32 v[212:213], v[212:213], v[4:5]
	v_lshlrev_b32_e32 v16, 16, v192
	v_and_b32_e32 v17, 0xffff0000, v192
	v_lshlrev_b32_e32 v18, 16, v193
	v_and_b32_e32 v19, 0xffff0000, v193
	v_pk_mul_f32 v[16:17], v[134:135], v[16:17] op_sel_hi:[0,1]
	v_pk_mul_f32 v[18:19], v[134:135], v[18:19] op_sel_hi:[0,1]
	v_pk_mul_f32 v[206:207], v[12:13], v[16:17]
	v_pk_mul_f32 v[208:209], v[14:15], v[18:19]
	v_lshlrev_b32_e32 v2, 16, v190
	v_and_b32_e32 v3, 0xffff0000, v190
	v_lshlrev_b32_e32 v4, 16, v191
	v_and_b32_e32 v5, 0xffff0000, v191
	v_pk_mul_f32 v[2:3], v[134:135], v[2:3] op_sel_hi:[0,1]
	v_pk_mul_f32 v[4:5], v[134:135], v[4:5] op_sel_hi:[0,1]
	v_pk_mul_f32 v[202:203], v[8:9], v[2:3]
	v_pk_mul_f32 v[204:205], v[10:11], v[4:5]
	v_lshlrev_b32_e32 v16, 16, v188
	v_and_b32_e32 v17, 0xffff0000, v188
	v_lshlrev_b32_e32 v18, 16, v189
	v_and_b32_e32 v19, 0xffff0000, v189
	v_pk_mul_f32 v[16:17], v[134:135], v[16:17] op_sel_hi:[0,1]
	v_pk_mul_f32 v[18:19], v[134:135], v[18:19] op_sel_hi:[0,1]
	v_pk_mul_f32 v[198:199], v[140:141], v[16:17]
	v_pk_mul_f32 v[200:201], v[142:143], v[18:19]
	v_lshlrev_b32_e32 v2, 16, v186
	v_and_b32_e32 v3, 0xffff0000, v186
	v_lshlrev_b32_e32 v4, 16, v187
	v_and_b32_e32 v5, 0xffff0000, v187
	v_pk_mul_f32 v[2:3], v[134:135], v[2:3] op_sel_hi:[0,1]
	v_pk_mul_f32 v[4:5], v[134:135], v[4:5] op_sel_hi:[0,1]
	v_pk_mul_f32 v[194:195], v[136:137], v[2:3]
	v_pk_mul_f32 v[196:197], v[138:139], v[4:5]
	v_lshlrev_b32_e32 v16, 16, v184
	v_and_b32_e32 v17, 0xffff0000, v184
	v_lshlrev_b32_e32 v18, 16, v185
	v_and_b32_e32 v19, 0xffff0000, v185
	v_pk_mul_f32 v[16:17], v[134:135], v[16:17] op_sel_hi:[0,1]
	v_pk_mul_f32 v[18:19], v[134:135], v[18:19] op_sel_hi:[0,1]
	v_pk_mul_f32 v[190:191], v[130:131], v[16:17]
	v_pk_mul_f32 v[192:193], v[132:133], v[18:19]
	v_lshlrev_b32_e32 v2, 16, v182
	v_and_b32_e32 v3, 0xffff0000, v182
	v_lshlrev_b32_e32 v4, 16, v183
	v_and_b32_e32 v5, 0xffff0000, v183
	v_pk_mul_f32 v[2:3], v[134:135], v[2:3] op_sel_hi:[0,1]
	v_pk_mul_f32 v[4:5], v[134:135], v[4:5] op_sel_hi:[0,1]
	v_pk_mul_f32 v[186:187], v[126:127], v[2:3]
	v_pk_mul_f32 v[188:189], v[128:129], v[4:5]
	v_lshlrev_b32_e32 v16, 16, v180
	v_and_b32_e32 v17, 0xffff0000, v180
	v_lshlrev_b32_e32 v18, 16, v181
	v_and_b32_e32 v19, 0xffff0000, v181
	v_pk_mul_f32 v[16:17], v[134:135], v[16:17] op_sel_hi:[0,1]
	v_pk_mul_f32 v[18:19], v[134:135], v[18:19] op_sel_hi:[0,1]
	v_pk_mul_f32 v[182:183], v[102:103], v[16:17]
	v_pk_mul_f32 v[184:185], v[104:105], v[18:19]
	v_lshlrev_b32_e32 v2, 16, v178
	v_and_b32_e32 v3, 0xffff0000, v178
	v_lshlrev_b32_e32 v4, 16, v179
	v_and_b32_e32 v5, 0xffff0000, v179
	v_pk_mul_f32 v[2:3], v[134:135], v[2:3] op_sel_hi:[0,1]
	v_pk_mul_f32 v[4:5], v[134:135], v[4:5] op_sel_hi:[0,1]
	v_pk_mul_f32 v[178:179], v[98:99], v[2:3]
	v_pk_mul_f32 v[180:181], v[100:101], v[4:5]
	s_waitcnt vmcnt(16)
	v_mul_f32_e32 v124, v115, v124
	v_mul_f32_e32 v122, v116, v122
	v_mul_f32_e32 v246, v71, v246
	v_mul_f32_e32 v247, v135, v247
	s_mov_b32 s46, 0
	s_waitcnt vmcnt(14)
	v_add_u32_e32 v4, s33, v70
	ds_read_b128 v[98:101], v4
	ds_read_b128 v[102:105], v4 offset:1024
	v_readlane_b32 s78, v112, 8
	s_lshr_b32 s78, s78, 8
	s_lshl_b32 s78, s78, 11
	s_mov_b32 s79, 0
	v_lshl_add_u64 v[2:3], v[72:73], 0, s[78:79]
	s_waitcnt lgkmcnt(0)
	s_mov_b32 m0, s33
	s_nop 0
	global_load_lds_dwordx4 v[2:3], off
	global_load_lds_dwordx4 v[2:3], off offset:1024
	v_mov_b32_e32 v6, 0

.Lpv3_next:
	s_add_i32 s46, s46, 2
	s_cmp_lg_u32 s46, 502
	s_cbranch_scc1 .Lpv3_even
	s_add_i32 s32, s46, 0
	s_bitcmp1_b64 s[70:71], s32
	s_cbranch_scc1 .Lpvt0B
	s_add_i32 s47, s46, 1
	s_and_b32 s47, s47, 7
	s_lshl_b32 s47, s47, 11
	s_add_i32 s77, s33, s47
	v_add_u32_e32 v4, s77, v70
	s_add_i32 s78, s46, 9
	s_and_b32 s75, s78, 63
	v_readlane_b32 s79, v112, s75
	v_readlane_b32 s47, v243, s75
	s_bitcmp1_b32 s78, 6
	s_cselect_b32 s47, s47, s79
	s_lshr_b32 s47, s47, 8
	s_lshl_b32 s47, s47, 11
	s_bitcmp1_b32 s78, 8
	s_cselect_b32 s78, s98, 0
	s_cselect_b32 s79, s99, 0
	s_add_u32 s78, s78, s47
	s_addc_u32 s79, s79, 0
	s_add_i32 s32, s46, 0
	v_readlane_b32 s74, v123, s32
	s_waitcnt vmcnt(14)
	ds_read_b128 v[126:129], v4
	ds_read_b128 v[130:133], v4 offset:1024
	v_lshl_add_u64 v[2:3], v[72:73], 0, s[78:79]
	v_cvt_scalef32_pk_f32_fp4 v[136:137], v98, 1.0
	v_cvt_scalef32_pk_f32_fp4 v[138:139], v98, 1.0 op_sel:[1,0,0]
	v_cvt_scalef32_pk_f32_fp4 v[140:141], v98, 1.0 op_sel:[0,1,0]
	v_cvt_scalef32_pk_f32_fp4 v[142:143], v98, 1.0 op_sel:[1,1,0]
	v_pk_fma_f32 v[94:95], s[74:75], v[136:137], v[94:95] op_sel_hi:[0,1,1]
	v_pk_fma_f32 v[96:97], s[74:75], v[138:139], v[96:97] op_sel_hi:[0,1,1]
	v_pk_fma_f32 v[92:93], s[74:75], v[140:141], v[92:93] op_sel_hi:[0,1,1]
	v_pk_fma_f32 v[90:91], s[74:75], v[142:143], v[90:91] op_sel_hi:[0,1,1]
	v_cvt_scalef32_pk_f32_fp4 v[136:137], v99, 1.0
	v_cvt_scalef32_pk_f32_fp4 v[138:139], v99, 1.0 op_sel:[1,0,0]
	v_cvt_scalef32_pk_f32_fp4 v[140:141], v99, 1.0 op_sel:[0,1,0]
	v_cvt_scalef32_pk_f32_fp4 v[142:143], v99, 1.0 op_sel:[1,1,0]
	v_pk_fma_f32 v[88:89], s[74:75], v[136:137], v[88:89] op_sel_hi:[0,1,1]
	v_pk_fma_f32 v[86:87], s[74:75], v[138:139], v[86:87] op_sel_hi:[0,1,1]
	v_pk_fma_f32 v[84:85], s[74:75], v[140:141], v[84:85] op_sel_hi:[0,1,1]
	v_pk_fma_f32 v[82:83], s[74:75], v[142:143], v[82:83] op_sel_hi:[0,1,1]
	v_cvt_scalef32_pk_f32_fp4 v[136:137], v100, 1.0
	v_cvt_scalef32_pk_f32_fp4 v[138:139], v100, 1.0 op_sel:[1,0,0]
	v_cvt_scalef32_pk_f32_fp4 v[140:141], v100, 1.0 op_sel:[0,1,0]
	v_cvt_scalef32_pk_f32_fp4 v[142:143], v100, 1.0 op_sel:[1,1,0]
	v_pk_fma_f32 v[64:65], s[74:75], v[136:137], v[64:65] op_sel_hi:[0,1,1]
	v_pk_fma_f32 v[80:81], s[74:75], v[138:139], v[80:81] op_sel_hi:[0,1,1]
	v_pk_fma_f32 v[62:63], s[74:75], v[140:141], v[62:63] op_sel_hi:[0,1,1]
	v_pk_fma_f32 v[60:61], s[74:75], v[142:143], v[60:61] op_sel_hi:[0,1,1]
	s_waitcnt lgkmcnt(0)
	s_mov_b32 m0, s77
	s_nop 0
	global_load_lds_dwordx4 v[2:3], off
	global_load_lds_dwordx4 v[2:3], off offset:1024
	v_cvt_scalef32_pk_f32_fp4 v[136:137], v101, 1.0
	v_cvt_scalef32_pk_f32_fp4 v[138:139], v101, 1.0 op_sel:[1,0,0]
	v_cvt_scalef32_pk_f32_fp4 v[140:141], v101, 1.0 op_sel:[0,1,0]
	v_cvt_scalef32_pk_f32_fp4 v[142:143], v101, 1.0 op_sel:[1,1,0]
	v_pk_fma_f32 v[58:59], s[74:75], v[136:137], v[58:59] op_sel_hi:[0,1,1]
	v_pk_fma_f32 v[56:57], s[74:75], v[138:139], v[56:57] op_sel_hi:[0,1,1]
	v_pk_fma_f32 v[54:55], s[74:75], v[140:141], v[54:55] op_sel_hi:[0,1,1]
	v_pk_fma_f32 v[52:53], s[74:75], v[142:143], v[52:53] op_sel_hi:[0,1,1]
	v_cvt_scalef32_pk_f32_fp4 v[136:137], v102, 1.0
	v_cvt_scalef32_pk_f32_fp4 v[138:139], v102, 1.0 op_sel:[1,0,0]
	v_cvt_scalef32_pk_f32_fp4 v[140:141], v102, 1.0 op_sel:[0,1,0]
	v_cvt_scalef32_pk_f32_fp4 v[142:143], v102, 1.0 op_sel:[1,1,0]
	v_pk_fma_f32 v[50:51], s[74:75], v[136:137], v[50:51] op_sel_hi:[0,1,1]
	v_pk_fma_f32 v[48:49], s[74:75], v[138:139], v[48:49] op_sel_hi:[0,1,1]
	v_pk_fma_f32 v[46:47], s[74:75], v[140:141], v[46:47] op_sel_hi:[0,1,1]
	v_pk_fma_f32 v[44:45], s[74:75], v[142:143], v[44:45] op_sel_hi:[0,1,1]
	v_cvt_scalef32_pk_f32_fp4 v[136:137], v103, 1.0
	v_cvt_scalef32_pk_f32_fp4 v[138:139], v103, 1.0 op_sel:[1,0,0]
	v_cvt_scalef32_pk_f32_fp4 v[140:141], v103, 1.0 op_sel:[0,1,0]
	v_cvt_scalef32_pk_f32_fp4 v[142:143], v103, 1.0 op_sel:[1,1,0]
	v_pk_fma_f32 v[42:43], s[74:75], v[136:137], v[42:43] op_sel_hi:[0,1,1]
	v_pk_fma_f32 v[40:41], s[74:75], v[138:139], v[40:41] op_sel_hi:[0,1,1]
	v_pk_fma_f32 v[38:39], s[74:75], v[140:141], v[38:39] op_sel_hi:[0,1,1]
	v_pk_fma_f32 v[36:37], s[74:75], v[142:143], v[36:37] op_sel_hi:[0,1,1]
	v_cvt_scalef32_pk_f32_fp4 v[136:137], v104, 1.0
	v_cvt_scalef32_pk_f32_fp4 v[138:139], v104, 1.0 op_sel:[1,0,0]
	v_cvt_scalef32_pk_f32_fp4 v[140:141], v104, 1.0 op_sel:[0,1,0]
	v_cvt_scalef32_pk_f32_fp4 v[142:143], v104, 1.0 op_sel:[1,1,0]
	v_pk_fma_f32 v[32:33], s[74:75], v[136:137], v[32:33] op_sel_hi:[0,1,1]
	v_pk_fma_f32 v[34:35], s[74:75], v[138:139], v[34:35] op_sel_hi:[0,1,1]
	v_pk_fma_f32 v[30:31], s[74:75], v[140:141], v[30:31] op_sel_hi:[0,1,1]
	v_pk_fma_f32 v[28:29], s[74:75], v[142:143], v[28:29] op_sel_hi:[0,1,1]
	v_cvt_scalef32_pk_f32_fp4 v[136:137], v105, 1.0
	v_cvt_scalef32_pk_f32_fp4 v[138:139], v105, 1.0 op_sel:[1,0,0]
	v_cvt_scalef32_pk_f32_fp4 v[140:141], v105, 1.0 op_sel:[0,1,0]
	v_cvt_scalef32_pk_f32_fp4 v[142:143], v105, 1.0 op_sel:[1,1,0]
	v_pk_fma_f32 v[26:27], s[74:75], v[136:137], v[26:27] op_sel_hi:[0,1,1]
	v_pk_fma_f32 v[24:25], s[74:75], v[138:139], v[24:25] op_sel_hi:[0,1,1]
	v_pk_fma_f32 v[20:21], s[74:75], v[140:141], v[20:21] op_sel_hi:[0,1,1]
	v_pk_fma_f32 v[22:23], s[74:75], v[142:143], v[22:23] op_sel_hi:[0,1,1]
	s_branch .Lpvt0E

.Lpvt0E:
	s_add_i32 s32, s46, 1
	s_bitcmp1_b64 s[70:71], s32
	s_cbranch_scc1 .Lpvt1B
	s_add_i32 s47, s46, 2
	s_and_b32 s47, s47, 7
	s_lshl_b32 s47, s47, 11
	s_add_i32 s77, s33, s47
	v_add_u32_e32 v4, s77, v70
	s_add_i32 s32, s46, 1
	v_readlane_b32 s74, v123, s32
	s_waitcnt vmcnt(14)
	ds_read_b128 v[98:101], v4
	ds_read_b128 v[102:105], v4 offset:1024
	v_cvt_scalef32_pk_f32_fp4 v[136:137], v126, 1.0
	v_cvt_scalef32_pk_f32_fp4 v[138:139], v126, 1.0 op_sel:[1,0,0]
	v_cvt_scalef32_pk_f32_fp4 v[140:141], v126, 1.0 op_sel:[0,1,0]
	v_cvt_scalef32_pk_f32_fp4 v[142:143], v126, 1.0 op_sel:[1,1,0]
	v_pk_fma_f32 v[94:95], s[74:75], v[136:137], v[94:95] op_sel_hi:[0,1,1]
	v_pk_fma_f32 v[96:97], s[74:75], v[138:139], v[96:97] op_sel_hi:[0,1,1]
	v_pk_fma_f32 v[92:93], s[74:75], v[140:141], v[92:93] op_sel_hi:[0,1,1]
	v_pk_fma_f32 v[90:91], s[74:75], v[142:143], v[90:91] op_sel_hi:[0,1,1]
	v_cvt_scalef32_pk_f32_fp4 v[136:137], v127, 1.0
	v_cvt_scalef32_pk_f32_fp4 v[138:139], v127, 1.0 op_sel:[1,0,0]
	v_cvt_scalef32_pk_f32_fp4 v[140:141], v127, 1.0 op_sel:[0,1,0]
	v_cvt_scalef32_pk_f32_fp4 v[142:143], v127, 1.0 op_sel:[1,1,0]
	v_pk_fma_f32 v[88:89], s[74:75], v[136:137], v[88:89] op_sel_hi:[0,1,1]
	v_pk_fma_f32 v[86:87], s[74:75], v[138:139], v[86:87] op_sel_hi:[0,1,1]
	v_pk_fma_f32 v[84:85], s[74:75], v[140:141], v[84:85] op_sel_hi:[0,1,1]
	v_pk_fma_f32 v[82:83], s[74:75], v[142:143], v[82:83] op_sel_hi:[0,1,1]
	v_cvt_scalef32_pk_f32_fp4 v[136:137], v128, 1.0
	v_cvt_scalef32_pk_f32_fp4 v[138:139], v128, 1.0 op_sel:[1,0,0]
	v_cvt_scalef32_pk_f32_fp4 v[140:141], v128, 1.0 op_sel:[0,1,0]
	v_cvt_scalef32_pk_f32_fp4 v[142:143], v128, 1.0 op_sel:[1,1,0]
	v_pk_fma_f32 v[64:65], s[74:75], v[136:137], v[64:65] op_sel_hi:[0,1,1]
	v_pk_fma_f32 v[80:81], s[74:75], v[138:139], v[80:81] op_sel_hi:[0,1,1]
	v_pk_fma_f32 v[62:63], s[74:75], v[140:141], v[62:63] op_sel_hi:[0,1,1]
	v_pk_fma_f32 v[60:61], s[74:75], v[142:143], v[60:61] op_sel_hi:[0,1,1]
	s_waitcnt lgkmcnt(0)
	v_cvt_scalef32_pk_f32_fp4 v[136:137], v129, 1.0
	v_cvt_scalef32_pk_f32_fp4 v[138:139], v129, 1.0 op_sel:[1,0,0]
	v_cvt_scalef32_pk_f32_fp4 v[140:141], v129, 1.0 op_sel:[0,1,0]
	v_cvt_scalef32_pk_f32_fp4 v[142:143], v129, 1.0 op_sel:[1,1,0]
	v_pk_fma_f32 v[58:59], s[74:75], v[136:137], v[58:59] op_sel_hi:[0,1,1]
	v_pk_fma_f32 v[56:57], s[74:75], v[138:139], v[56:57] op_sel_hi:[0,1,1]
	v_pk_fma_f32 v[54:55], s[74:75], v[140:141], v[54:55] op_sel_hi:[0,1,1]
	v_pk_fma_f32 v[52:53], s[74:75], v[142:143], v[52:53] op_sel_hi:[0,1,1]
	v_cvt_scalef32_pk_f32_fp4 v[136:137], v130, 1.0
	v_cvt_scalef32_pk_f32_fp4 v[138:139], v130, 1.0 op_sel:[1,0,0]
	v_cvt_scalef32_pk_f32_fp4 v[140:141], v130, 1.0 op_sel:[0,1,0]
	v_cvt_scalef32_pk_f32_fp4 v[142:143], v130, 1.0 op_sel:[1,1,0]
	v_pk_fma_f32 v[50:51], s[74:75], v[136:137], v[50:51] op_sel_hi:[0,1,1]
	v_pk_fma_f32 v[48:49], s[74:75], v[138:139], v[48:49] op_sel_hi:[0,1,1]
	v_pk_fma_f32 v[46:47], s[74:75], v[140:141], v[46:47] op_sel_hi:[0,1,1]
	v_pk_fma_f32 v[44:45], s[74:75], v[142:143], v[44:45] op_sel_hi:[0,1,1]
	v_cvt_scalef32_pk_f32_fp4 v[136:137], v131, 1.0
	v_cvt_scalef32_pk_f32_fp4 v[138:139], v131, 1.0 op_sel:[1,0,0]
	v_cvt_scalef32_pk_f32_fp4 v[140:141], v131, 1.0 op_sel:[0,1,0]
	v_cvt_scalef32_pk_f32_fp4 v[142:143], v131, 1.0 op_sel:[1,1,0]
	v_pk_fma_f32 v[42:43], s[74:75], v[136:137], v[42:43] op_sel_hi:[0,1,1]
	v_pk_fma_f32 v[40:41], s[74:75], v[138:139], v[40:41] op_sel_hi:[0,1,1]
	v_pk_fma_f32 v[38:39], s[74:75], v[140:141], v[38:39] op_sel_hi:[0,1,1]
	v_pk_fma_f32 v[36:37], s[74:75], v[142:143], v[36:37] op_sel_hi:[0,1,1]
	v_cvt_scalef32_pk_f32_fp4 v[136:137], v132, 1.0
	v_cvt_scalef32_pk_f32_fp4 v[138:139], v132, 1.0 op_sel:[1,0,0]
	v_cvt_scalef32_pk_f32_fp4 v[140:141], v132, 1.0 op_sel:[0,1,0]
	v_cvt_scalef32_pk_f32_fp4 v[142:143], v132, 1.0 op_sel:[1,1,0]
	v_pk_fma_f32 v[32:33], s[74:75], v[136:137], v[32:33] op_sel_hi:[0,1,1]
	v_pk_fma_f32 v[34:35], s[74:75], v[138:139], v[34:35] op_sel_hi:[0,1,1]
	v_pk_fma_f32 v[30:31], s[74:75], v[140:141], v[30:31] op_sel_hi:[0,1,1]
	v_pk_fma_f32 v[28:29], s[74:75], v[142:143], v[28:29] op_sel_hi:[0,1,1]
	v_cvt_scalef32_pk_f32_fp4 v[136:137], v133, 1.0
	v_cvt_scalef32_pk_f32_fp4 v[138:139], v133, 1.0 op_sel:[1,0,0]
	v_cvt_scalef32_pk_f32_fp4 v[140:141], v133, 1.0 op_sel:[0,1,0]
	v_cvt_scalef32_pk_f32_fp4 v[142:143], v133, 1.0 op_sel:[1,1,0]
	v_pk_fma_f32 v[26:27], s[74:75], v[136:137], v[26:27] op_sel_hi:[0,1,1]
	v_pk_fma_f32 v[24:25], s[74:75], v[138:139], v[24:25] op_sel_hi:[0,1,1]
	v_pk_fma_f32 v[20:21], s[74:75], v[140:141], v[20:21] op_sel_hi:[0,1,1]
	v_pk_fma_f32 v[22:23], s[74:75], v[142:143], v[22:23] op_sel_hi:[0,1,1]
	s_branch .Lpvt1E
.Lpvt1B:
	s_add_i32 s47, s46, 2
	s_and_b32 s47, s47, 7
	s_lshl_b32 s47, s47, 11
	s_add_i32 s77, s33, s47
	v_add_u32_e32 v4, s77, v70
	s_add_i32 s32, s46, 1
	v_readlane_b32 s74, v123, s32
	s_waitcnt vmcnt(14)
	ds_read_b128 v[98:101], v4
	ds_read_b128 v[102:105], v4 offset:1024
	v_cvt_scalef32_pk_f32_fp4 v[136:137], v126, 1.0
	v_cvt_scalef32_pk_f32_fp4 v[138:139], v126, 1.0 op_sel:[1,0,0]
	v_cvt_scalef32_pk_f32_fp4 v[140:141], v126, 1.0 op_sel:[0,1,0]
	v_cvt_scalef32_pk_f32_fp4 v[142:143], v126, 1.0 op_sel:[1,1,0]
	v_pk_fma_f32 v[178:179], s[74:75], v[136:137], v[178:179] op_sel_hi:[0,1,1]
	v_pk_fma_f32 v[180:181], s[74:75], v[138:139], v[180:181] op_sel_hi:[0,1,1]
	v_pk_fma_f32 v[182:183], s[74:75], v[140:141], v[182:183] op_sel_hi:[0,1,1]
	v_pk_fma_f32 v[184:185], s[74:75], v[142:143], v[184:185] op_sel_hi:[0,1,1]
	v_cvt_scalef32_pk_f32_fp4 v[136:137], v127, 1.0
	v_cvt_scalef32_pk_f32_fp4 v[138:139], v127, 1.0 op_sel:[1,0,0]
	v_cvt_scalef32_pk_f32_fp4 v[140:141], v127, 1.0 op_sel:[0,1,0]
	v_cvt_scalef32_pk_f32_fp4 v[142:143], v127, 1.0 op_sel:[1,1,0]
	v_pk_fma_f32 v[186:187], s[74:75], v[136:137], v[186:187] op_sel_hi:[0,1,1]
	v_pk_fma_f32 v[188:189], s[74:75], v[138:139], v[188:189] op_sel_hi:[0,1,1]
	v_pk_fma_f32 v[190:191], s[74:75], v[140:141], v[190:191] op_sel_hi:[0,1,1]
	v_pk_fma_f32 v[192:193], s[74:75], v[142:143], v[192:193] op_sel_hi:[0,1,1]
	v_cvt_scalef32_pk_f32_fp4 v[136:137], v128, 1.0
	v_cvt_scalef32_pk_f32_fp4 v[138:139], v128, 1.0 op_sel:[1,0,0]
	v_cvt_scalef32_pk_f32_fp4 v[140:141], v128, 1.0 op_sel:[0,1,0]
	v_cvt_scalef32_pk_f32_fp4 v[142:143], v128, 1.0 op_sel:[1,1,0]
	v_pk_fma_f32 v[194:195], s[74:75], v[136:137], v[194:195] op_sel_hi:[0,1,1]
	v_pk_fma_f32 v[196:197], s[74:75], v[138:139], v[196:197] op_sel_hi:[0,1,1]
	v_pk_fma_f32 v[198:199], s[74:75], v[140:141], v[198:199] op_sel_hi:[0,1,1]
	v_pk_fma_f32 v[200:201], s[74:75], v[142:143], v[200:201] op_sel_hi:[0,1,1]
	s_waitcnt lgkmcnt(0)
	v_cvt_scalef32_pk_f32_fp4 v[136:137], v129, 1.0
	v_cvt_scalef32_pk_f32_fp4 v[138:139], v129, 1.0 op_sel:[1,0,0]
	v_cvt_scalef32_pk_f32_fp4 v[140:141], v129, 1.0 op_sel:[0,1,0]
	v_cvt_scalef32_pk_f32_fp4 v[142:143], v129, 1.0 op_sel:[1,1,0]
	v_pk_fma_f32 v[202:203], s[74:75], v[136:137], v[202:203] op_sel_hi:[0,1,1]
	v_pk_fma_f32 v[204:205], s[74:75], v[138:139], v[204:205] op_sel_hi:[0,1,1]
	v_pk_fma_f32 v[206:207], s[74:75], v[140:141], v[206:207] op_sel_hi:[0,1,1]
	v_pk_fma_f32 v[208:209], s[74:75], v[142:143], v[208:209] op_sel_hi:[0,1,1]
	v_cvt_scalef32_pk_f32_fp4 v[136:137], v130, 1.0
	v_cvt_scalef32_pk_f32_fp4 v[138:139], v130, 1.0 op_sel:[1,0,0]
	v_cvt_scalef32_pk_f32_fp4 v[140:141], v130, 1.0 op_sel:[0,1,0]
	v_cvt_scalef32_pk_f32_fp4 v[142:143], v130, 1.0 op_sel:[1,1,0]
	v_pk_fma_f32 v[210:211], s[74:75], v[136:137], v[210:211] op_sel_hi:[0,1,1]
	v_pk_fma_f32 v[212:213], s[74:75], v[138:139], v[212:213] op_sel_hi:[0,1,1]
	v_pk_fma_f32 v[214:215], s[74:75], v[140:141], v[214:215] op_sel_hi:[0,1,1]
	v_pk_fma_f32 v[216:217], s[74:75], v[142:143], v[216:217] op_sel_hi:[0,1,1]
	v_cvt_scalef32_pk_f32_fp4 v[136:137], v131, 1.0
	v_cvt_scalef32_pk_f32_fp4 v[138:139], v131, 1.0 op_sel:[1,0,0]
	v_cvt_scalef32_pk_f32_fp4 v[140:141], v131, 1.0 op_sel:[0,1,0]
	v_cvt_scalef32_pk_f32_fp4 v[142:143], v131, 1.0 op_sel:[1,1,0]
	v_pk_fma_f32 v[218:219], s[74:75], v[136:137], v[218:219] op_sel_hi:[0,1,1]
	v_pk_fma_f32 v[220:221], s[74:75], v[138:139], v[220:221] op_sel_hi:[0,1,1]
	v_pk_fma_f32 v[222:223], s[74:75], v[140:141], v[222:223] op_sel_hi:[0,1,1]
	v_pk_fma_f32 v[224:225], s[74:75], v[142:143], v[224:225] op_sel_hi:[0,1,1]
	v_cvt_scalef32_pk_f32_fp4 v[136:137], v132, 1.0
	v_cvt_scalef32_pk_f32_fp4 v[138:139], v132, 1.0 op_sel:[1,0,0]
	v_cvt_scalef32_pk_f32_fp4 v[140:141], v132, 1.0 op_sel:[0,1,0]
	v_cvt_scalef32_pk_f32_fp4 v[142:143], v132, 1.0 op_sel:[1,1,0]
	v_pk_fma_f32 v[226:227], s[74:75], v[136:137], v[226:227] op_sel_hi:[0,1,1]
	v_pk_fma_f32 v[228:229], s[74:75], v[138:139], v[228:229] op_sel_hi:[0,1,1]
	v_pk_fma_f32 v[230:231], s[74:75], v[140:141], v[230:231] op_sel_hi:[0,1,1]
	v_pk_fma_f32 v[232:233], s[74:75], v[142:143], v[232:233] op_sel_hi:[0,1,1]
	v_cvt_scalef32_pk_f32_fp4 v[136:137], v133, 1.0
	v_cvt_scalef32_pk_f32_fp4 v[138:139], v133, 1.0 op_sel:[1,0,0]
	v_cvt_scalef32_pk_f32_fp4 v[140:141], v133, 1.0 op_sel:[0,1,0]
	v_cvt_scalef32_pk_f32_fp4 v[142:143], v133, 1.0 op_sel:[1,1,0]
	v_pk_fma_f32 v[234:235], s[74:75], v[136:137], v[234:235] op_sel_hi:[0,1,1]
	v_pk_fma_f32 v[236:237], s[74:75], v[138:139], v[236:237] op_sel_hi:[0,1,1]
	v_pk_fma_f32 v[238:239], s[74:75], v[140:141], v[238:239] op_sel_hi:[0,1,1]
	v_pk_fma_f32 v[240:241], s[74:75], v[142:143], v[240:241] op_sel_hi:[0,1,1]
.Lpvt1E:
	s_add_i32 s32, s46, 2
	s_bitcmp1_b64 s[70:71], s32
	s_cbranch_scc1 .Lpvt2B
	s_add_i32 s47, s46, 3
	s_and_b32 s47, s47, 7
	s_lshl_b32 s47, s47, 11
	s_add_i32 s77, s33, s47
	v_add_u32_e32 v4, s77, v70
	s_add_i32 s32, s46, 2
	v_readlane_b32 s74, v123, s32
	s_waitcnt vmcnt(12)
	ds_read_b128 v[126:129], v4
	ds_read_b128 v[130:133], v4 offset:1024
	v_cvt_scalef32_pk_f32_fp4 v[136:137], v98, 1.0
	v_cvt_scalef32_pk_f32_fp4 v[138:139], v98, 1.0 op_sel:[1,0,0]
	v_cvt_scalef32_pk_f32_fp4 v[140:141], v98, 1.0 op_sel:[0,1,0]
	v_cvt_scalef32_pk_f32_fp4 v[142:143], v98, 1.0 op_sel:[1,1,0]
	v_pk_fma_f32 v[94:95], s[74:75], v[136:137], v[94:95] op_sel_hi:[0,1,1]
	v_pk_fma_f32 v[96:97], s[74:75], v[138:139], v[96:97] op_sel_hi:[0,1,1]
	v_pk_fma_f32 v[92:93], s[74:75], v[140:141], v[92:93] op_sel_hi:[0,1,1]
	v_pk_fma_f32 v[90:91], s[74:75], v[142:143], v[90:91] op_sel_hi:[0,1,1]
	v_cvt_scalef32_pk_f32_fp4 v[136:137], v99, 1.0
	v_cvt_scalef32_pk_f32_fp4 v[138:139], v99, 1.0 op_sel:[1,0,0]
	v_cvt_scalef32_pk_f32_fp4 v[140:141], v99, 1.0 op_sel:[0,1,0]
	v_cvt_scalef32_pk_f32_fp4 v[142:143], v99, 1.0 op_sel:[1,1,0]
	v_pk_fma_f32 v[88:89], s[74:75], v[136:137], v[88:89] op_sel_hi:[0,1,1]
	v_pk_fma_f32 v[86:87], s[74:75], v[138:139], v[86:87] op_sel_hi:[0,1,1]
	v_pk_fma_f32 v[84:85], s[74:75], v[140:141], v[84:85] op_sel_hi:[0,1,1]
	v_pk_fma_f32 v[82:83], s[74:75], v[142:143], v[82:83] op_sel_hi:[0,1,1]
	v_cvt_scalef32_pk_f32_fp4 v[136:137], v100, 1.0
	v_cvt_scalef32_pk_f32_fp4 v[138:139], v100, 1.0 op_sel:[1,0,0]
	v_cvt_scalef32_pk_f32_fp4 v[140:141], v100, 1.0 op_sel:[0,1,0]
	v_cvt_scalef32_pk_f32_fp4 v[142:143], v100, 1.0 op_sel:[1,1,0]
	v_pk_fma_f32 v[64:65], s[74:75], v[136:137], v[64:65] op_sel_hi:[0,1,1]
	v_pk_fma_f32 v[80:81], s[74:75], v[138:139], v[80:81] op_sel_hi:[0,1,1]
	v_pk_fma_f32 v[62:63], s[74:75], v[140:141], v[62:63] op_sel_hi:[0,1,1]
	v_pk_fma_f32 v[60:61], s[74:75], v[142:143], v[60:61] op_sel_hi:[0,1,1]
	s_waitcnt lgkmcnt(0)
	v_cvt_scalef32_pk_f32_fp4 v[136:137], v101, 1.0
	v_cvt_scalef32_pk_f32_fp4 v[138:139], v101, 1.0 op_sel:[1,0,0]
	v_cvt_scalef32_pk_f32_fp4 v[140:141], v101, 1.0 op_sel:[0,1,0]
	v_cvt_scalef32_pk_f32_fp4 v[142:143], v101, 1.0 op_sel:[1,1,0]
	v_pk_fma_f32 v[58:59], s[74:75], v[136:137], v[58:59] op_sel_hi:[0,1,1]
	v_pk_fma_f32 v[56:57], s[74:75], v[138:139], v[56:57] op_sel_hi:[0,1,1]
	v_pk_fma_f32 v[54:55], s[74:75], v[140:141], v[54:55] op_sel_hi:[0,1,1]
	v_pk_fma_f32 v[52:53], s[74:75], v[142:143], v[52:53] op_sel_hi:[0,1,1]
	v_cvt_scalef32_pk_f32_fp4 v[136:137], v102, 1.0
	v_cvt_scalef32_pk_f32_fp4 v[138:139], v102, 1.0 op_sel:[1,0,0]
	v_cvt_scalef32_pk_f32_fp4 v[140:141], v102, 1.0 op_sel:[0,1,0]
	v_cvt_scalef32_pk_f32_fp4 v[142:143], v102, 1.0 op_sel:[1,1,0]
	v_pk_fma_f32 v[50:51], s[74:75], v[136:137], v[50:51] op_sel_hi:[0,1,1]
	v_pk_fma_f32 v[48:49], s[74:75], v[138:139], v[48:49] op_sel_hi:[0,1,1]
	v_pk_fma_f32 v[46:47], s[74:75], v[140:141], v[46:47] op_sel_hi:[0,1,1]
	v_pk_fma_f32 v[44:45], s[74:75], v[142:143], v[44:45] op_sel_hi:[0,1,1]
	v_cvt_scalef32_pk_f32_fp4 v[136:137], v103, 1.0
	v_cvt_scalef32_pk_f32_fp4 v[138:139], v103, 1.0 op_sel:[1,0,0]
	v_cvt_scalef32_pk_f32_fp4 v[140:141], v103, 1.0 op_sel:[0,1,0]
	v_cvt_scalef32_pk_f32_fp4 v[142:143], v103, 1.0 op_sel:[1,1,0]
	v_pk_fma_f32 v[42:43], s[74:75], v[136:137], v[42:43] op_sel_hi:[0,1,1]
	v_pk_fma_f32 v[40:41], s[74:75], v[138:139], v[40:41] op_sel_hi:[0,1,1]
	v_pk_fma_f32 v[38:39], s[74:75], v[140:141], v[38:39] op_sel_hi:[0,1,1]
	v_pk_fma_f32 v[36:37], s[74:75], v[142:143], v[36:37] op_sel_hi:[0,1,1]
	v_cvt_scalef32_pk_f32_fp4 v[136:137], v104, 1.0
	v_cvt_scalef32_pk_f32_fp4 v[138:139], v104, 1.0 op_sel:[1,0,0]
	v_cvt_scalef32_pk_f32_fp4 v[140:141], v104, 1.0 op_sel:[0,1,0]
	v_cvt_scalef32_pk_f32_fp4 v[142:143], v104, 1.0 op_sel:[1,1,0]
	v_pk_fma_f32 v[32:33], s[74:75], v[136:137], v[32:33] op_sel_hi:[0,1,1]
	v_pk_fma_f32 v[34:35], s[74:75], v[138:139], v[34:35] op_sel_hi:[0,1,1]
	v_pk_fma_f32 v[30:31], s[74:75], v[140:141], v[30:31] op_sel_hi:[0,1,1]
	v_pk_fma_f32 v[28:29], s[74:75], v[142:143], v[28:29] op_sel_hi:[0,1,1]
	v_cvt_scalef32_pk_f32_fp4 v[136:137], v105, 1.0
	v_cvt_scalef32_pk_f32_fp4 v[138:139], v105, 1.0 op_sel:[1,0,0]
	v_cvt_scalef32_pk_f32_fp4 v[140:141], v105, 1.0 op_sel:[0,1,0]
	v_cvt_scalef32_pk_f32_fp4 v[142:143], v105, 1.0 op_sel:[1,1,0]
	v_pk_fma_f32 v[26:27], s[74:75], v[136:137], v[26:27] op_sel_hi:[0,1,1]
	v_pk_fma_f32 v[24:25], s[74:75], v[138:139], v[24:25] op_sel_hi:[0,1,1]
	v_pk_fma_f32 v[20:21], s[74:75], v[140:141], v[20:21] op_sel_hi:[0,1,1]
	v_pk_fma_f32 v[22:23], s[74:75], v[142:143], v[22:23] op_sel_hi:[0,1,1]
	s_branch .Lpvt2E
.Lpvt2B:
	s_add_i32 s47, s46, 3
	s_and_b32 s47, s47, 7
	s_lshl_b32 s47, s47, 11
	s_add_i32 s77, s33, s47
	v_add_u32_e32 v4, s77, v70
	s_add_i32 s32, s46, 2
	v_readlane_b32 s74, v123, s32
	s_waitcnt vmcnt(12)
	ds_read_b128 v[126:129], v4
	ds_read_b128 v[130:133], v4 offset:1024
	v_cvt_scalef32_pk_f32_fp4 v[136:137], v98, 1.0
	v_cvt_scalef32_pk_f32_fp4 v[138:139], v98, 1.0 op_sel:[1,0,0]
	v_cvt_scalef32_pk_f32_fp4 v[140:141], v98, 1.0 op_sel:[0,1,0]
	v_cvt_scalef32_pk_f32_fp4 v[142:143], v98, 1.0 op_sel:[1,1,0]
	v_pk_fma_f32 v[178:179], s[74:75], v[136:137], v[178:179] op_sel_hi:[0,1,1]
	v_pk_fma_f32 v[180:181], s[74:75], v[138:139], v[180:181] op_sel_hi:[0,1,1]
	v_pk_fma_f32 v[182:183], s[74:75], v[140:141], v[182:183] op_sel_hi:[0,1,1]
	v_pk_fma_f32 v[184:185], s[74:75], v[142:143], v[184:185] op_sel_hi:[0,1,1]
	v_cvt_scalef32_pk_f32_fp4 v[136:137], v99, 1.0
	v_cvt_scalef32_pk_f32_fp4 v[138:139], v99, 1.0 op_sel:[1,0,0]
	v_cvt_scalef32_pk_f32_fp4 v[140:141], v99, 1.0 op_sel:[0,1,0]
	v_cvt_scalef32_pk_f32_fp4 v[142:143], v99, 1.0 op_sel:[1,1,0]
	v_pk_fma_f32 v[186:187], s[74:75], v[136:137], v[186:187] op_sel_hi:[0,1,1]
	v_pk_fma_f32 v[188:189], s[74:75], v[138:139], v[188:189] op_sel_hi:[0,1,1]
	v_pk_fma_f32 v[190:191], s[74:75], v[140:141], v[190:191] op_sel_hi:[0,1,1]
	v_pk_fma_f32 v[192:193], s[74:75], v[142:143], v[192:193] op_sel_hi:[0,1,1]
	v_cvt_scalef32_pk_f32_fp4 v[136:137], v100, 1.0
	v_cvt_scalef32_pk_f32_fp4 v[138:139], v100, 1.0 op_sel:[1,0,0]
	v_cvt_scalef32_pk_f32_fp4 v[140:141], v100, 1.0 op_sel:[0,1,0]
	v_cvt_scalef32_pk_f32_fp4 v[142:143], v100, 1.0 op_sel:[1,1,0]
	v_pk_fma_f32 v[194:195], s[74:75], v[136:137], v[194:195] op_sel_hi:[0,1,1]
	v_pk_fma_f32 v[196:197], s[74:75], v[138:139], v[196:197] op_sel_hi:[0,1,1]
	v_pk_fma_f32 v[198:199], s[74:75], v[140:141], v[198:199] op_sel_hi:[0,1,1]
	v_pk_fma_f32 v[200:201], s[74:75], v[142:143], v[200:201] op_sel_hi:[0,1,1]
	s_waitcnt lgkmcnt(0)
	v_cvt_scalef32_pk_f32_fp4 v[136:137], v101, 1.0
	v_cvt_scalef32_pk_f32_fp4 v[138:139], v101, 1.0 op_sel:[1,0,0]
	v_cvt_scalef32_pk_f32_fp4 v[140:141], v101, 1.0 op_sel:[0,1,0]
	v_cvt_scalef32_pk_f32_fp4 v[142:143], v101, 1.0 op_sel:[1,1,0]
	v_pk_fma_f32 v[202:203], s[74:75], v[136:137], v[202:203] op_sel_hi:[0,1,1]
	v_pk_fma_f32 v[204:205], s[74:75], v[138:139], v[204:205] op_sel_hi:[0,1,1]
	v_pk_fma_f32 v[206:207], s[74:75], v[140:141], v[206:207] op_sel_hi:[0,1,1]
	v_pk_fma_f32 v[208:209], s[74:75], v[142:143], v[208:209] op_sel_hi:[0,1,1]
	v_cvt_scalef32_pk_f32_fp4 v[136:137], v102, 1.0
	v_cvt_scalef32_pk_f32_fp4 v[138:139], v102, 1.0 op_sel:[1,0,0]
	v_cvt_scalef32_pk_f32_fp4 v[140:141], v102, 1.0 op_sel:[0,1,0]
	v_cvt_scalef32_pk_f32_fp4 v[142:143], v102, 1.0 op_sel:[1,1,0]
	v_pk_fma_f32 v[210:211], s[74:75], v[136:137], v[210:211] op_sel_hi:[0,1,1]
	v_pk_fma_f32 v[212:213], s[74:75], v[138:139], v[212:213] op_sel_hi:[0,1,1]
	v_pk_fma_f32 v[214:215], s[74:75], v[140:141], v[214:215] op_sel_hi:[0,1,1]
	v_pk_fma_f32 v[216:217], s[74:75], v[142:143], v[216:217] op_sel_hi:[0,1,1]
	v_cvt_scalef32_pk_f32_fp4 v[136:137], v103, 1.0
	v_cvt_scalef32_pk_f32_fp4 v[138:139], v103, 1.0 op_sel:[1,0,0]
	v_cvt_scalef32_pk_f32_fp4 v[140:141], v103, 1.0 op_sel:[0,1,0]
	v_cvt_scalef32_pk_f32_fp4 v[142:143], v103, 1.0 op_sel:[1,1,0]
	v_pk_fma_f32 v[218:219], s[74:75], v[136:137], v[218:219] op_sel_hi:[0,1,1]
	v_pk_fma_f32 v[220:221], s[74:75], v[138:139], v[220:221] op_sel_hi:[0,1,1]
	v_pk_fma_f32 v[222:223], s[74:75], v[140:141], v[222:223] op_sel_hi:[0,1,1]
	v_pk_fma_f32 v[224:225], s[74:75], v[142:143], v[224:225] op_sel_hi:[0,1,1]
	v_cvt_scalef32_pk_f32_fp4 v[136:137], v104, 1.0
	v_cvt_scalef32_pk_f32_fp4 v[138:139], v104, 1.0 op_sel:[1,0,0]
	v_cvt_scalef32_pk_f32_fp4 v[140:141], v104, 1.0 op_sel:[0,1,0]
	v_cvt_scalef32_pk_f32_fp4 v[142:143], v104, 1.0 op_sel:[1,1,0]
	v_pk_fma_f32 v[226:227], s[74:75], v[136:137], v[226:227] op_sel_hi:[0,1,1]
	v_pk_fma_f32 v[228:229], s[74:75], v[138:139], v[228:229] op_sel_hi:[0,1,1]
	v_pk_fma_f32 v[230:231], s[74:75], v[140:141], v[230:231] op_sel_hi:[0,1,1]
	v_pk_fma_f32 v[232:233], s[74:75], v[142:143], v[232:233] op_sel_hi:[0,1,1]
	v_cvt_scalef32_pk_f32_fp4 v[136:137], v105, 1.0
	v_cvt_scalef32_pk_f32_fp4 v[138:139], v105, 1.0 op_sel:[1,0,0]
	v_cvt_scalef32_pk_f32_fp4 v[140:141], v105, 1.0 op_sel:[0,1,0]
	v_cvt_scalef32_pk_f32_fp4 v[142:143], v105, 1.0 op_sel:[1,1,0]
	v_pk_fma_f32 v[234:235], s[74:75], v[136:137], v[234:235] op_sel_hi:[0,1,1]
	v_pk_fma_f32 v[236:237], s[74:75], v[138:139], v[236:237] op_sel_hi:[0,1,1]
	v_pk_fma_f32 v[238:239], s[74:75], v[140:141], v[238:239] op_sel_hi:[0,1,1]
	v_pk_fma_f32 v[240:241], s[74:75], v[142:143], v[240:241] op_sel_hi:[0,1,1]
.Lpvt2E:
	s_add_i32 s32, s46, 3
	s_bitcmp1_b64 s[70:71], s32
	s_cbranch_scc1 .Lpvt3B
	s_add_i32 s47, s46, 4
	s_and_b32 s47, s47, 7
	s_lshl_b32 s47, s47, 11
	s_add_i32 s77, s33, s47
	v_add_u32_e32 v4, s77, v70
	s_add_i32 s32, s46, 3
	v_readlane_b32 s74, v123, s32
	s_waitcnt vmcnt(10)
	ds_read_b128 v[98:101], v4
	ds_read_b128 v[102:105], v4 offset:1024
	v_cvt_scalef32_pk_f32_fp4 v[136:137], v126, 1.0
	v_cvt_scalef32_pk_f32_fp4 v[138:139], v126, 1.0 op_sel:[1,0,0]
	v_cvt_scalef32_pk_f32_fp4 v[140:141], v126, 1.0 op_sel:[0,1,0]
	v_cvt_scalef32_pk_f32_fp4 v[142:143], v126, 1.0 op_sel:[1,1,0]
	v_pk_fma_f32 v[94:95], s[74:75], v[136:137], v[94:95] op_sel_hi:[0,1,1]
	v_pk_fma_f32 v[96:97], s[74:75], v[138:139], v[96:97] op_sel_hi:[0,1,1]
	v_pk_fma_f32 v[92:93], s[74:75], v[140:141], v[92:93] op_sel_hi:[0,1,1]
	v_pk_fma_f32 v[90:91], s[74:75], v[142:143], v[90:91] op_sel_hi:[0,1,1]
	v_cvt_scalef32_pk_f32_fp4 v[136:137], v127, 1.0
	v_cvt_scalef32_pk_f32_fp4 v[138:139], v127, 1.0 op_sel:[1,0,0]
	v_cvt_scalef32_pk_f32_fp4 v[140:141], v127, 1.0 op_sel:[0,1,0]
	v_cvt_scalef32_pk_f32_fp4 v[142:143], v127, 1.0 op_sel:[1,1,0]
	v_pk_fma_f32 v[88:89], s[74:75], v[136:137], v[88:89] op_sel_hi:[0,1,1]
	v_pk_fma_f32 v[86:87], s[74:75], v[138:139], v[86:87] op_sel_hi:[0,1,1]
	v_pk_fma_f32 v[84:85], s[74:75], v[140:141], v[84:85] op_sel_hi:[0,1,1]
	v_pk_fma_f32 v[82:83], s[74:75], v[142:143], v[82:83] op_sel_hi:[0,1,1]
	v_cvt_scalef32_pk_f32_fp4 v[136:137], v128, 1.0
	v_cvt_scalef32_pk_f32_fp4 v[138:139], v128, 1.0 op_sel:[1,0,0]
	v_cvt_scalef32_pk_f32_fp4 v[140:141], v128, 1.0 op_sel:[0,1,0]
	v_cvt_scalef32_pk_f32_fp4 v[142:143], v128, 1.0 op_sel:[1,1,0]
	v_pk_fma_f32 v[64:65], s[74:75], v[136:137], v[64:65] op_sel_hi:[0,1,1]
	v_pk_fma_f32 v[80:81], s[74:75], v[138:139], v[80:81] op_sel_hi:[0,1,1]
	v_pk_fma_f32 v[62:63], s[74:75], v[140:141], v[62:63] op_sel_hi:[0,1,1]
	v_pk_fma_f32 v[60:61], s[74:75], v[142:143], v[60:61] op_sel_hi:[0,1,1]
	s_waitcnt lgkmcnt(0)
	v_cvt_scalef32_pk_f32_fp4 v[136:137], v129, 1.0
	v_cvt_scalef32_pk_f32_fp4 v[138:139], v129, 1.0 op_sel:[1,0,0]
	v_cvt_scalef32_pk_f32_fp4 v[140:141], v129, 1.0 op_sel:[0,1,0]
	v_cvt_scalef32_pk_f32_fp4 v[142:143], v129, 1.0 op_sel:[1,1,0]
	v_pk_fma_f32 v[58:59], s[74:75], v[136:137], v[58:59] op_sel_hi:[0,1,1]
	v_pk_fma_f32 v[56:57], s[74:75], v[138:139], v[56:57] op_sel_hi:[0,1,1]
	v_pk_fma_f32 v[54:55], s[74:75], v[140:141], v[54:55] op_sel_hi:[0,1,1]
	v_pk_fma_f32 v[52:53], s[74:75], v[142:143], v[52:53] op_sel_hi:[0,1,1]
	v_cvt_scalef32_pk_f32_fp4 v[136:137], v130, 1.0
	v_cvt_scalef32_pk_f32_fp4 v[138:139], v130, 1.0 op_sel:[1,0,0]
	v_cvt_scalef32_pk_f32_fp4 v[140:141], v130, 1.0 op_sel:[0,1,0]
	v_cvt_scalef32_pk_f32_fp4 v[142:143], v130, 1.0 op_sel:[1,1,0]
	v_pk_fma_f32 v[50:51], s[74:75], v[136:137], v[50:51] op_sel_hi:[0,1,1]
	v_pk_fma_f32 v[48:49], s[74:75], v[138:139], v[48:49] op_sel_hi:[0,1,1]
	v_pk_fma_f32 v[46:47], s[74:75], v[140:141], v[46:47] op_sel_hi:[0,1,1]
	v_pk_fma_f32 v[44:45], s[74:75], v[142:143], v[44:45] op_sel_hi:[0,1,1]
	v_cvt_scalef32_pk_f32_fp4 v[136:137], v131, 1.0
	v_cvt_scalef32_pk_f32_fp4 v[138:139], v131, 1.0 op_sel:[1,0,0]
	v_cvt_scalef32_pk_f32_fp4 v[140:141], v131, 1.0 op_sel:[0,1,0]
	v_cvt_scalef32_pk_f32_fp4 v[142:143], v131, 1.0 op_sel:[1,1,0]
	v_pk_fma_f32 v[42:43], s[74:75], v[136:137], v[42:43] op_sel_hi:[0,1,1]
	v_pk_fma_f32 v[40:41], s[74:75], v[138:139], v[40:41] op_sel_hi:[0,1,1]
	v_pk_fma_f32 v[38:39], s[74:75], v[140:141], v[38:39] op_sel_hi:[0,1,1]
	v_pk_fma_f32 v[36:37], s[74:75], v[142:143], v[36:37] op_sel_hi:[0,1,1]
	v_cvt_scalef32_pk_f32_fp4 v[136:137], v132, 1.0
	v_cvt_scalef32_pk_f32_fp4 v[138:139], v132, 1.0 op_sel:[1,0,0]
	v_cvt_scalef32_pk_f32_fp4 v[140:141], v132, 1.0 op_sel:[0,1,0]
	v_cvt_scalef32_pk_f32_fp4 v[142:143], v132, 1.0 op_sel:[1,1,0]
	v_pk_fma_f32 v[32:33], s[74:75], v[136:137], v[32:33] op_sel_hi:[0,1,1]
	v_pk_fma_f32 v[34:35], s[74:75], v[138:139], v[34:35] op_sel_hi:[0,1,1]
	v_pk_fma_f32 v[30:31], s[74:75], v[140:141], v[30:31] op_sel_hi:[0,1,1]
	v_pk_fma_f32 v[28:29], s[74:75], v[142:143], v[28:29] op_sel_hi:[0,1,1]
	v_cvt_scalef32_pk_f32_fp4 v[136:137], v133, 1.0
	v_cvt_scalef32_pk_f32_fp4 v[138:139], v133, 1.0 op_sel:[1,0,0]
	v_cvt_scalef32_pk_f32_fp4 v[140:141], v133, 1.0 op_sel:[0,1,0]
	v_cvt_scalef32_pk_f32_fp4 v[142:143], v133, 1.0 op_sel:[1,1,0]
	v_pk_fma_f32 v[26:27], s[74:75], v[136:137], v[26:27] op_sel_hi:[0,1,1]
	v_pk_fma_f32 v[24:25], s[74:75], v[138:139], v[24:25] op_sel_hi:[0,1,1]
	v_pk_fma_f32 v[20:21], s[74:75], v[140:141], v[20:21] op_sel_hi:[0,1,1]
	v_pk_fma_f32 v[22:23], s[74:75], v[142:143], v[22:23] op_sel_hi:[0,1,1]
	s_branch .Lpvt3E
.Lpvt3B:
	s_add_i32 s47, s46, 4
	s_and_b32 s47, s47, 7
	s_lshl_b32 s47, s47, 11
	s_add_i32 s77, s33, s47
	v_add_u32_e32 v4, s77, v70
	s_add_i32 s32, s46, 3
	v_readlane_b32 s74, v123, s32
	s_waitcnt vmcnt(10)
	ds_read_b128 v[98:101], v4
	ds_read_b128 v[102:105], v4 offset:1024
	v_cvt_scalef32_pk_f32_fp4 v[136:137], v126, 1.0
	v_cvt_scalef32_pk_f32_fp4 v[138:139], v126, 1.0 op_sel:[1,0,0]
	v_cvt_scalef32_pk_f32_fp4 v[140:141], v126, 1.0 op_sel:[0,1,0]
	v_cvt_scalef32_pk_f32_fp4 v[142:143], v126, 1.0 op_sel:[1,1,0]
	v_pk_fma_f32 v[178:179], s[74:75], v[136:137], v[178:179] op_sel_hi:[0,1,1]
	v_pk_fma_f32 v[180:181], s[74:75], v[138:139], v[180:181] op_sel_hi:[0,1,1]
	v_pk_fma_f32 v[182:183], s[74:75], v[140:141], v[182:183] op_sel_hi:[0,1,1]
	v_pk_fma_f32 v[184:185], s[74:75], v[142:143], v[184:185] op_sel_hi:[0,1,1]
	v_cvt_scalef32_pk_f32_fp4 v[136:137], v127, 1.0
	v_cvt_scalef32_pk_f32_fp4 v[138:139], v127, 1.0 op_sel:[1,0,0]
	v_cvt_scalef32_pk_f32_fp4 v[140:141], v127, 1.0 op_sel:[0,1,0]
	v_cvt_scalef32_pk_f32_fp4 v[142:143], v127, 1.0 op_sel:[1,1,0]
	v_pk_fma_f32 v[186:187], s[74:75], v[136:137], v[186:187] op_sel_hi:[0,1,1]
	v_pk_fma_f32 v[188:189], s[74:75], v[138:139], v[188:189] op_sel_hi:[0,1,1]
	v_pk_fma_f32 v[190:191], s[74:75], v[140:141], v[190:191] op_sel_hi:[0,1,1]
	v_pk_fma_f32 v[192:193], s[74:75], v[142:143], v[192:193] op_sel_hi:[0,1,1]
	v_cvt_scalef32_pk_f32_fp4 v[136:137], v128, 1.0
	v_cvt_scalef32_pk_f32_fp4 v[138:139], v128, 1.0 op_sel:[1,0,0]
	v_cvt_scalef32_pk_f32_fp4 v[140:141], v128, 1.0 op_sel:[0,1,0]
	v_cvt_scalef32_pk_f32_fp4 v[142:143], v128, 1.0 op_sel:[1,1,0]
	v_pk_fma_f32 v[194:195], s[74:75], v[136:137], v[194:195] op_sel_hi:[0,1,1]
	v_pk_fma_f32 v[196:197], s[74:75], v[138:139], v[196:197] op_sel_hi:[0,1,1]
	v_pk_fma_f32 v[198:199], s[74:75], v[140:141], v[198:199] op_sel_hi:[0,1,1]
	v_pk_fma_f32 v[200:201], s[74:75], v[142:143], v[200:201] op_sel_hi:[0,1,1]
	s_waitcnt lgkmcnt(0)
	v_cvt_scalef32_pk_f32_fp4 v[136:137], v129, 1.0
	v_cvt_scalef32_pk_f32_fp4 v[138:139], v129, 1.0 op_sel:[1,0,0]
	v_cvt_scalef32_pk_f32_fp4 v[140:141], v129, 1.0 op_sel:[0,1,0]
	v_cvt_scalef32_pk_f32_fp4 v[142:143], v129, 1.0 op_sel:[1,1,0]
	v_pk_fma_f32 v[202:203], s[74:75], v[136:137], v[202:203] op_sel_hi:[0,1,1]
	v_pk_fma_f32 v[204:205], s[74:75], v[138:139], v[204:205] op_sel_hi:[0,1,1]
	v_pk_fma_f32 v[206:207], s[74:75], v[140:141], v[206:207] op_sel_hi:[0,1,1]
	v_pk_fma_f32 v[208:209], s[74:75], v[142:143], v[208:209] op_sel_hi:[0,1,1]
	v_cvt_scalef32_pk_f32_fp4 v[136:137], v130, 1.0
	v_cvt_scalef32_pk_f32_fp4 v[138:139], v130, 1.0 op_sel:[1,0,0]
	v_cvt_scalef32_pk_f32_fp4 v[140:141], v130, 1.0 op_sel:[0,1,0]
	v_cvt_scalef32_pk_f32_fp4 v[142:143], v130, 1.0 op_sel:[1,1,0]
	v_pk_fma_f32 v[210:211], s[74:75], v[136:137], v[210:211] op_sel_hi:[0,1,1]
	v_pk_fma_f32 v[212:213], s[74:75], v[138:139], v[212:213] op_sel_hi:[0,1,1]
	v_pk_fma_f32 v[214:215], s[74:75], v[140:141], v[214:215] op_sel_hi:[0,1,1]
	v_pk_fma_f32 v[216:217], s[74:75], v[142:143], v[216:217] op_sel_hi:[0,1,1]
	v_cvt_scalef32_pk_f32_fp4 v[136:137], v131, 1.0
	v_cvt_scalef32_pk_f32_fp4 v[138:139], v131, 1.0 op_sel:[1,0,0]
	v_cvt_scalef32_pk_f32_fp4 v[140:141], v131, 1.0 op_sel:[0,1,0]
	v_cvt_scalef32_pk_f32_fp4 v[142:143], v131, 1.0 op_sel:[1,1,0]
	v_pk_fma_f32 v[218:219], s[74:75], v[136:137], v[218:219] op_sel_hi:[0,1,1]
	v_pk_fma_f32 v[220:221], s[74:75], v[138:139], v[220:221] op_sel_hi:[0,1,1]
	v_pk_fma_f32 v[222:223], s[74:75], v[140:141], v[222:223] op_sel_hi:[0,1,1]
	v_pk_fma_f32 v[224:225], s[74:75], v[142:143], v[224:225] op_sel_hi:[0,1,1]
	v_cvt_scalef32_pk_f32_fp4 v[136:137], v132, 1.0
	v_cvt_scalef32_pk_f32_fp4 v[138:139], v132, 1.0 op_sel:[1,0,0]
	v_cvt_scalef32_pk_f32_fp4 v[140:141], v132, 1.0 op_sel:[0,1,0]
	v_cvt_scalef32_pk_f32_fp4 v[142:143], v132, 1.0 op_sel:[1,1,0]
	v_pk_fma_f32 v[226:227], s[74:75], v[136:137], v[226:227] op_sel_hi:[0,1,1]
	v_pk_fma_f32 v[228:229], s[74:75], v[138:139], v[228:229] op_sel_hi:[0,1,1]
	v_pk_fma_f32 v[230:231], s[74:75], v[140:141], v[230:231] op_sel_hi:[0,1,1]
	v_pk_fma_f32 v[232:233], s[74:75], v[142:143], v[232:233] op_sel_hi:[0,1,1]
	v_cvt_scalef32_pk_f32_fp4 v[136:137], v133, 1.0
	v_cvt_scalef32_pk_f32_fp4 v[138:139], v133, 1.0 op_sel:[1,0,0]
	v_cvt_scalef32_pk_f32_fp4 v[140:141], v133, 1.0 op_sel:[0,1,0]
	v_cvt_scalef32_pk_f32_fp4 v[142:143], v133, 1.0 op_sel:[1,1,0]
	v_pk_fma_f32 v[234:235], s[74:75], v[136:137], v[234:235] op_sel_hi:[0,1,1]
	v_pk_fma_f32 v[236:237], s[74:75], v[138:139], v[236:237] op_sel_hi:[0,1,1]
	v_pk_fma_f32 v[238:239], s[74:75], v[140:141], v[238:239] op_sel_hi:[0,1,1]
	v_pk_fma_f32 v[240:241], s[74:75], v[142:143], v[240:241] op_sel_hi:[0,1,1]
.Lpvt3E:
	s_add_i32 s32, s46, 4
	s_bitcmp1_b64 s[70:71], s32
	s_cbranch_scc1 .Lpvt4B
	s_add_i32 s47, s46, 5
	s_and_b32 s47, s47, 7
	s_lshl_b32 s47, s47, 11
	s_add_i32 s77, s33, s47
	v_add_u32_e32 v4, s77, v70
	s_add_i32 s32, s46, 4
	v_readlane_b32 s74, v123, s32
	s_waitcnt vmcnt(8)
	ds_read_b128 v[126:129], v4
	ds_read_b128 v[130:133], v4 offset:1024
	v_cvt_scalef32_pk_f32_fp4 v[136:137], v98, 1.0
	v_cvt_scalef32_pk_f32_fp4 v[138:139], v98, 1.0 op_sel:[1,0,0]
	v_cvt_scalef32_pk_f32_fp4 v[140:141], v98, 1.0 op_sel:[0,1,0]
	v_cvt_scalef32_pk_f32_fp4 v[142:143], v98, 1.0 op_sel:[1,1,0]
	v_pk_fma_f32 v[94:95], s[74:75], v[136:137], v[94:95] op_sel_hi:[0,1,1]
	v_pk_fma_f32 v[96:97], s[74:75], v[138:139], v[96:97] op_sel_hi:[0,1,1]
	v_pk_fma_f32 v[92:93], s[74:75], v[140:141], v[92:93] op_sel_hi:[0,1,1]
	v_pk_fma_f32 v[90:91], s[74:75], v[142:143], v[90:91] op_sel_hi:[0,1,1]
	v_cvt_scalef32_pk_f32_fp4 v[136:137], v99, 1.0
	v_cvt_scalef32_pk_f32_fp4 v[138:139], v99, 1.0 op_sel:[1,0,0]
	v_cvt_scalef32_pk_f32_fp4 v[140:141], v99, 1.0 op_sel:[0,1,0]
	v_cvt_scalef32_pk_f32_fp4 v[142:143], v99, 1.0 op_sel:[1,1,0]
	v_pk_fma_f32 v[88:89], s[74:75], v[136:137], v[88:89] op_sel_hi:[0,1,1]
	v_pk_fma_f32 v[86:87], s[74:75], v[138:139], v[86:87] op_sel_hi:[0,1,1]
	v_pk_fma_f32 v[84:85], s[74:75], v[140:141], v[84:85] op_sel_hi:[0,1,1]
	v_pk_fma_f32 v[82:83], s[74:75], v[142:143], v[82:83] op_sel_hi:[0,1,1]
	v_cvt_scalef32_pk_f32_fp4 v[136:137], v100, 1.0
	v_cvt_scalef32_pk_f32_fp4 v[138:139], v100, 1.0 op_sel:[1,0,0]
	v_cvt_scalef32_pk_f32_fp4 v[140:141], v100, 1.0 op_sel:[0,1,0]
	v_cvt_scalef32_pk_f32_fp4 v[142:143], v100, 1.0 op_sel:[1,1,0]
	v_pk_fma_f32 v[64:65], s[74:75], v[136:137], v[64:65] op_sel_hi:[0,1,1]
	v_pk_fma_f32 v[80:81], s[74:75], v[138:139], v[80:81] op_sel_hi:[0,1,1]
	v_pk_fma_f32 v[62:63], s[74:75], v[140:141], v[62:63] op_sel_hi:[0,1,1]
	v_pk_fma_f32 v[60:61], s[74:75], v[142:143], v[60:61] op_sel_hi:[0,1,1]
	s_waitcnt lgkmcnt(0)
	v_cvt_scalef32_pk_f32_fp4 v[136:137], v101, 1.0
	v_cvt_scalef32_pk_f32_fp4 v[138:139], v101, 1.0 op_sel:[1,0,0]
	v_cvt_scalef32_pk_f32_fp4 v[140:141], v101, 1.0 op_sel:[0,1,0]
	v_cvt_scalef32_pk_f32_fp4 v[142:143], v101, 1.0 op_sel:[1,1,0]
	v_pk_fma_f32 v[58:59], s[74:75], v[136:137], v[58:59] op_sel_hi:[0,1,1]
	v_pk_fma_f32 v[56:57], s[74:75], v[138:139], v[56:57] op_sel_hi:[0,1,1]
	v_pk_fma_f32 v[54:55], s[74:75], v[140:141], v[54:55] op_sel_hi:[0,1,1]
	v_pk_fma_f32 v[52:53], s[74:75], v[142:143], v[52:53] op_sel_hi:[0,1,1]
	v_cvt_scalef32_pk_f32_fp4 v[136:137], v102, 1.0
	v_cvt_scalef32_pk_f32_fp4 v[138:139], v102, 1.0 op_sel:[1,0,0]
	v_cvt_scalef32_pk_f32_fp4 v[140:141], v102, 1.0 op_sel:[0,1,0]
	v_cvt_scalef32_pk_f32_fp4 v[142:143], v102, 1.0 op_sel:[1,1,0]
	v_pk_fma_f32 v[50:51], s[74:75], v[136:137], v[50:51] op_sel_hi:[0,1,1]
	v_pk_fma_f32 v[48:49], s[74:75], v[138:139], v[48:49] op_sel_hi:[0,1,1]
	v_pk_fma_f32 v[46:47], s[74:75], v[140:141], v[46:47] op_sel_hi:[0,1,1]
	v_pk_fma_f32 v[44:45], s[74:75], v[142:143], v[44:45] op_sel_hi:[0,1,1]
	v_cvt_scalef32_pk_f32_fp4 v[136:137], v103, 1.0
	v_cvt_scalef32_pk_f32_fp4 v[138:139], v103, 1.0 op_sel:[1,0,0]
	v_cvt_scalef32_pk_f32_fp4 v[140:141], v103, 1.0 op_sel:[0,1,0]
	v_cvt_scalef32_pk_f32_fp4 v[142:143], v103, 1.0 op_sel:[1,1,0]
	v_pk_fma_f32 v[42:43], s[74:75], v[136:137], v[42:43] op_sel_hi:[0,1,1]
	v_pk_fma_f32 v[40:41], s[74:75], v[138:139], v[40:41] op_sel_hi:[0,1,1]
	v_pk_fma_f32 v[38:39], s[74:75], v[140:141], v[38:39] op_sel_hi:[0,1,1]
	v_pk_fma_f32 v[36:37], s[74:75], v[142:143], v[36:37] op_sel_hi:[0,1,1]
	v_cvt_scalef32_pk_f32_fp4 v[136:137], v104, 1.0
	v_cvt_scalef32_pk_f32_fp4 v[138:139], v104, 1.0 op_sel:[1,0,0]
	v_cvt_scalef32_pk_f32_fp4 v[140:141], v104, 1.0 op_sel:[0,1,0]
	v_cvt_scalef32_pk_f32_fp4 v[142:143], v104, 1.0 op_sel:[1,1,0]
	v_pk_fma_f32 v[32:33], s[74:75], v[136:137], v[32:33] op_sel_hi:[0,1,1]
	v_pk_fma_f32 v[34:35], s[74:75], v[138:139], v[34:35] op_sel_hi:[0,1,1]
	v_pk_fma_f32 v[30:31], s[74:75], v[140:141], v[30:31] op_sel_hi:[0,1,1]
	v_pk_fma_f32 v[28:29], s[74:75], v[142:143], v[28:29] op_sel_hi:[0,1,1]
	v_cvt_scalef32_pk_f32_fp4 v[136:137], v105, 1.0
	v_cvt_scalef32_pk_f32_fp4 v[138:139], v105, 1.0 op_sel:[1,0,0]
	v_cvt_scalef32_pk_f32_fp4 v[140:141], v105, 1.0 op_sel:[0,1,0]
	v_cvt_scalef32_pk_f32_fp4 v[142:143], v105, 1.0 op_sel:[1,1,0]
	v_pk_fma_f32 v[26:27], s[74:75], v[136:137], v[26:27] op_sel_hi:[0,1,1]
	v_pk_fma_f32 v[24:25], s[74:75], v[138:139], v[24:25] op_sel_hi:[0,1,1]
	v_pk_fma_f32 v[20:21], s[74:75], v[140:141], v[20:21] op_sel_hi:[0,1,1]
	v_pk_fma_f32 v[22:23], s[74:75], v[142:143], v[22:23] op_sel_hi:[0,1,1]
	s_branch .Lpvt4E
.Lpvt4B:
	s_add_i32 s47, s46, 5
	s_and_b32 s47, s47, 7
	s_lshl_b32 s47, s47, 11
	s_add_i32 s77, s33, s47
	v_add_u32_e32 v4, s77, v70
	s_add_i32 s32, s46, 4
	v_readlane_b32 s74, v123, s32
	s_waitcnt vmcnt(8)
	ds_read_b128 v[126:129], v4
	ds_read_b128 v[130:133], v4 offset:1024
	v_cvt_scalef32_pk_f32_fp4 v[136:137], v98, 1.0
	v_cvt_scalef32_pk_f32_fp4 v[138:139], v98, 1.0 op_sel:[1,0,0]
	v_cvt_scalef32_pk_f32_fp4 v[140:141], v98, 1.0 op_sel:[0,1,0]
	v_cvt_scalef32_pk_f32_fp4 v[142:143], v98, 1.0 op_sel:[1,1,0]
	v_pk_fma_f32 v[178:179], s[74:75], v[136:137], v[178:179] op_sel_hi:[0,1,1]
	v_pk_fma_f32 v[180:181], s[74:75], v[138:139], v[180:181] op_sel_hi:[0,1,1]
	v_pk_fma_f32 v[182:183], s[74:75], v[140:141], v[182:183] op_sel_hi:[0,1,1]
	v_pk_fma_f32 v[184:185], s[74:75], v[142:143], v[184:185] op_sel_hi:[0,1,1]
	v_cvt_scalef32_pk_f32_fp4 v[136:137], v99, 1.0
	v_cvt_scalef32_pk_f32_fp4 v[138:139], v99, 1.0 op_sel:[1,0,0]
	v_cvt_scalef32_pk_f32_fp4 v[140:141], v99, 1.0 op_sel:[0,1,0]
	v_cvt_scalef32_pk_f32_fp4 v[142:143], v99, 1.0 op_sel:[1,1,0]
	v_pk_fma_f32 v[186:187], s[74:75], v[136:137], v[186:187] op_sel_hi:[0,1,1]
	v_pk_fma_f32 v[188:189], s[74:75], v[138:139], v[188:189] op_sel_hi:[0,1,1]
	v_pk_fma_f32 v[190:191], s[74:75], v[140:141], v[190:191] op_sel_hi:[0,1,1]
	v_pk_fma_f32 v[192:193], s[74:75], v[142:143], v[192:193] op_sel_hi:[0,1,1]
	v_cvt_scalef32_pk_f32_fp4 v[136:137], v100, 1.0
	v_cvt_scalef32_pk_f32_fp4 v[138:139], v100, 1.0 op_sel:[1,0,0]
	v_cvt_scalef32_pk_f32_fp4 v[140:141], v100, 1.0 op_sel:[0,1,0]
	v_cvt_scalef32_pk_f32_fp4 v[142:143], v100, 1.0 op_sel:[1,1,0]
	v_pk_fma_f32 v[194:195], s[74:75], v[136:137], v[194:195] op_sel_hi:[0,1,1]
	v_pk_fma_f32 v[196:197], s[74:75], v[138:139], v[196:197] op_sel_hi:[0,1,1]
	v_pk_fma_f32 v[198:199], s[74:75], v[140:141], v[198:199] op_sel_hi:[0,1,1]
	v_pk_fma_f32 v[200:201], s[74:75], v[142:143], v[200:201] op_sel_hi:[0,1,1]
	s_waitcnt lgkmcnt(0)
	v_cvt_scalef32_pk_f32_fp4 v[136:137], v101, 1.0
	v_cvt_scalef32_pk_f32_fp4 v[138:139], v101, 1.0 op_sel:[1,0,0]
	v_cvt_scalef32_pk_f32_fp4 v[140:141], v101, 1.0 op_sel:[0,1,0]
	v_cvt_scalef32_pk_f32_fp4 v[142:143], v101, 1.0 op_sel:[1,1,0]
	v_pk_fma_f32 v[202:203], s[74:75], v[136:137], v[202:203] op_sel_hi:[0,1,1]
	v_pk_fma_f32 v[204:205], s[74:75], v[138:139], v[204:205] op_sel_hi:[0,1,1]
	v_pk_fma_f32 v[206:207], s[74:75], v[140:141], v[206:207] op_sel_hi:[0,1,1]
	v_pk_fma_f32 v[208:209], s[74:75], v[142:143], v[208:209] op_sel_hi:[0,1,1]
	v_cvt_scalef32_pk_f32_fp4 v[136:137], v102, 1.0
	v_cvt_scalef32_pk_f32_fp4 v[138:139], v102, 1.0 op_sel:[1,0,0]
	v_cvt_scalef32_pk_f32_fp4 v[140:141], v102, 1.0 op_sel:[0,1,0]
	v_cvt_scalef32_pk_f32_fp4 v[142:143], v102, 1.0 op_sel:[1,1,0]
	v_pk_fma_f32 v[210:211], s[74:75], v[136:137], v[210:211] op_sel_hi:[0,1,1]
	v_pk_fma_f32 v[212:213], s[74:75], v[138:139], v[212:213] op_sel_hi:[0,1,1]
	v_pk_fma_f32 v[214:215], s[74:75], v[140:141], v[214:215] op_sel_hi:[0,1,1]
	v_pk_fma_f32 v[216:217], s[74:75], v[142:143], v[216:217] op_sel_hi:[0,1,1]
	v_cvt_scalef32_pk_f32_fp4 v[136:137], v103, 1.0
	v_cvt_scalef32_pk_f32_fp4 v[138:139], v103, 1.0 op_sel:[1,0,0]
	v_cvt_scalef32_pk_f32_fp4 v[140:141], v103, 1.0 op_sel:[0,1,0]
	v_cvt_scalef32_pk_f32_fp4 v[142:143], v103, 1.0 op_sel:[1,1,0]
	v_pk_fma_f32 v[218:219], s[74:75], v[136:137], v[218:219] op_sel_hi:[0,1,1]
	v_pk_fma_f32 v[220:221], s[74:75], v[138:139], v[220:221] op_sel_hi:[0,1,1]
	v_pk_fma_f32 v[222:223], s[74:75], v[140:141], v[222:223] op_sel_hi:[0,1,1]
	v_pk_fma_f32 v[224:225], s[74:75], v[142:143], v[224:225] op_sel_hi:[0,1,1]
	v_cvt_scalef32_pk_f32_fp4 v[136:137], v104, 1.0
	v_cvt_scalef32_pk_f32_fp4 v[138:139], v104, 1.0 op_sel:[1,0,0]
	v_cvt_scalef32_pk_f32_fp4 v[140:141], v104, 1.0 op_sel:[0,1,0]
	v_cvt_scalef32_pk_f32_fp4 v[142:143], v104, 1.0 op_sel:[1,1,0]
	v_pk_fma_f32 v[226:227], s[74:75], v[136:137], v[226:227] op_sel_hi:[0,1,1]
	v_pk_fma_f32 v[228:229], s[74:75], v[138:139], v[228:229] op_sel_hi:[0,1,1]
	v_pk_fma_f32 v[230:231], s[74:75], v[140:141], v[230:231] op_sel_hi:[0,1,1]
	v_pk_fma_f32 v[232:233], s[74:75], v[142:143], v[232:233] op_sel_hi:[0,1,1]
	v_cvt_scalef32_pk_f32_fp4 v[136:137], v105, 1.0
	v_cvt_scalef32_pk_f32_fp4 v[138:139], v105, 1.0 op_sel:[1,0,0]
	v_cvt_scalef32_pk_f32_fp4 v[140:141], v105, 1.0 op_sel:[0,1,0]
	v_cvt_scalef32_pk_f32_fp4 v[142:143], v105, 1.0 op_sel:[1,1,0]
	v_pk_fma_f32 v[234:235], s[74:75], v[136:137], v[234:235] op_sel_hi:[0,1,1]
	v_pk_fma_f32 v[236:237], s[74:75], v[138:139], v[236:237] op_sel_hi:[0,1,1]
	v_pk_fma_f32 v[238:239], s[74:75], v[140:141], v[238:239] op_sel_hi:[0,1,1]
	v_pk_fma_f32 v[240:241], s[74:75], v[142:143], v[240:241] op_sel_hi:[0,1,1]
.Lpvt4E:
	s_add_i32 s32, s46, 5
	s_bitcmp1_b64 s[70:71], s32
	s_cbranch_scc1 .Lpvt5B
	s_add_i32 s47, s46, 6
	s_and_b32 s47, s47, 7
	s_lshl_b32 s47, s47, 11
	s_add_i32 s77, s33, s47
	v_add_u32_e32 v4, s77, v70
	s_add_i32 s32, s46, 5
	v_readlane_b32 s74, v123, s32
	s_waitcnt vmcnt(6)
	ds_read_b128 v[98:101], v4
	ds_read_b128 v[102:105], v4 offset:1024
	v_cvt_scalef32_pk_f32_fp4 v[136:137], v126, 1.0
	v_cvt_scalef32_pk_f32_fp4 v[138:139], v126, 1.0 op_sel:[1,0,0]
	v_cvt_scalef32_pk_f32_fp4 v[140:141], v126, 1.0 op_sel:[0,1,0]
	v_cvt_scalef32_pk_f32_fp4 v[142:143], v126, 1.0 op_sel:[1,1,0]
	v_pk_fma_f32 v[94:95], s[74:75], v[136:137], v[94:95] op_sel_hi:[0,1,1]
	v_pk_fma_f32 v[96:97], s[74:75], v[138:139], v[96:97] op_sel_hi:[0,1,1]
	v_pk_fma_f32 v[92:93], s[74:75], v[140:141], v[92:93] op_sel_hi:[0,1,1]
	v_pk_fma_f32 v[90:91], s[74:75], v[142:143], v[90:91] op_sel_hi:[0,1,1]
	v_cvt_scalef32_pk_f32_fp4 v[136:137], v127, 1.0
	v_cvt_scalef32_pk_f32_fp4 v[138:139], v127, 1.0 op_sel:[1,0,0]
	v_cvt_scalef32_pk_f32_fp4 v[140:141], v127, 1.0 op_sel:[0,1,0]
	v_cvt_scalef32_pk_f32_fp4 v[142:143], v127, 1.0 op_sel:[1,1,0]
	v_pk_fma_f32 v[88:89], s[74:75], v[136:137], v[88:89] op_sel_hi:[0,1,1]
	v_pk_fma_f32 v[86:87], s[74:75], v[138:139], v[86:87] op_sel_hi:[0,1,1]
	v_pk_fma_f32 v[84:85], s[74:75], v[140:141], v[84:85] op_sel_hi:[0,1,1]
	v_pk_fma_f32 v[82:83], s[74:75], v[142:143], v[82:83] op_sel_hi:[0,1,1]
	v_cvt_scalef32_pk_f32_fp4 v[136:137], v128, 1.0
	v_cvt_scalef32_pk_f32_fp4 v[138:139], v128, 1.0 op_sel:[1,0,0]
	v_cvt_scalef32_pk_f32_fp4 v[140:141], v128, 1.0 op_sel:[0,1,0]
	v_cvt_scalef32_pk_f32_fp4 v[142:143], v128, 1.0 op_sel:[1,1,0]
	v_pk_fma_f32 v[64:65], s[74:75], v[136:137], v[64:65] op_sel_hi:[0,1,1]
	v_pk_fma_f32 v[80:81], s[74:75], v[138:139], v[80:81] op_sel_hi:[0,1,1]
	v_pk_fma_f32 v[62:63], s[74:75], v[140:141], v[62:63] op_sel_hi:[0,1,1]
	v_pk_fma_f32 v[60:61], s[74:75], v[142:143], v[60:61] op_sel_hi:[0,1,1]
	s_waitcnt lgkmcnt(0)
	v_cvt_scalef32_pk_f32_fp4 v[136:137], v129, 1.0
	v_cvt_scalef32_pk_f32_fp4 v[138:139], v129, 1.0 op_sel:[1,0,0]
	v_cvt_scalef32_pk_f32_fp4 v[140:141], v129, 1.0 op_sel:[0,1,0]
	v_cvt_scalef32_pk_f32_fp4 v[142:143], v129, 1.0 op_sel:[1,1,0]
	v_pk_fma_f32 v[58:59], s[74:75], v[136:137], v[58:59] op_sel_hi:[0,1,1]
	v_pk_fma_f32 v[56:57], s[74:75], v[138:139], v[56:57] op_sel_hi:[0,1,1]
	v_pk_fma_f32 v[54:55], s[74:75], v[140:141], v[54:55] op_sel_hi:[0,1,1]
	v_pk_fma_f32 v[52:53], s[74:75], v[142:143], v[52:53] op_sel_hi:[0,1,1]
	v_cvt_scalef32_pk_f32_fp4 v[136:137], v130, 1.0
	v_cvt_scalef32_pk_f32_fp4 v[138:139], v130, 1.0 op_sel:[1,0,0]
	v_cvt_scalef32_pk_f32_fp4 v[140:141], v130, 1.0 op_sel:[0,1,0]
	v_cvt_scalef32_pk_f32_fp4 v[142:143], v130, 1.0 op_sel:[1,1,0]
	v_pk_fma_f32 v[50:51], s[74:75], v[136:137], v[50:51] op_sel_hi:[0,1,1]
	v_pk_fma_f32 v[48:49], s[74:75], v[138:139], v[48:49] op_sel_hi:[0,1,1]
	v_pk_fma_f32 v[46:47], s[74:75], v[140:141], v[46:47] op_sel_hi:[0,1,1]
	v_pk_fma_f32 v[44:45], s[74:75], v[142:143], v[44:45] op_sel_hi:[0,1,1]
	v_cvt_scalef32_pk_f32_fp4 v[136:137], v131, 1.0
	v_cvt_scalef32_pk_f32_fp4 v[138:139], v131, 1.0 op_sel:[1,0,0]
	v_cvt_scalef32_pk_f32_fp4 v[140:141], v131, 1.0 op_sel:[0,1,0]
	v_cvt_scalef32_pk_f32_fp4 v[142:143], v131, 1.0 op_sel:[1,1,0]
	v_pk_fma_f32 v[42:43], s[74:75], v[136:137], v[42:43] op_sel_hi:[0,1,1]
	v_pk_fma_f32 v[40:41], s[74:75], v[138:139], v[40:41] op_sel_hi:[0,1,1]
	v_pk_fma_f32 v[38:39], s[74:75], v[140:141], v[38:39] op_sel_hi:[0,1,1]
	v_pk_fma_f32 v[36:37], s[74:75], v[142:143], v[36:37] op_sel_hi:[0,1,1]
	v_cvt_scalef32_pk_f32_fp4 v[136:137], v132, 1.0
	v_cvt_scalef32_pk_f32_fp4 v[138:139], v132, 1.0 op_sel:[1,0,0]
	v_cvt_scalef32_pk_f32_fp4 v[140:141], v132, 1.0 op_sel:[0,1,0]
	v_cvt_scalef32_pk_f32_fp4 v[142:143], v132, 1.0 op_sel:[1,1,0]
	v_pk_fma_f32 v[32:33], s[74:75], v[136:137], v[32:33] op_sel_hi:[0,1,1]
	v_pk_fma_f32 v[34:35], s[74:75], v[138:139], v[34:35] op_sel_hi:[0,1,1]
	v_pk_fma_f32 v[30:31], s[74:75], v[140:141], v[30:31] op_sel_hi:[0,1,1]
	v_pk_fma_f32 v[28:29], s[74:75], v[142:143], v[28:29] op_sel_hi:[0,1,1]
	v_cvt_scalef32_pk_f32_fp4 v[136:137], v133, 1.0
	v_cvt_scalef32_pk_f32_fp4 v[138:139], v133, 1.0 op_sel:[1,0,0]
	v_cvt_scalef32_pk_f32_fp4 v[140:141], v133, 1.0 op_sel:[0,1,0]
	v_cvt_scalef32_pk_f32_fp4 v[142:143], v133, 1.0 op_sel:[1,1,0]
	v_pk_fma_f32 v[26:27], s[74:75], v[136:137], v[26:27] op_sel_hi:[0,1,1]
	v_pk_fma_f32 v[24:25], s[74:75], v[138:139], v[24:25] op_sel_hi:[0,1,1]
	v_pk_fma_f32 v[20:21], s[74:75], v[140:141], v[20:21] op_sel_hi:[0,1,1]
	v_pk_fma_f32 v[22:23], s[74:75], v[142:143], v[22:23] op_sel_hi:[0,1,1]
	s_branch .Lpvt5E
.Lpvt5B:
	s_add_i32 s47, s46, 6
	s_and_b32 s47, s47, 7
	s_lshl_b32 s47, s47, 11
	s_add_i32 s77, s33, s47
	v_add_u32_e32 v4, s77, v70
	s_add_i32 s32, s46, 5
	v_readlane_b32 s74, v123, s32
	s_waitcnt vmcnt(6)
	ds_read_b128 v[98:101], v4
	ds_read_b128 v[102:105], v4 offset:1024
	v_cvt_scalef32_pk_f32_fp4 v[136:137], v126, 1.0
	v_cvt_scalef32_pk_f32_fp4 v[138:139], v126, 1.0 op_sel:[1,0,0]
	v_cvt_scalef32_pk_f32_fp4 v[140:141], v126, 1.0 op_sel:[0,1,0]
	v_cvt_scalef32_pk_f32_fp4 v[142:143], v126, 1.0 op_sel:[1,1,0]
	v_pk_fma_f32 v[178:179], s[74:75], v[136:137], v[178:179] op_sel_hi:[0,1,1]
	v_pk_fma_f32 v[180:181], s[74:75], v[138:139], v[180:181] op_sel_hi:[0,1,1]
	v_pk_fma_f32 v[182:183], s[74:75], v[140:141], v[182:183] op_sel_hi:[0,1,1]
	v_pk_fma_f32 v[184:185], s[74:75], v[142:143], v[184:185] op_sel_hi:[0,1,1]
	v_cvt_scalef32_pk_f32_fp4 v[136:137], v127, 1.0
	v_cvt_scalef32_pk_f32_fp4 v[138:139], v127, 1.0 op_sel:[1,0,0]
	v_cvt_scalef32_pk_f32_fp4 v[140:141], v127, 1.0 op_sel:[0,1,0]
	v_cvt_scalef32_pk_f32_fp4 v[142:143], v127, 1.0 op_sel:[1,1,0]
	v_pk_fma_f32 v[186:187], s[74:75], v[136:137], v[186:187] op_sel_hi:[0,1,1]
	v_pk_fma_f32 v[188:189], s[74:75], v[138:139], v[188:189] op_sel_hi:[0,1,1]
	v_pk_fma_f32 v[190:191], s[74:75], v[140:141], v[190:191] op_sel_hi:[0,1,1]
	v_pk_fma_f32 v[192:193], s[74:75], v[142:143], v[192:193] op_sel_hi:[0,1,1]
	v_cvt_scalef32_pk_f32_fp4 v[136:137], v128, 1.0
	v_cvt_scalef32_pk_f32_fp4 v[138:139], v128, 1.0 op_sel:[1,0,0]
	v_cvt_scalef32_pk_f32_fp4 v[140:141], v128, 1.0 op_sel:[0,1,0]
	v_cvt_scalef32_pk_f32_fp4 v[142:143], v128, 1.0 op_sel:[1,1,0]
	v_pk_fma_f32 v[194:195], s[74:75], v[136:137], v[194:195] op_sel_hi:[0,1,1]
	v_pk_fma_f32 v[196:197], s[74:75], v[138:139], v[196:197] op_sel_hi:[0,1,1]
	v_pk_fma_f32 v[198:199], s[74:75], v[140:141], v[198:199] op_sel_hi:[0,1,1]
	v_pk_fma_f32 v[200:201], s[74:75], v[142:143], v[200:201] op_sel_hi:[0,1,1]
	s_waitcnt lgkmcnt(0)
	v_cvt_scalef32_pk_f32_fp4 v[136:137], v129, 1.0
	v_cvt_scalef32_pk_f32_fp4 v[138:139], v129, 1.0 op_sel:[1,0,0]
	v_cvt_scalef32_pk_f32_fp4 v[140:141], v129, 1.0 op_sel:[0,1,0]
	v_cvt_scalef32_pk_f32_fp4 v[142:143], v129, 1.0 op_sel:[1,1,0]
	v_pk_fma_f32 v[202:203], s[74:75], v[136:137], v[202:203] op_sel_hi:[0,1,1]
	v_pk_fma_f32 v[204:205], s[74:75], v[138:139], v[204:205] op_sel_hi:[0,1,1]
	v_pk_fma_f32 v[206:207], s[74:75], v[140:141], v[206:207] op_sel_hi:[0,1,1]
	v_pk_fma_f32 v[208:209], s[74:75], v[142:143], v[208:209] op_sel_hi:[0,1,1]
	v_cvt_scalef32_pk_f32_fp4 v[136:137], v130, 1.0
	v_cvt_scalef32_pk_f32_fp4 v[138:139], v130, 1.0 op_sel:[1,0,0]
	v_cvt_scalef32_pk_f32_fp4 v[140:141], v130, 1.0 op_sel:[0,1,0]
	v_cvt_scalef32_pk_f32_fp4 v[142:143], v130, 1.0 op_sel:[1,1,0]
	v_pk_fma_f32 v[210:211], s[74:75], v[136:137], v[210:211] op_sel_hi:[0,1,1]
	v_pk_fma_f32 v[212:213], s[74:75], v[138:139], v[212:213] op_sel_hi:[0,1,1]
	v_pk_fma_f32 v[214:215], s[74:75], v[140:141], v[214:215] op_sel_hi:[0,1,1]
	v_pk_fma_f32 v[216:217], s[74:75], v[142:143], v[216:217] op_sel_hi:[0,1,1]
	v_cvt_scalef32_pk_f32_fp4 v[136:137], v131, 1.0
	v_cvt_scalef32_pk_f32_fp4 v[138:139], v131, 1.0 op_sel:[1,0,0]
	v_cvt_scalef32_pk_f32_fp4 v[140:141], v131, 1.0 op_sel:[0,1,0]
	v_cvt_scalef32_pk_f32_fp4 v[142:143], v131, 1.0 op_sel:[1,1,0]
	v_pk_fma_f32 v[218:219], s[74:75], v[136:137], v[218:219] op_sel_hi:[0,1,1]
	v_pk_fma_f32 v[220:221], s[74:75], v[138:139], v[220:221] op_sel_hi:[0,1,1]
	v_pk_fma_f32 v[222:223], s[74:75], v[140:141], v[222:223] op_sel_hi:[0,1,1]
	v_pk_fma_f32 v[224:225], s[74:75], v[142:143], v[224:225] op_sel_hi:[0,1,1]
	v_cvt_scalef32_pk_f32_fp4 v[136:137], v132, 1.0
	v_cvt_scalef32_pk_f32_fp4 v[138:139], v132, 1.0 op_sel:[1,0,0]
	v_cvt_scalef32_pk_f32_fp4 v[140:141], v132, 1.0 op_sel:[0,1,0]
	v_cvt_scalef32_pk_f32_fp4 v[142:143], v132, 1.0 op_sel:[1,1,0]
	v_pk_fma_f32 v[226:227], s[74:75], v[136:137], v[226:227] op_sel_hi:[0,1,1]
	v_pk_fma_f32 v[228:229], s[74:75], v[138:139], v[228:229] op_sel_hi:[0,1,1]
	v_pk_fma_f32 v[230:231], s[74:75], v[140:141], v[230:231] op_sel_hi:[0,1,1]
	v_pk_fma_f32 v[232:233], s[74:75], v[142:143], v[232:233] op_sel_hi:[0,1,1]
	v_cvt_scalef32_pk_f32_fp4 v[136:137], v133, 1.0
	v_cvt_scalef32_pk_f32_fp4 v[138:139], v133, 1.0 op_sel:[1,0,0]
	v_cvt_scalef32_pk_f32_fp4 v[140:141], v133, 1.0 op_sel:[0,1,0]
	v_cvt_scalef32_pk_f32_fp4 v[142:143], v133, 1.0 op_sel:[1,1,0]
	v_pk_fma_f32 v[234:235], s[74:75], v[136:137], v[234:235] op_sel_hi:[0,1,1]
	v_pk_fma_f32 v[236:237], s[74:75], v[138:139], v[236:237] op_sel_hi:[0,1,1]
	v_pk_fma_f32 v[238:239], s[74:75], v[140:141], v[238:239] op_sel_hi:[0,1,1]
	v_pk_fma_f32 v[240:241], s[74:75], v[142:143], v[240:241] op_sel_hi:[0,1,1]
.Lpvt5E:
	s_add_i32 s32, s46, 6
	s_bitcmp1_b64 s[70:71], s32
	s_cbranch_scc1 .Lpvt6B
	s_add_i32 s47, s46, 7
	s_and_b32 s47, s47, 7
	s_lshl_b32 s47, s47, 11
	s_add_i32 s77, s33, s47
	v_add_u32_e32 v4, s77, v70
	s_add_i32 s32, s46, 6
	v_readlane_b32 s74, v123, s32
	s_waitcnt vmcnt(4)
	ds_read_b128 v[126:129], v4
	ds_read_b128 v[130:133], v4 offset:1024
	v_cvt_scalef32_pk_f32_fp4 v[136:137], v98, 1.0
	v_cvt_scalef32_pk_f32_fp4 v[138:139], v98, 1.0 op_sel:[1,0,0]
	v_cvt_scalef32_pk_f32_fp4 v[140:141], v98, 1.0 op_sel:[0,1,0]
	v_cvt_scalef32_pk_f32_fp4 v[142:143], v98, 1.0 op_sel:[1,1,0]
	v_pk_fma_f32 v[94:95], s[74:75], v[136:137], v[94:95] op_sel_hi:[0,1,1]
	v_pk_fma_f32 v[96:97], s[74:75], v[138:139], v[96:97] op_sel_hi:[0,1,1]
	v_pk_fma_f32 v[92:93], s[74:75], v[140:141], v[92:93] op_sel_hi:[0,1,1]
	v_pk_fma_f32 v[90:91], s[74:75], v[142:143], v[90:91] op_sel_hi:[0,1,1]
	v_cvt_scalef32_pk_f32_fp4 v[136:137], v99, 1.0
	v_cvt_scalef32_pk_f32_fp4 v[138:139], v99, 1.0 op_sel:[1,0,0]
	v_cvt_scalef32_pk_f32_fp4 v[140:141], v99, 1.0 op_sel:[0,1,0]
	v_cvt_scalef32_pk_f32_fp4 v[142:143], v99, 1.0 op_sel:[1,1,0]
	v_pk_fma_f32 v[88:89], s[74:75], v[136:137], v[88:89] op_sel_hi:[0,1,1]
	v_pk_fma_f32 v[86:87], s[74:75], v[138:139], v[86:87] op_sel_hi:[0,1,1]
	v_pk_fma_f32 v[84:85], s[74:75], v[140:141], v[84:85] op_sel_hi:[0,1,1]
	v_pk_fma_f32 v[82:83], s[74:75], v[142:143], v[82:83] op_sel_hi:[0,1,1]
	v_cvt_scalef32_pk_f32_fp4 v[136:137], v100, 1.0
	v_cvt_scalef32_pk_f32_fp4 v[138:139], v100, 1.0 op_sel:[1,0,0]
	v_cvt_scalef32_pk_f32_fp4 v[140:141], v100, 1.0 op_sel:[0,1,0]
	v_cvt_scalef32_pk_f32_fp4 v[142:143], v100, 1.0 op_sel:[1,1,0]
	v_pk_fma_f32 v[64:65], s[74:75], v[136:137], v[64:65] op_sel_hi:[0,1,1]
	v_pk_fma_f32 v[80:81], s[74:75], v[138:139], v[80:81] op_sel_hi:[0,1,1]
	v_pk_fma_f32 v[62:63], s[74:75], v[140:141], v[62:63] op_sel_hi:[0,1,1]
	v_pk_fma_f32 v[60:61], s[74:75], v[142:143], v[60:61] op_sel_hi:[0,1,1]
	s_waitcnt lgkmcnt(0)
	v_cvt_scalef32_pk_f32_fp4 v[136:137], v101, 1.0
	v_cvt_scalef32_pk_f32_fp4 v[138:139], v101, 1.0 op_sel:[1,0,0]
	v_cvt_scalef32_pk_f32_fp4 v[140:141], v101, 1.0 op_sel:[0,1,0]
	v_cvt_scalef32_pk_f32_fp4 v[142:143], v101, 1.0 op_sel:[1,1,0]
	v_pk_fma_f32 v[58:59], s[74:75], v[136:137], v[58:59] op_sel_hi:[0,1,1]
	v_pk_fma_f32 v[56:57], s[74:75], v[138:139], v[56:57] op_sel_hi:[0,1,1]
	v_pk_fma_f32 v[54:55], s[74:75], v[140:141], v[54:55] op_sel_hi:[0,1,1]
	v_pk_fma_f32 v[52:53], s[74:75], v[142:143], v[52:53] op_sel_hi:[0,1,1]
	v_cvt_scalef32_pk_f32_fp4 v[136:137], v102, 1.0
	v_cvt_scalef32_pk_f32_fp4 v[138:139], v102, 1.0 op_sel:[1,0,0]
	v_cvt_scalef32_pk_f32_fp4 v[140:141], v102, 1.0 op_sel:[0,1,0]
	v_cvt_scalef32_pk_f32_fp4 v[142:143], v102, 1.0 op_sel:[1,1,0]
	v_pk_fma_f32 v[50:51], s[74:75], v[136:137], v[50:51] op_sel_hi:[0,1,1]
	v_pk_fma_f32 v[48:49], s[74:75], v[138:139], v[48:49] op_sel_hi:[0,1,1]
	v_pk_fma_f32 v[46:47], s[74:75], v[140:141], v[46:47] op_sel_hi:[0,1,1]
	v_pk_fma_f32 v[44:45], s[74:75], v[142:143], v[44:45] op_sel_hi:[0,1,1]
	v_cvt_scalef32_pk_f32_fp4 v[136:137], v103, 1.0
	v_cvt_scalef32_pk_f32_fp4 v[138:139], v103, 1.0 op_sel:[1,0,0]
	v_cvt_scalef32_pk_f32_fp4 v[140:141], v103, 1.0 op_sel:[0,1,0]
	v_cvt_scalef32_pk_f32_fp4 v[142:143], v103, 1.0 op_sel:[1,1,0]
	v_pk_fma_f32 v[42:43], s[74:75], v[136:137], v[42:43] op_sel_hi:[0,1,1]
	v_pk_fma_f32 v[40:41], s[74:75], v[138:139], v[40:41] op_sel_hi:[0,1,1]
	v_pk_fma_f32 v[38:39], s[74:75], v[140:141], v[38:39] op_sel_hi:[0,1,1]
	v_pk_fma_f32 v[36:37], s[74:75], v[142:143], v[36:37] op_sel_hi:[0,1,1]
	v_cvt_scalef32_pk_f32_fp4 v[136:137], v104, 1.0
	v_cvt_scalef32_pk_f32_fp4 v[138:139], v104, 1.0 op_sel:[1,0,0]
	v_cvt_scalef32_pk_f32_fp4 v[140:141], v104, 1.0 op_sel:[0,1,0]
	v_cvt_scalef32_pk_f32_fp4 v[142:143], v104, 1.0 op_sel:[1,1,0]
	v_pk_fma_f32 v[32:33], s[74:75], v[136:137], v[32:33] op_sel_hi:[0,1,1]
	v_pk_fma_f32 v[34:35], s[74:75], v[138:139], v[34:35] op_sel_hi:[0,1,1]
	v_pk_fma_f32 v[30:31], s[74:75], v[140:141], v[30:31] op_sel_hi:[0,1,1]
	v_pk_fma_f32 v[28:29], s[74:75], v[142:143], v[28:29] op_sel_hi:[0,1,1]
	v_cvt_scalef32_pk_f32_fp4 v[136:137], v105, 1.0
	v_cvt_scalef32_pk_f32_fp4 v[138:139], v105, 1.0 op_sel:[1,0,0]
	v_cvt_scalef32_pk_f32_fp4 v[140:141], v105, 1.0 op_sel:[0,1,0]
	v_cvt_scalef32_pk_f32_fp4 v[142:143], v105, 1.0 op_sel:[1,1,0]
	v_pk_fma_f32 v[26:27], s[74:75], v[136:137], v[26:27] op_sel_hi:[0,1,1]
	v_pk_fma_f32 v[24:25], s[74:75], v[138:139], v[24:25] op_sel_hi:[0,1,1]
	v_pk_fma_f32 v[20:21], s[74:75], v[140:141], v[20:21] op_sel_hi:[0,1,1]
	v_pk_fma_f32 v[22:23], s[74:75], v[142:143], v[22:23] op_sel_hi:[0,1,1]
	s_branch .Lpvt6E
.Lpvt6B:
	s_add_i32 s47, s46, 7
	s_and_b32 s47, s47, 7
	s_lshl_b32 s47, s47, 11
	s_add_i32 s77, s33, s47
	v_add_u32_e32 v4, s77, v70
	s_add_i32 s32, s46, 6
	v_readlane_b32 s74, v123, s32
	s_waitcnt vmcnt(4)
	ds_read_b128 v[126:129], v4
	ds_read_b128 v[130:133], v4 offset:1024
	v_cvt_scalef32_pk_f32_fp4 v[136:137], v98, 1.0
	v_cvt_scalef32_pk_f32_fp4 v[138:139], v98, 1.0 op_sel:[1,0,0]
	v_cvt_scalef32_pk_f32_fp4 v[140:141], v98, 1.0 op_sel:[0,1,0]
	v_cvt_scalef32_pk_f32_fp4 v[142:143], v98, 1.0 op_sel:[1,1,0]
	v_pk_fma_f32 v[178:179], s[74:75], v[136:137], v[178:179] op_sel_hi:[0,1,1]
	v_pk_fma_f32 v[180:181], s[74:75], v[138:139], v[180:181] op_sel_hi:[0,1,1]
	v_pk_fma_f32 v[182:183], s[74:75], v[140:141], v[182:183] op_sel_hi:[0,1,1]
	v_pk_fma_f32 v[184:185], s[74:75], v[142:143], v[184:185] op_sel_hi:[0,1,1]
	v_cvt_scalef32_pk_f32_fp4 v[136:137], v99, 1.0
	v_cvt_scalef32_pk_f32_fp4 v[138:139], v99, 1.0 op_sel:[1,0,0]
	v_cvt_scalef32_pk_f32_fp4 v[140:141], v99, 1.0 op_sel:[0,1,0]
	v_cvt_scalef32_pk_f32_fp4 v[142:143], v99, 1.0 op_sel:[1,1,0]
	v_pk_fma_f32 v[186:187], s[74:75], v[136:137], v[186:187] op_sel_hi:[0,1,1]
	v_pk_fma_f32 v[188:189], s[74:75], v[138:139], v[188:189] op_sel_hi:[0,1,1]
	v_pk_fma_f32 v[190:191], s[74:75], v[140:141], v[190:191] op_sel_hi:[0,1,1]
	v_pk_fma_f32 v[192:193], s[74:75], v[142:143], v[192:193] op_sel_hi:[0,1,1]
	v_cvt_scalef32_pk_f32_fp4 v[136:137], v100, 1.0
	v_cvt_scalef32_pk_f32_fp4 v[138:139], v100, 1.0 op_sel:[1,0,0]
	v_cvt_scalef32_pk_f32_fp4 v[140:141], v100, 1.0 op_sel:[0,1,0]
	v_cvt_scalef32_pk_f32_fp4 v[142:143], v100, 1.0 op_sel:[1,1,0]
	v_pk_fma_f32 v[194:195], s[74:75], v[136:137], v[194:195] op_sel_hi:[0,1,1]
	v_pk_fma_f32 v[196:197], s[74:75], v[138:139], v[196:197] op_sel_hi:[0,1,1]
	v_pk_fma_f32 v[198:199], s[74:75], v[140:141], v[198:199] op_sel_hi:[0,1,1]
	v_pk_fma_f32 v[200:201], s[74:75], v[142:143], v[200:201] op_sel_hi:[0,1,1]
	s_waitcnt lgkmcnt(0)
	v_cvt_scalef32_pk_f32_fp4 v[136:137], v101, 1.0
	v_cvt_scalef32_pk_f32_fp4 v[138:139], v101, 1.0 op_sel:[1,0,0]
	v_cvt_scalef32_pk_f32_fp4 v[140:141], v101, 1.0 op_sel:[0,1,0]
	v_cvt_scalef32_pk_f32_fp4 v[142:143], v101, 1.0 op_sel:[1,1,0]
	v_pk_fma_f32 v[202:203], s[74:75], v[136:137], v[202:203] op_sel_hi:[0,1,1]
	v_pk_fma_f32 v[204:205], s[74:75], v[138:139], v[204:205] op_sel_hi:[0,1,1]
	v_pk_fma_f32 v[206:207], s[74:75], v[140:141], v[206:207] op_sel_hi:[0,1,1]
	v_pk_fma_f32 v[208:209], s[74:75], v[142:143], v[208:209] op_sel_hi:[0,1,1]
	v_cvt_scalef32_pk_f32_fp4 v[136:137], v102, 1.0
	v_cvt_scalef32_pk_f32_fp4 v[138:139], v102, 1.0 op_sel:[1,0,0]
	v_cvt_scalef32_pk_f32_fp4 v[140:141], v102, 1.0 op_sel:[0,1,0]
	v_cvt_scalef32_pk_f32_fp4 v[142:143], v102, 1.0 op_sel:[1,1,0]
	v_pk_fma_f32 v[210:211], s[74:75], v[136:137], v[210:211] op_sel_hi:[0,1,1]
	v_pk_fma_f32 v[212:213], s[74:75], v[138:139], v[212:213] op_sel_hi:[0,1,1]
	v_pk_fma_f32 v[214:215], s[74:75], v[140:141], v[214:215] op_sel_hi:[0,1,1]
	v_pk_fma_f32 v[216:217], s[74:75], v[142:143], v[216:217] op_sel_hi:[0,1,1]
	v_cvt_scalef32_pk_f32_fp4 v[136:137], v103, 1.0
	v_cvt_scalef32_pk_f32_fp4 v[138:139], v103, 1.0 op_sel:[1,0,0]
	v_cvt_scalef32_pk_f32_fp4 v[140:141], v103, 1.0 op_sel:[0,1,0]
	v_cvt_scalef32_pk_f32_fp4 v[142:143], v103, 1.0 op_sel:[1,1,0]
	v_pk_fma_f32 v[218:219], s[74:75], v[136:137], v[218:219] op_sel_hi:[0,1,1]
	v_pk_fma_f32 v[220:221], s[74:75], v[138:139], v[220:221] op_sel_hi:[0,1,1]
	v_pk_fma_f32 v[222:223], s[74:75], v[140:141], v[222:223] op_sel_hi:[0,1,1]
	v_pk_fma_f32 v[224:225], s[74:75], v[142:143], v[224:225] op_sel_hi:[0,1,1]
	v_cvt_scalef32_pk_f32_fp4 v[136:137], v104, 1.0
	v_cvt_scalef32_pk_f32_fp4 v[138:139], v104, 1.0 op_sel:[1,0,0]
	v_cvt_scalef32_pk_f32_fp4 v[140:141], v104, 1.0 op_sel:[0,1,0]
	v_cvt_scalef32_pk_f32_fp4 v[142:143], v104, 1.0 op_sel:[1,1,0]
	v_pk_fma_f32 v[226:227], s[74:75], v[136:137], v[226:227] op_sel_hi:[0,1,1]
	v_pk_fma_f32 v[228:229], s[74:75], v[138:139], v[228:229] op_sel_hi:[0,1,1]
	v_pk_fma_f32 v[230:231], s[74:75], v[140:141], v[230:231] op_sel_hi:[0,1,1]
	v_pk_fma_f32 v[232:233], s[74:75], v[142:143], v[232:233] op_sel_hi:[0,1,1]
	v_cvt_scalef32_pk_f32_fp4 v[136:137], v105, 1.0
	v_cvt_scalef32_pk_f32_fp4 v[138:139], v105, 1.0 op_sel:[1,0,0]
	v_cvt_scalef32_pk_f32_fp4 v[140:141], v105, 1.0 op_sel:[0,1,0]
	v_cvt_scalef32_pk_f32_fp4 v[142:143], v105, 1.0 op_sel:[1,1,0]
	v_pk_fma_f32 v[234:235], s[74:75], v[136:137], v[234:235] op_sel_hi:[0,1,1]
	v_pk_fma_f32 v[236:237], s[74:75], v[138:139], v[236:237] op_sel_hi:[0,1,1]
	v_pk_fma_f32 v[238:239], s[74:75], v[140:141], v[238:239] op_sel_hi:[0,1,1]
	v_pk_fma_f32 v[240:241], s[74:75], v[142:143], v[240:241] op_sel_hi:[0,1,1]
.Lpvt6E:
	s_add_i32 s32, s46, 7
	s_bitcmp1_b64 s[70:71], s32
	s_cbranch_scc1 .Lpvt7B
	s_add_i32 s47, s46, 8
	s_and_b32 s47, s47, 7
	s_lshl_b32 s47, s47, 11
	s_add_i32 s77, s33, s47
	v_add_u32_e32 v4, s77, v70
	s_add_i32 s32, s46, 7
	v_readlane_b32 s74, v123, s32
	s_waitcnt vmcnt(2)
	ds_read_b128 v[98:101], v4
	ds_read_b128 v[102:105], v4 offset:1024
	v_cvt_scalef32_pk_f32_fp4 v[136:137], v126, 1.0
	v_cvt_scalef32_pk_f32_fp4 v[138:139], v126, 1.0 op_sel:[1,0,0]
	v_cvt_scalef32_pk_f32_fp4 v[140:141], v126, 1.0 op_sel:[0,1,0]
	v_cvt_scalef32_pk_f32_fp4 v[142:143], v126, 1.0 op_sel:[1,1,0]
	v_pk_fma_f32 v[94:95], s[74:75], v[136:137], v[94:95] op_sel_hi:[0,1,1]
	v_pk_fma_f32 v[96:97], s[74:75], v[138:139], v[96:97] op_sel_hi:[0,1,1]
	v_pk_fma_f32 v[92:93], s[74:75], v[140:141], v[92:93] op_sel_hi:[0,1,1]
	v_pk_fma_f32 v[90:91], s[74:75], v[142:143], v[90:91] op_sel_hi:[0,1,1]
	v_cvt_scalef32_pk_f32_fp4 v[136:137], v127, 1.0
	v_cvt_scalef32_pk_f32_fp4 v[138:139], v127, 1.0 op_sel:[1,0,0]
	v_cvt_scalef32_pk_f32_fp4 v[140:141], v127, 1.0 op_sel:[0,1,0]
	v_cvt_scalef32_pk_f32_fp4 v[142:143], v127, 1.0 op_sel:[1,1,0]
	v_pk_fma_f32 v[88:89], s[74:75], v[136:137], v[88:89] op_sel_hi:[0,1,1]
	v_pk_fma_f32 v[86:87], s[74:75], v[138:139], v[86:87] op_sel_hi:[0,1,1]
	v_pk_fma_f32 v[84:85], s[74:75], v[140:141], v[84:85] op_sel_hi:[0,1,1]
	v_pk_fma_f32 v[82:83], s[74:75], v[142:143], v[82:83] op_sel_hi:[0,1,1]
	v_cvt_scalef32_pk_f32_fp4 v[136:137], v128, 1.0
	v_cvt_scalef32_pk_f32_fp4 v[138:139], v128, 1.0 op_sel:[1,0,0]
	v_cvt_scalef32_pk_f32_fp4 v[140:141], v128, 1.0 op_sel:[0,1,0]
	v_cvt_scalef32_pk_f32_fp4 v[142:143], v128, 1.0 op_sel:[1,1,0]
	v_pk_fma_f32 v[64:65], s[74:75], v[136:137], v[64:65] op_sel_hi:[0,1,1]
	v_pk_fma_f32 v[80:81], s[74:75], v[138:139], v[80:81] op_sel_hi:[0,1,1]
	v_pk_fma_f32 v[62:63], s[74:75], v[140:141], v[62:63] op_sel_hi:[0,1,1]
	v_pk_fma_f32 v[60:61], s[74:75], v[142:143], v[60:61] op_sel_hi:[0,1,1]
	s_waitcnt lgkmcnt(0)
	v_cvt_scalef32_pk_f32_fp4 v[136:137], v129, 1.0
	v_cvt_scalef32_pk_f32_fp4 v[138:139], v129, 1.0 op_sel:[1,0,0]
	v_cvt_scalef32_pk_f32_fp4 v[140:141], v129, 1.0 op_sel:[0,1,0]
	v_cvt_scalef32_pk_f32_fp4 v[142:143], v129, 1.0 op_sel:[1,1,0]
	v_pk_fma_f32 v[58:59], s[74:75], v[136:137], v[58:59] op_sel_hi:[0,1,1]
	v_pk_fma_f32 v[56:57], s[74:75], v[138:139], v[56:57] op_sel_hi:[0,1,1]
	v_pk_fma_f32 v[54:55], s[74:75], v[140:141], v[54:55] op_sel_hi:[0,1,1]
	v_pk_fma_f32 v[52:53], s[74:75], v[142:143], v[52:53] op_sel_hi:[0,1,1]
	v_cvt_scalef32_pk_f32_fp4 v[136:137], v130, 1.0
	v_cvt_scalef32_pk_f32_fp4 v[138:139], v130, 1.0 op_sel:[1,0,0]
	v_cvt_scalef32_pk_f32_fp4 v[140:141], v130, 1.0 op_sel:[0,1,0]
	v_cvt_scalef32_pk_f32_fp4 v[142:143], v130, 1.0 op_sel:[1,1,0]
	v_pk_fma_f32 v[50:51], s[74:75], v[136:137], v[50:51] op_sel_hi:[0,1,1]
	v_pk_fma_f32 v[48:49], s[74:75], v[138:139], v[48:49] op_sel_hi:[0,1,1]
	v_pk_fma_f32 v[46:47], s[74:75], v[140:141], v[46:47] op_sel_hi:[0,1,1]
	v_pk_fma_f32 v[44:45], s[74:75], v[142:143], v[44:45] op_sel_hi:[0,1,1]
	v_cvt_scalef32_pk_f32_fp4 v[136:137], v131, 1.0
	v_cvt_scalef32_pk_f32_fp4 v[138:139], v131, 1.0 op_sel:[1,0,0]
	v_cvt_scalef32_pk_f32_fp4 v[140:141], v131, 1.0 op_sel:[0,1,0]
	v_cvt_scalef32_pk_f32_fp4 v[142:143], v131, 1.0 op_sel:[1,1,0]
	v_pk_fma_f32 v[42:43], s[74:75], v[136:137], v[42:43] op_sel_hi:[0,1,1]
	v_pk_fma_f32 v[40:41], s[74:75], v[138:139], v[40:41] op_sel_hi:[0,1,1]
	v_pk_fma_f32 v[38:39], s[74:75], v[140:141], v[38:39] op_sel_hi:[0,1,1]
	v_pk_fma_f32 v[36:37], s[74:75], v[142:143], v[36:37] op_sel_hi:[0,1,1]
	v_cvt_scalef32_pk_f32_fp4 v[136:137], v132, 1.0
	v_cvt_scalef32_pk_f32_fp4 v[138:139], v132, 1.0 op_sel:[1,0,0]
	v_cvt_scalef32_pk_f32_fp4 v[140:141], v132, 1.0 op_sel:[0,1,0]
	v_cvt_scalef32_pk_f32_fp4 v[142:143], v132, 1.0 op_sel:[1,1,0]
	v_pk_fma_f32 v[32:33], s[74:75], v[136:137], v[32:33] op_sel_hi:[0,1,1]
	v_pk_fma_f32 v[34:35], s[74:75], v[138:139], v[34:35] op_sel_hi:[0,1,1]
	v_pk_fma_f32 v[30:31], s[74:75], v[140:141], v[30:31] op_sel_hi:[0,1,1]
	v_pk_fma_f32 v[28:29], s[74:75], v[142:143], v[28:29] op_sel_hi:[0,1,1]
	v_cvt_scalef32_pk_f32_fp4 v[136:137], v133, 1.0
	v_cvt_scalef32_pk_f32_fp4 v[138:139], v133, 1.0 op_sel:[1,0,0]
	v_cvt_scalef32_pk_f32_fp4 v[140:141], v133, 1.0 op_sel:[0,1,0]
	v_cvt_scalef32_pk_f32_fp4 v[142:143], v133, 1.0 op_sel:[1,1,0]
	v_pk_fma_f32 v[26:27], s[74:75], v[136:137], v[26:27] op_sel_hi:[0,1,1]
	v_pk_fma_f32 v[24:25], s[74:75], v[138:139], v[24:25] op_sel_hi:[0,1,1]
	v_pk_fma_f32 v[20:21], s[74:75], v[140:141], v[20:21] op_sel_hi:[0,1,1]
	v_pk_fma_f32 v[22:23], s[74:75], v[142:143], v[22:23] op_sel_hi:[0,1,1]
	s_branch .Lpvt7E
.Lpvt7B:
	s_add_i32 s47, s46, 8
	s_and_b32 s47, s47, 7
	s_lshl_b32 s47, s47, 11
	s_add_i32 s77, s33, s47
	v_add_u32_e32 v4, s77, v70
	s_add_i32 s32, s46, 7
	v_readlane_b32 s74, v123, s32
	s_waitcnt vmcnt(2)
	ds_read_b128 v[98:101], v4
	ds_read_b128 v[102:105], v4 offset:1024
	v_cvt_scalef32_pk_f32_fp4 v[136:137], v126, 1.0
	v_cvt_scalef32_pk_f32_fp4 v[138:139], v126, 1.0 op_sel:[1,0,0]
	v_cvt_scalef32_pk_f32_fp4 v[140:141], v126, 1.0 op_sel:[0,1,0]
	v_cvt_scalef32_pk_f32_fp4 v[142:143], v126, 1.0 op_sel:[1,1,0]
	v_pk_fma_f32 v[178:179], s[74:75], v[136:137], v[178:179] op_sel_hi:[0,1,1]
	v_pk_fma_f32 v[180:181], s[74:75], v[138:139], v[180:181] op_sel_hi:[0,1,1]
	v_pk_fma_f32 v[182:183], s[74:75], v[140:141], v[182:183] op_sel_hi:[0,1,1]
	v_pk_fma_f32 v[184:185], s[74:75], v[142:143], v[184:185] op_sel_hi:[0,1,1]
	v_cvt_scalef32_pk_f32_fp4 v[136:137], v127, 1.0
	v_cvt_scalef32_pk_f32_fp4 v[138:139], v127, 1.0 op_sel:[1,0,0]
	v_cvt_scalef32_pk_f32_fp4 v[140:141], v127, 1.0 op_sel:[0,1,0]
	v_cvt_scalef32_pk_f32_fp4 v[142:143], v127, 1.0 op_sel:[1,1,0]
	v_pk_fma_f32 v[186:187], s[74:75], v[136:137], v[186:187] op_sel_hi:[0,1,1]
	v_pk_fma_f32 v[188:189], s[74:75], v[138:139], v[188:189] op_sel_hi:[0,1,1]
	v_pk_fma_f32 v[190:191], s[74:75], v[140:141], v[190:191] op_sel_hi:[0,1,1]
	v_pk_fma_f32 v[192:193], s[74:75], v[142:143], v[192:193] op_sel_hi:[0,1,1]
	v_cvt_scalef32_pk_f32_fp4 v[136:137], v128, 1.0
	v_cvt_scalef32_pk_f32_fp4 v[138:139], v128, 1.0 op_sel:[1,0,0]
	v_cvt_scalef32_pk_f32_fp4 v[140:141], v128, 1.0 op_sel:[0,1,0]
	v_cvt_scalef32_pk_f32_fp4 v[142:143], v128, 1.0 op_sel:[1,1,0]
	v_pk_fma_f32 v[194:195], s[74:75], v[136:137], v[194:195] op_sel_hi:[0,1,1]
	v_pk_fma_f32 v[196:197], s[74:75], v[138:139], v[196:197] op_sel_hi:[0,1,1]
	v_pk_fma_f32 v[198:199], s[74:75], v[140:141], v[198:199] op_sel_hi:[0,1,1]
	v_pk_fma_f32 v[200:201], s[74:75], v[142:143], v[200:201] op_sel_hi:[0,1,1]
	s_waitcnt lgkmcnt(0)
	v_cvt_scalef32_pk_f32_fp4 v[136:137], v129, 1.0
	v_cvt_scalef32_pk_f32_fp4 v[138:139], v129, 1.0 op_sel:[1,0,0]
	v_cvt_scalef32_pk_f32_fp4 v[140:141], v129, 1.0 op_sel:[0,1,0]
	v_cvt_scalef32_pk_f32_fp4 v[142:143], v129, 1.0 op_sel:[1,1,0]
	v_pk_fma_f32 v[202:203], s[74:75], v[136:137], v[202:203] op_sel_hi:[0,1,1]
	v_pk_fma_f32 v[204:205], s[74:75], v[138:139], v[204:205] op_sel_hi:[0,1,1]
	v_pk_fma_f32 v[206:207], s[74:75], v[140:141], v[206:207] op_sel_hi:[0,1,1]
	v_pk_fma_f32 v[208:209], s[74:75], v[142:143], v[208:209] op_sel_hi:[0,1,1]
	v_cvt_scalef32_pk_f32_fp4 v[136:137], v130, 1.0
	v_cvt_scalef32_pk_f32_fp4 v[138:139], v130, 1.0 op_sel:[1,0,0]
	v_cvt_scalef32_pk_f32_fp4 v[140:141], v130, 1.0 op_sel:[0,1,0]
	v_cvt_scalef32_pk_f32_fp4 v[142:143], v130, 1.0 op_sel:[1,1,0]
	v_pk_fma_f32 v[210:211], s[74:75], v[136:137], v[210:211] op_sel_hi:[0,1,1]
	v_pk_fma_f32 v[212:213], s[74:75], v[138:139], v[212:213] op_sel_hi:[0,1,1]
	v_pk_fma_f32 v[214:215], s[74:75], v[140:141], v[214:215] op_sel_hi:[0,1,1]
	v_pk_fma_f32 v[216:217], s[74:75], v[142:143], v[216:217] op_sel_hi:[0,1,1]
	v_cvt_scalef32_pk_f32_fp4 v[136:137], v131, 1.0
	v_cvt_scalef32_pk_f32_fp4 v[138:139], v131, 1.0 op_sel:[1,0,0]
	v_cvt_scalef32_pk_f32_fp4 v[140:141], v131, 1.0 op_sel:[0,1,0]
	v_cvt_scalef32_pk_f32_fp4 v[142:143], v131, 1.0 op_sel:[1,1,0]
	v_pk_fma_f32 v[218:219], s[74:75], v[136:137], v[218:219] op_sel_hi:[0,1,1]
	v_pk_fma_f32 v[220:221], s[74:75], v[138:139], v[220:221] op_sel_hi:[0,1,1]
	v_pk_fma_f32 v[222:223], s[74:75], v[140:141], v[222:223] op_sel_hi:[0,1,1]
	v_pk_fma_f32 v[224:225], s[74:75], v[142:143], v[224:225] op_sel_hi:[0,1,1]
	v_cvt_scalef32_pk_f32_fp4 v[136:137], v132, 1.0
	v_cvt_scalef32_pk_f32_fp4 v[138:139], v132, 1.0 op_sel:[1,0,0]
	v_cvt_scalef32_pk_f32_fp4 v[140:141], v132, 1.0 op_sel:[0,1,0]
	v_cvt_scalef32_pk_f32_fp4 v[142:143], v132, 1.0 op_sel:[1,1,0]
	v_pk_fma_f32 v[226:227], s[74:75], v[136:137], v[226:227] op_sel_hi:[0,1,1]
	v_pk_fma_f32 v[228:229], s[74:75], v[138:139], v[228:229] op_sel_hi:[0,1,1]
	v_pk_fma_f32 v[230:231], s[74:75], v[140:141], v[230:231] op_sel_hi:[0,1,1]
	v_pk_fma_f32 v[232:233], s[74:75], v[142:143], v[232:233] op_sel_hi:[0,1,1]
	v_cvt_scalef32_pk_f32_fp4 v[136:137], v133, 1.0
	v_cvt_scalef32_pk_f32_fp4 v[138:139], v133, 1.0 op_sel:[1,0,0]
	v_cvt_scalef32_pk_f32_fp4 v[140:141], v133, 1.0 op_sel:[0,1,0]
	v_cvt_scalef32_pk_f32_fp4 v[142:143], v133, 1.0 op_sel:[1,1,0]
	v_pk_fma_f32 v[234:235], s[74:75], v[136:137], v[234:235] op_sel_hi:[0,1,1]
	v_pk_fma_f32 v[236:237], s[74:75], v[138:139], v[236:237] op_sel_hi:[0,1,1]
	v_pk_fma_f32 v[238:239], s[74:75], v[140:141], v[238:239] op_sel_hi:[0,1,1]
	v_pk_fma_f32 v[240:241], s[74:75], v[142:143], v[240:241] op_sel_hi:[0,1,1]
.Lpvt7E:
	s_add_i32 s32, s46, 8
	s_bitcmp1_b64 s[70:71], s32
	s_cbranch_scc1 .Lpvt8B
	s_add_i32 s47, s46, 9
	s_and_b32 s47, s47, 7
	s_lshl_b32 s47, s47, 11
	s_add_i32 s77, s33, s47
	v_add_u32_e32 v4, s77, v70
	s_add_i32 s32, s46, 8
	v_readlane_b32 s74, v123, s32
	s_waitcnt vmcnt(0)
	ds_read_b128 v[126:129], v4
	ds_read_b128 v[130:133], v4 offset:1024
	v_cvt_scalef32_pk_f32_fp4 v[136:137], v98, 1.0
	v_cvt_scalef32_pk_f32_fp4 v[138:139], v98, 1.0 op_sel:[1,0,0]
	v_cvt_scalef32_pk_f32_fp4 v[140:141], v98, 1.0 op_sel:[0,1,0]
	v_cvt_scalef32_pk_f32_fp4 v[142:143], v98, 1.0 op_sel:[1,1,0]
	v_pk_fma_f32 v[94:95], s[74:75], v[136:137], v[94:95] op_sel_hi:[0,1,1]
	v_pk_fma_f32 v[96:97], s[74:75], v[138:139], v[96:97] op_sel_hi:[0,1,1]
	v_pk_fma_f32 v[92:93], s[74:75], v[140:141], v[92:93] op_sel_hi:[0,1,1]
	v_pk_fma_f32 v[90:91], s[74:75], v[142:143], v[90:91] op_sel_hi:[0,1,1]
	v_cvt_scalef32_pk_f32_fp4 v[136:137], v99, 1.0
	v_cvt_scalef32_pk_f32_fp4 v[138:139], v99, 1.0 op_sel:[1,0,0]
	v_cvt_scalef32_pk_f32_fp4 v[140:141], v99, 1.0 op_sel:[0,1,0]
	v_cvt_scalef32_pk_f32_fp4 v[142:143], v99, 1.0 op_sel:[1,1,0]
	v_pk_fma_f32 v[88:89], s[74:75], v[136:137], v[88:89] op_sel_hi:[0,1,1]
	v_pk_fma_f32 v[86:87], s[74:75], v[138:139], v[86:87] op_sel_hi:[0,1,1]
	v_pk_fma_f32 v[84:85], s[74:75], v[140:141], v[84:85] op_sel_hi:[0,1,1]
	v_pk_fma_f32 v[82:83], s[74:75], v[142:143], v[82:83] op_sel_hi:[0,1,1]
	v_cvt_scalef32_pk_f32_fp4 v[136:137], v100, 1.0
	v_cvt_scalef32_pk_f32_fp4 v[138:139], v100, 1.0 op_sel:[1,0,0]
	v_cvt_scalef32_pk_f32_fp4 v[140:141], v100, 1.0 op_sel:[0,1,0]
	v_cvt_scalef32_pk_f32_fp4 v[142:143], v100, 1.0 op_sel:[1,1,0]
	v_pk_fma_f32 v[64:65], s[74:75], v[136:137], v[64:65] op_sel_hi:[0,1,1]
	v_pk_fma_f32 v[80:81], s[74:75], v[138:139], v[80:81] op_sel_hi:[0,1,1]
	v_pk_fma_f32 v[62:63], s[74:75], v[140:141], v[62:63] op_sel_hi:[0,1,1]
	v_pk_fma_f32 v[60:61], s[74:75], v[142:143], v[60:61] op_sel_hi:[0,1,1]
	s_waitcnt lgkmcnt(0)
	v_cvt_scalef32_pk_f32_fp4 v[136:137], v101, 1.0
	v_cvt_scalef32_pk_f32_fp4 v[138:139], v101, 1.0 op_sel:[1,0,0]
	v_cvt_scalef32_pk_f32_fp4 v[140:141], v101, 1.0 op_sel:[0,1,0]
	v_cvt_scalef32_pk_f32_fp4 v[142:143], v101, 1.0 op_sel:[1,1,0]
	v_pk_fma_f32 v[58:59], s[74:75], v[136:137], v[58:59] op_sel_hi:[0,1,1]
	v_pk_fma_f32 v[56:57], s[74:75], v[138:139], v[56:57] op_sel_hi:[0,1,1]
	v_pk_fma_f32 v[54:55], s[74:75], v[140:141], v[54:55] op_sel_hi:[0,1,1]
	v_pk_fma_f32 v[52:53], s[74:75], v[142:143], v[52:53] op_sel_hi:[0,1,1]
	v_cvt_scalef32_pk_f32_fp4 v[136:137], v102, 1.0
	v_cvt_scalef32_pk_f32_fp4 v[138:139], v102, 1.0 op_sel:[1,0,0]
	v_cvt_scalef32_pk_f32_fp4 v[140:141], v102, 1.0 op_sel:[0,1,0]
	v_cvt_scalef32_pk_f32_fp4 v[142:143], v102, 1.0 op_sel:[1,1,0]
	v_pk_fma_f32 v[50:51], s[74:75], v[136:137], v[50:51] op_sel_hi:[0,1,1]
	v_pk_fma_f32 v[48:49], s[74:75], v[138:139], v[48:49] op_sel_hi:[0,1,1]
	v_pk_fma_f32 v[46:47], s[74:75], v[140:141], v[46:47] op_sel_hi:[0,1,1]
	v_pk_fma_f32 v[44:45], s[74:75], v[142:143], v[44:45] op_sel_hi:[0,1,1]
	v_cvt_scalef32_pk_f32_fp4 v[136:137], v103, 1.0
	v_cvt_scalef32_pk_f32_fp4 v[138:139], v103, 1.0 op_sel:[1,0,0]
	v_cvt_scalef32_pk_f32_fp4 v[140:141], v103, 1.0 op_sel:[0,1,0]
	v_cvt_scalef32_pk_f32_fp4 v[142:143], v103, 1.0 op_sel:[1,1,0]
	v_pk_fma_f32 v[42:43], s[74:75], v[136:137], v[42:43] op_sel_hi:[0,1,1]
	v_pk_fma_f32 v[40:41], s[74:75], v[138:139], v[40:41] op_sel_hi:[0,1,1]
	v_pk_fma_f32 v[38:39], s[74:75], v[140:141], v[38:39] op_sel_hi:[0,1,1]
	v_pk_fma_f32 v[36:37], s[74:75], v[142:143], v[36:37] op_sel_hi:[0,1,1]
	v_cvt_scalef32_pk_f32_fp4 v[136:137], v104, 1.0
	v_cvt_scalef32_pk_f32_fp4 v[138:139], v104, 1.0 op_sel:[1,0,0]
	v_cvt_scalef32_pk_f32_fp4 v[140:141], v104, 1.0 op_sel:[0,1,0]
	v_cvt_scalef32_pk_f32_fp4 v[142:143], v104, 1.0 op_sel:[1,1,0]
	v_pk_fma_f32 v[32:33], s[74:75], v[136:137], v[32:33] op_sel_hi:[0,1,1]
	v_pk_fma_f32 v[34:35], s[74:75], v[138:139], v[34:35] op_sel_hi:[0,1,1]
	v_pk_fma_f32 v[30:31], s[74:75], v[140:141], v[30:31] op_sel_hi:[0,1,1]
	v_pk_fma_f32 v[28:29], s[74:75], v[142:143], v[28:29] op_sel_hi:[0,1,1]
	v_cvt_scalef32_pk_f32_fp4 v[136:137], v105, 1.0
	v_cvt_scalef32_pk_f32_fp4 v[138:139], v105, 1.0 op_sel:[1,0,0]
	v_cvt_scalef32_pk_f32_fp4 v[140:141], v105, 1.0 op_sel:[0,1,0]
	v_cvt_scalef32_pk_f32_fp4 v[142:143], v105, 1.0 op_sel:[1,1,0]
	v_pk_fma_f32 v[26:27], s[74:75], v[136:137], v[26:27] op_sel_hi:[0,1,1]
	v_pk_fma_f32 v[24:25], s[74:75], v[138:139], v[24:25] op_sel_hi:[0,1,1]
	v_pk_fma_f32 v[20:21], s[74:75], v[140:141], v[20:21] op_sel_hi:[0,1,1]
	v_pk_fma_f32 v[22:23], s[74:75], v[142:143], v[22:23] op_sel_hi:[0,1,1]
	s_branch .Lpvt8E
.Lpvt8B:
	s_add_i32 s47, s46, 9
	s_and_b32 s47, s47, 7
	s_lshl_b32 s47, s47, 11
	s_add_i32 s77, s33, s47
	v_add_u32_e32 v4, s77, v70
	s_add_i32 s32, s46, 8
	v_readlane_b32 s74, v123, s32
	s_waitcnt vmcnt(0)
	ds_read_b128 v[126:129], v4
	ds_read_b128 v[130:133], v4 offset:1024
	v_cvt_scalef32_pk_f32_fp4 v[136:137], v98, 1.0
	v_cvt_scalef32_pk_f32_fp4 v[138:139], v98, 1.0 op_sel:[1,0,0]
	v_cvt_scalef32_pk_f32_fp4 v[140:141], v98, 1.0 op_sel:[0,1,0]
	v_cvt_scalef32_pk_f32_fp4 v[142:143], v98, 1.0 op_sel:[1,1,0]
	v_pk_fma_f32 v[178:179], s[74:75], v[136:137], v[178:179] op_sel_hi:[0,1,1]
	v_pk_fma_f32 v[180:181], s[74:75], v[138:139], v[180:181] op_sel_hi:[0,1,1]
	v_pk_fma_f32 v[182:183], s[74:75], v[140:141], v[182:183] op_sel_hi:[0,1,1]
	v_pk_fma_f32 v[184:185], s[74:75], v[142:143], v[184:185] op_sel_hi:[0,1,1]
	v_cvt_scalef32_pk_f32_fp4 v[136:137], v99, 1.0
	v_cvt_scalef32_pk_f32_fp4 v[138:139], v99, 1.0 op_sel:[1,0,0]
	v_cvt_scalef32_pk_f32_fp4 v[140:141], v99, 1.0 op_sel:[0,1,0]
	v_cvt_scalef32_pk_f32_fp4 v[142:143], v99, 1.0 op_sel:[1,1,0]
	v_pk_fma_f32 v[186:187], s[74:75], v[136:137], v[186:187] op_sel_hi:[0,1,1]
	v_pk_fma_f32 v[188:189], s[74:75], v[138:139], v[188:189] op_sel_hi:[0,1,1]
	v_pk_fma_f32 v[190:191], s[74:75], v[140:141], v[190:191] op_sel_hi:[0,1,1]
	v_pk_fma_f32 v[192:193], s[74:75], v[142:143], v[192:193] op_sel_hi:[0,1,1]
	v_cvt_scalef32_pk_f32_fp4 v[136:137], v100, 1.0
	v_cvt_scalef32_pk_f32_fp4 v[138:139], v100, 1.0 op_sel:[1,0,0]
	v_cvt_scalef32_pk_f32_fp4 v[140:141], v100, 1.0 op_sel:[0,1,0]
	v_cvt_scalef32_pk_f32_fp4 v[142:143], v100, 1.0 op_sel:[1,1,0]
	v_pk_fma_f32 v[194:195], s[74:75], v[136:137], v[194:195] op_sel_hi:[0,1,1]
	v_pk_fma_f32 v[196:197], s[74:75], v[138:139], v[196:197] op_sel_hi:[0,1,1]
	v_pk_fma_f32 v[198:199], s[74:75], v[140:141], v[198:199] op_sel_hi:[0,1,1]
	v_pk_fma_f32 v[200:201], s[74:75], v[142:143], v[200:201] op_sel_hi:[0,1,1]
	s_waitcnt lgkmcnt(0)
	v_cvt_scalef32_pk_f32_fp4 v[136:137], v101, 1.0
	v_cvt_scalef32_pk_f32_fp4 v[138:139], v101, 1.0 op_sel:[1,0,0]
	v_cvt_scalef32_pk_f32_fp4 v[140:141], v101, 1.0 op_sel:[0,1,0]
	v_cvt_scalef32_pk_f32_fp4 v[142:143], v101, 1.0 op_sel:[1,1,0]
	v_pk_fma_f32 v[202:203], s[74:75], v[136:137], v[202:203] op_sel_hi:[0,1,1]
	v_pk_fma_f32 v[204:205], s[74:75], v[138:139], v[204:205] op_sel_hi:[0,1,1]
	v_pk_fma_f32 v[206:207], s[74:75], v[140:141], v[206:207] op_sel_hi:[0,1,1]
	v_pk_fma_f32 v[208:209], s[74:75], v[142:143], v[208:209] op_sel_hi:[0,1,1]
	v_cvt_scalef32_pk_f32_fp4 v[136:137], v102, 1.0
	v_cvt_scalef32_pk_f32_fp4 v[138:139], v102, 1.0 op_sel:[1,0,0]
	v_cvt_scalef32_pk_f32_fp4 v[140:141], v102, 1.0 op_sel:[0,1,0]
	v_cvt_scalef32_pk_f32_fp4 v[142:143], v102, 1.0 op_sel:[1,1,0]
	v_pk_fma_f32 v[210:211], s[74:75], v[136:137], v[210:211] op_sel_hi:[0,1,1]
	v_pk_fma_f32 v[212:213], s[74:75], v[138:139], v[212:213] op_sel_hi:[0,1,1]
	v_pk_fma_f32 v[214:215], s[74:75], v[140:141], v[214:215] op_sel_hi:[0,1,1]
	v_pk_fma_f32 v[216:217], s[74:75], v[142:143], v[216:217] op_sel_hi:[0,1,1]
	v_cvt_scalef32_pk_f32_fp4 v[136:137], v103, 1.0
	v_cvt_scalef32_pk_f32_fp4 v[138:139], v103, 1.0 op_sel:[1,0,0]
	v_cvt_scalef32_pk_f32_fp4 v[140:141], v103, 1.0 op_sel:[0,1,0]
	v_cvt_scalef32_pk_f32_fp4 v[142:143], v103, 1.0 op_sel:[1,1,0]
	v_pk_fma_f32 v[218:219], s[74:75], v[136:137], v[218:219] op_sel_hi:[0,1,1]
	v_pk_fma_f32 v[220:221], s[74:75], v[138:139], v[220:221] op_sel_hi:[0,1,1]
	v_pk_fma_f32 v[222:223], s[74:75], v[140:141], v[222:223] op_sel_hi:[0,1,1]
	v_pk_fma_f32 v[224:225], s[74:75], v[142:143], v[224:225] op_sel_hi:[0,1,1]
	v_cvt_scalef32_pk_f32_fp4 v[136:137], v104, 1.0
	v_cvt_scalef32_pk_f32_fp4 v[138:139], v104, 1.0 op_sel:[1,0,0]
	v_cvt_scalef32_pk_f32_fp4 v[140:141], v104, 1.0 op_sel:[0,1,0]
	v_cvt_scalef32_pk_f32_fp4 v[142:143], v104, 1.0 op_sel:[1,1,0]
	v_pk_fma_f32 v[226:227], s[74:75], v[136:137], v[226:227] op_sel_hi:[0,1,1]
	v_pk_fma_f32 v[228:229], s[74:75], v[138:139], v[228:229] op_sel_hi:[0,1,1]
	v_pk_fma_f32 v[230:231], s[74:75], v[140:141], v[230:231] op_sel_hi:[0,1,1]
	v_pk_fma_f32 v[232:233], s[74:75], v[142:143], v[232:233] op_sel_hi:[0,1,1]
	v_cvt_scalef32_pk_f32_fp4 v[136:137], v105, 1.0
	v_cvt_scalef32_pk_f32_fp4 v[138:139], v105, 1.0 op_sel:[1,0,0]
	v_cvt_scalef32_pk_f32_fp4 v[140:141], v105, 1.0 op_sel:[0,1,0]
	v_cvt_scalef32_pk_f32_fp4 v[142:143], v105, 1.0 op_sel:[1,1,0]
	v_pk_fma_f32 v[234:235], s[74:75], v[136:137], v[234:235] op_sel_hi:[0,1,1]
	v_pk_fma_f32 v[236:237], s[74:75], v[138:139], v[236:237] op_sel_hi:[0,1,1]
	v_pk_fma_f32 v[238:239], s[74:75], v[140:141], v[238:239] op_sel_hi:[0,1,1]
	v_pk_fma_f32 v[240:241], s[74:75], v[142:143], v[240:241] op_sel_hi:[0,1,1]
.Lpvt8E:
	s_add_i32 s32, s46, 9
	s_bitcmp1_b64 s[70:71], s32
	s_cbranch_scc1 .Lpvt9B
	s_add_i32 s32, s46, 9
	v_readlane_b32 s74, v123, s32
	s_nop 1
	v_cvt_scalef32_pk_f32_fp4 v[136:137], v126, 1.0
	v_cvt_scalef32_pk_f32_fp4 v[138:139], v126, 1.0 op_sel:[1,0,0]
	v_cvt_scalef32_pk_f32_fp4 v[140:141], v126, 1.0 op_sel:[0,1,0]
	v_cvt_scalef32_pk_f32_fp4 v[142:143], v126, 1.0 op_sel:[1,1,0]
	v_pk_fma_f32 v[94:95], s[74:75], v[136:137], v[94:95] op_sel_hi:[0,1,1]
	v_pk_fma_f32 v[96:97], s[74:75], v[138:139], v[96:97] op_sel_hi:[0,1,1]
	v_pk_fma_f32 v[92:93], s[74:75], v[140:141], v[92:93] op_sel_hi:[0,1,1]
	v_pk_fma_f32 v[90:91], s[74:75], v[142:143], v[90:91] op_sel_hi:[0,1,1]
	v_cvt_scalef32_pk_f32_fp4 v[136:137], v127, 1.0
	v_cvt_scalef32_pk_f32_fp4 v[138:139], v127, 1.0 op_sel:[1,0,0]
	v_cvt_scalef32_pk_f32_fp4 v[140:141], v127, 1.0 op_sel:[0,1,0]
	v_cvt_scalef32_pk_f32_fp4 v[142:143], v127, 1.0 op_sel:[1,1,0]
	v_pk_fma_f32 v[88:89], s[74:75], v[136:137], v[88:89] op_sel_hi:[0,1,1]
	v_pk_fma_f32 v[86:87], s[74:75], v[138:139], v[86:87] op_sel_hi:[0,1,1]
	v_pk_fma_f32 v[84:85], s[74:75], v[140:141], v[84:85] op_sel_hi:[0,1,1]
	v_pk_fma_f32 v[82:83], s[74:75], v[142:143], v[82:83] op_sel_hi:[0,1,1]
	v_cvt_scalef32_pk_f32_fp4 v[136:137], v128, 1.0
	v_cvt_scalef32_pk_f32_fp4 v[138:139], v128, 1.0 op_sel:[1,0,0]
	v_cvt_scalef32_pk_f32_fp4 v[140:141], v128, 1.0 op_sel:[0,1,0]
	v_cvt_scalef32_pk_f32_fp4 v[142:143], v128, 1.0 op_sel:[1,1,0]
	v_pk_fma_f32 v[64:65], s[74:75], v[136:137], v[64:65] op_sel_hi:[0,1,1]
	v_pk_fma_f32 v[80:81], s[74:75], v[138:139], v[80:81] op_sel_hi:[0,1,1]
	v_pk_fma_f32 v[62:63], s[74:75], v[140:141], v[62:63] op_sel_hi:[0,1,1]
	v_pk_fma_f32 v[60:61], s[74:75], v[142:143], v[60:61] op_sel_hi:[0,1,1]
	v_cvt_scalef32_pk_f32_fp4 v[136:137], v129, 1.0
	v_cvt_scalef32_pk_f32_fp4 v[138:139], v129, 1.0 op_sel:[1,0,0]
	v_cvt_scalef32_pk_f32_fp4 v[140:141], v129, 1.0 op_sel:[0,1,0]
	v_cvt_scalef32_pk_f32_fp4 v[142:143], v129, 1.0 op_sel:[1,1,0]
	v_pk_fma_f32 v[58:59], s[74:75], v[136:137], v[58:59] op_sel_hi:[0,1,1]
	v_pk_fma_f32 v[56:57], s[74:75], v[138:139], v[56:57] op_sel_hi:[0,1,1]
	v_pk_fma_f32 v[54:55], s[74:75], v[140:141], v[54:55] op_sel_hi:[0,1,1]
	v_pk_fma_f32 v[52:53], s[74:75], v[142:143], v[52:53] op_sel_hi:[0,1,1]
	v_cvt_scalef32_pk_f32_fp4 v[136:137], v130, 1.0
	v_cvt_scalef32_pk_f32_fp4 v[138:139], v130, 1.0 op_sel:[1,0,0]
	v_cvt_scalef32_pk_f32_fp4 v[140:141], v130, 1.0 op_sel:[0,1,0]
	v_cvt_scalef32_pk_f32_fp4 v[142:143], v130, 1.0 op_sel:[1,1,0]
	v_pk_fma_f32 v[50:51], s[74:75], v[136:137], v[50:51] op_sel_hi:[0,1,1]
	v_pk_fma_f32 v[48:49], s[74:75], v[138:139], v[48:49] op_sel_hi:[0,1,1]
	v_pk_fma_f32 v[46:47], s[74:75], v[140:141], v[46:47] op_sel_hi:[0,1,1]
	v_pk_fma_f32 v[44:45], s[74:75], v[142:143], v[44:45] op_sel_hi:[0,1,1]
	v_cvt_scalef32_pk_f32_fp4 v[136:137], v131, 1.0
	v_cvt_scalef32_pk_f32_fp4 v[138:139], v131, 1.0 op_sel:[1,0,0]
	v_cvt_scalef32_pk_f32_fp4 v[140:141], v131, 1.0 op_sel:[0,1,0]
	v_cvt_scalef32_pk_f32_fp4 v[142:143], v131, 1.0 op_sel:[1,1,0]
	v_pk_fma_f32 v[42:43], s[74:75], v[136:137], v[42:43] op_sel_hi:[0,1,1]
	v_pk_fma_f32 v[40:41], s[74:75], v[138:139], v[40:41] op_sel_hi:[0,1,1]
	v_pk_fma_f32 v[38:39], s[74:75], v[140:141], v[38:39] op_sel_hi:[0,1,1]
	v_pk_fma_f32 v[36:37], s[74:75], v[142:143], v[36:37] op_sel_hi:[0,1,1]
	v_cvt_scalef32_pk_f32_fp4 v[136:137], v132, 1.0
	v_cvt_scalef32_pk_f32_fp4 v[138:139], v132, 1.0 op_sel:[1,0,0]
	v_cvt_scalef32_pk_f32_fp4 v[140:141], v132, 1.0 op_sel:[0,1,0]
	v_cvt_scalef32_pk_f32_fp4 v[142:143], v132, 1.0 op_sel:[1,1,0]
	v_pk_fma_f32 v[32:33], s[74:75], v[136:137], v[32:33] op_sel_hi:[0,1,1]
	v_pk_fma_f32 v[34:35], s[74:75], v[138:139], v[34:35] op_sel_hi:[0,1,1]
	v_pk_fma_f32 v[30:31], s[74:75], v[140:141], v[30:31] op_sel_hi:[0,1,1]
	v_pk_fma_f32 v[28:29], s[74:75], v[142:143], v[28:29] op_sel_hi:[0,1,1]
	v_cvt_scalef32_pk_f32_fp4 v[136:137], v133, 1.0
	v_cvt_scalef32_pk_f32_fp4 v[138:139], v133, 1.0 op_sel:[1,0,0]
	v_cvt_scalef32_pk_f32_fp4 v[140:141], v133, 1.0 op_sel:[0,1,0]
	v_cvt_scalef32_pk_f32_fp4 v[142:143], v133, 1.0 op_sel:[1,1,0]
	v_pk_fma_f32 v[26:27], s[74:75], v[136:137], v[26:27] op_sel_hi:[0,1,1]
	v_pk_fma_f32 v[24:25], s[74:75], v[138:139], v[24:25] op_sel_hi:[0,1,1]
	v_pk_fma_f32 v[20:21], s[74:75], v[140:141], v[20:21] op_sel_hi:[0,1,1]
	v_pk_fma_f32 v[22:23], s[74:75], v[142:143], v[22:23] op_sel_hi:[0,1,1]
	s_branch .Lpvt9E
.Lpvt9B:
	s_add_i32 s32, s46, 9
	v_readlane_b32 s74, v123, s32
	s_nop 1
	v_cvt_scalef32_pk_f32_fp4 v[136:137], v126, 1.0
	v_cvt_scalef32_pk_f32_fp4 v[138:139], v126, 1.0 op_sel:[1,0,0]
	v_cvt_scalef32_pk_f32_fp4 v[140:141], v126, 1.0 op_sel:[0,1,0]
	v_cvt_scalef32_pk_f32_fp4 v[142:143], v126, 1.0 op_sel:[1,1,0]
	v_pk_fma_f32 v[178:179], s[74:75], v[136:137], v[178:179] op_sel_hi:[0,1,1]
	v_pk_fma_f32 v[180:181], s[74:75], v[138:139], v[180:181] op_sel_hi:[0,1,1]
	v_pk_fma_f32 v[182:183], s[74:75], v[140:141], v[182:183] op_sel_hi:[0,1,1]
	v_pk_fma_f32 v[184:185], s[74:75], v[142:143], v[184:185] op_sel_hi:[0,1,1]
	v_cvt_scalef32_pk_f32_fp4 v[136:137], v127, 1.0
	v_cvt_scalef32_pk_f32_fp4 v[138:139], v127, 1.0 op_sel:[1,0,0]
	v_cvt_scalef32_pk_f32_fp4 v[140:141], v127, 1.0 op_sel:[0,1,0]
	v_cvt_scalef32_pk_f32_fp4 v[142:143], v127, 1.0 op_sel:[1,1,0]
	v_pk_fma_f32 v[186:187], s[74:75], v[136:137], v[186:187] op_sel_hi:[0,1,1]
	v_pk_fma_f32 v[188:189], s[74:75], v[138:139], v[188:189] op_sel_hi:[0,1,1]
	v_pk_fma_f32 v[190:191], s[74:75], v[140:141], v[190:191] op_sel_hi:[0,1,1]
	v_pk_fma_f32 v[192:193], s[74:75], v[142:143], v[192:193] op_sel_hi:[0,1,1]
	v_cvt_scalef32_pk_f32_fp4 v[136:137], v128, 1.0
	v_cvt_scalef32_pk_f32_fp4 v[138:139], v128, 1.0 op_sel:[1,0,0]
	v_cvt_scalef32_pk_f32_fp4 v[140:141], v128, 1.0 op_sel:[0,1,0]
	v_cvt_scalef32_pk_f32_fp4 v[142:143], v128, 1.0 op_sel:[1,1,0]
	v_pk_fma_f32 v[194:195], s[74:75], v[136:137], v[194:195] op_sel_hi:[0,1,1]
	v_pk_fma_f32 v[196:197], s[74:75], v[138:139], v[196:197] op_sel_hi:[0,1,1]
	v_pk_fma_f32 v[198:199], s[74:75], v[140:141], v[198:199] op_sel_hi:[0,1,1]
	v_pk_fma_f32 v[200:201], s[74:75], v[142:143], v[200:201] op_sel_hi:[0,1,1]
	v_cvt_scalef32_pk_f32_fp4 v[136:137], v129, 1.0
	v_cvt_scalef32_pk_f32_fp4 v[138:139], v129, 1.0 op_sel:[1,0,0]
	v_cvt_scalef32_pk_f32_fp4 v[140:141], v129, 1.0 op_sel:[0,1,0]
	v_cvt_scalef32_pk_f32_fp4 v[142:143], v129, 1.0 op_sel:[1,1,0]
	v_pk_fma_f32 v[202:203], s[74:75], v[136:137], v[202:203] op_sel_hi:[0,1,1]
	v_pk_fma_f32 v[204:205], s[74:75], v[138:139], v[204:205] op_sel_hi:[0,1,1]
	v_pk_fma_f32 v[206:207], s[74:75], v[140:141], v[206:207] op_sel_hi:[0,1,1]
	v_pk_fma_f32 v[208:209], s[74:75], v[142:143], v[208:209] op_sel_hi:[0,1,1]
	v_cvt_scalef32_pk_f32_fp4 v[136:137], v130, 1.0
	v_cvt_scalef32_pk_f32_fp4 v[138:139], v130, 1.0 op_sel:[1,0,0]
	v_cvt_scalef32_pk_f32_fp4 v[140:141], v130, 1.0 op_sel:[0,1,0]
	v_cvt_scalef32_pk_f32_fp4 v[142:143], v130, 1.0 op_sel:[1,1,0]
	v_pk_fma_f32 v[210:211], s[74:75], v[136:137], v[210:211] op_sel_hi:[0,1,1]
	v_pk_fma_f32 v[212:213], s[74:75], v[138:139], v[212:213] op_sel_hi:[0,1,1]
	v_pk_fma_f32 v[214:215], s[74:75], v[140:141], v[214:215] op_sel_hi:[0,1,1]
	v_pk_fma_f32 v[216:217], s[74:75], v[142:143], v[216:217] op_sel_hi:[0,1,1]
	v_cvt_scalef32_pk_f32_fp4 v[136:137], v131, 1.0
	v_cvt_scalef32_pk_f32_fp4 v[138:139], v131, 1.0 op_sel:[1,0,0]
	v_cvt_scalef32_pk_f32_fp4 v[140:141], v131, 1.0 op_sel:[0,1,0]
	v_cvt_scalef32_pk_f32_fp4 v[142:143], v131, 1.0 op_sel:[1,1,0]
	v_pk_fma_f32 v[218:219], s[74:75], v[136:137], v[218:219] op_sel_hi:[0,1,1]
	v_pk_fma_f32 v[220:221], s[74:75], v[138:139], v[220:221] op_sel_hi:[0,1,1]
	v_pk_fma_f32 v[222:223], s[74:75], v[140:141], v[222:223] op_sel_hi:[0,1,1]
	v_pk_fma_f32 v[224:225], s[74:75], v[142:143], v[224:225] op_sel_hi:[0,1,1]
	v_cvt_scalef32_pk_f32_fp4 v[136:137], v132, 1.0
	v_cvt_scalef32_pk_f32_fp4 v[138:139], v132, 1.0 op_sel:[1,0,0]
	v_cvt_scalef32_pk_f32_fp4 v[140:141], v132, 1.0 op_sel:[0,1,0]
	v_cvt_scalef32_pk_f32_fp4 v[142:143], v132, 1.0 op_sel:[1,1,0]
	v_pk_fma_f32 v[226:227], s[74:75], v[136:137], v[226:227] op_sel_hi:[0,1,1]
	v_pk_fma_f32 v[228:229], s[74:75], v[138:139], v[228:229] op_sel_hi:[0,1,1]
	v_pk_fma_f32 v[230:231], s[74:75], v[140:141], v[230:231] op_sel_hi:[0,1,1]
	v_pk_fma_f32 v[232:233], s[74:75], v[142:143], v[232:233] op_sel_hi:[0,1,1]
	v_cvt_scalef32_pk_f32_fp4 v[136:137], v133, 1.0
	v_cvt_scalef32_pk_f32_fp4 v[138:139], v133, 1.0 op_sel:[1,0,0]
	v_cvt_scalef32_pk_f32_fp4 v[140:141], v133, 1.0 op_sel:[0,1,0]
	v_cvt_scalef32_pk_f32_fp4 v[142:143], v133, 1.0 op_sel:[1,1,0]
	v_pk_fma_f32 v[234:235], s[74:75], v[136:137], v[234:235] op_sel_hi:[0,1,1]
	v_pk_fma_f32 v[236:237], s[74:75], v[138:139], v[236:237] op_sel_hi:[0,1,1]
	v_pk_fma_f32 v[238:239], s[74:75], v[140:141], v[238:239] op_sel_hi:[0,1,1]
	v_pk_fma_f32 v[240:241], s[74:75], v[142:143], v[240:241] op_sel_hi:[0,1,1]
; DI void peer_token(LAS unsigned char* ring, const bf16* x1row, float inv2, const float* nffn, const int* ex, const float* pg, const unsigned char* U6, const unsigned char* V6,
;                    const float* usc, const float* vsc, float* orow, int lane) {
;     ...
;     const float ysc = 1.0f;
;     asm volatile("s_waitcnt vmcnt(0)" ::: "memory");
; #pragma unroll
;     for (int i = 0; i < 16; ++i) {
;         const v2u aw = *(const v2u*)(x1row + i * 256 + lane * 4);
;         *(f32x4*)(orow + i * 256 + lane * 4) = (f32x4){bflo(aw.x) + ysc * y[2 * i].x, bfhi(aw.x) + ysc * y[2 * i].y, bflo(aw.y) + ysc * y[2 * i + 1].x, bfhi(aw.y) + ysc * y[2 * i + 1].y};
;     }
; __global__ void __launch_bounds__(NTHREADS, 2) fwd(Args args) {
;     ...
; #pragma unroll 1
;             for (int j = 0; j < 4; ++j) { const int t = tb * 32 + wave * 4 + j;
;                 peer_token(lds + wave * (4 * RSLOT), XB + (size_t)t * DM, inv2[t], norm_ffn, experts + (size_t)t * 128, pgates + (size_t)t * 128, U8, V8, usc, vsc, out + (size_t)t * DM, lane); }
.Lpvt9E:
	s_lshl_b32 s46, s76, 1
	s_add_i32 s46, s46, s97
	s_ashr_i32 s47, s46, 31
	s_lshl_b64 s[46:47], s[46:47], 13
	v_lshl_add_u64 v[16:17], v[68:69], 0, s[46:47]
	s_mov_b64 s[46:47], 0x2000
	v_lshl_add_u64 v[2:3], v[16:17], 0, s[46:47]
	s_mov_b64 s[46:47], 0x3000
	v_lshl_add_u64 v[4:5], v[16:17], 0, s[46:47]
	global_load_dwordx2 v[98:99], v[2:3], off
	global_load_dwordx2 v[100:101], v[2:3], off offset:512
	global_load_dwordx2 v[102:103], v[2:3], off offset:1024
	global_load_dwordx2 v[104:105], v[2:3], off offset:1536
	global_load_dwordx2 v[126:127], v[2:3], off offset:2048
	global_load_dwordx2 v[128:129], v[2:3], off offset:2560
	global_load_dwordx2 v[130:131], v[2:3], off offset:3072
	global_load_dwordx2 v[132:133], v[2:3], off offset:3584
	global_load_dwordx2 v[136:137], v[4:5], off
	global_load_dwordx2 v[138:139], v[4:5], off offset:512
	global_load_dwordx2 v[140:141], v[4:5], off offset:1024
	global_load_dwordx2 v[142:143], v[4:5], off offset:1536
	global_load_dwordx2 v[8:9], v[4:5], off offset:2048
	global_load_dwordx2 v[10:11], v[4:5], off offset:2560
	global_load_dwordx2 v[12:13], v[4:5], off offset:3072
	global_load_dwordx2 v[14:15], v[4:5], off offset:3584
	v_lshl_add_u64 v[18:19], s[44:45], 2, v[76:77]
	s_mov_b64 s[46:47], 0x2000
	v_lshl_add_u64 v[6:7], v[18:19], 0, s[46:47]
	s_mov_b64 s[46:47], 0x3000
	v_lshl_add_u64 v[16:17], v[18:19], 0, s[46:47]
	s_mov_b64 s[46:47], 0x4000
	v_lshl_add_u64 v[112:113], v[18:19], 0, s[46:47]
	s_mov_b64 s[46:47], 0x6000
	v_lshl_add_u64 v[242:243], v[18:19], 0, s[46:47]
	s_mov_b64 s[46:47], 0x7000
	v_lshl_add_u64 v[124:125], v[18:19], 0, s[46:47]
	v_lshlrev_b32_e32 v2, 16, v146
	v_and_b32_e32 v3, 0xffff0000, v146
	v_lshlrev_b32_e32 v4, 16, v147
	v_and_b32_e32 v5, 0xffff0000, v147
	v_pk_add_f32 v[2:3], v[94:95], v[2:3]
	v_pk_add_f32 v[4:5], v[96:97], v[4:5]
	global_store_dwordx4 v[18:19], v[2:5], off
	v_lshlrev_b32_e32 v244, 16, v148
	v_and_b32_e32 v245, 0xffff0000, v148
	v_lshlrev_b32_e32 v246, 16, v149
	v_and_b32_e32 v247, 0xffff0000, v149
	v_pk_add_f32 v[244:245], v[92:93], v[244:245]
	v_pk_add_f32 v[246:247], v[90:91], v[246:247]
	global_store_dwordx4 v[18:19], v[244:247], off offset:1024
	v_lshlrev_b32_e32 v120, 16, v150
	v_and_b32_e32 v121, 0xffff0000, v150
	v_lshlrev_b32_e32 v122, 16, v151
	v_and_b32_e32 v123, 0xffff0000, v151
	v_pk_add_f32 v[120:121], v[88:89], v[120:121]
	v_pk_add_f32 v[122:123], v[86:87], v[122:123]
	global_store_dwordx4 v[18:19], v[120:123], off offset:2048
	v_lshlrev_b32_e32 v2, 16, v152
	v_and_b32_e32 v3, 0xffff0000, v152
	v_lshlrev_b32_e32 v4, 16, v153
	v_and_b32_e32 v5, 0xffff0000, v153
	v_pk_add_f32 v[2:3], v[84:85], v[2:3]
	v_pk_add_f32 v[4:5], v[82:83], v[4:5]
	global_store_dwordx4 v[18:19], v[2:5], off offset:3072
	v_lshlrev_b32_e32 v244, 16, v154
	v_and_b32_e32 v245, 0xffff0000, v154
	v_lshlrev_b32_e32 v246, 16, v155
	v_and_b32_e32 v247, 0xffff0000, v155
	v_pk_add_f32 v[244:245], v[64:65], v[244:245]
	v_pk_add_f32 v[246:247], v[80:81], v[246:247]
	global_store_dwordx4 v[6:7], v[244:247], off offset:-4096
	v_lshlrev_b32_e32 v120, 16, v156
	v_and_b32_e32 v121, 0xffff0000, v156
	v_lshlrev_b32_e32 v122, 16, v157
	v_and_b32_e32 v123, 0xffff0000, v157
	v_pk_add_f32 v[120:121], v[62:63], v[120:121]
	v_pk_add_f32 v[122:123], v[60:61], v[122:123]
	global_store_dwordx4 v[6:7], v[120:123], off offset:-3072
	v_lshlrev_b32_e32 v2, 16, v158
	v_and_b32_e32 v3, 0xffff0000, v158
	v_lshlrev_b32_e32 v4, 16, v159
	v_and_b32_e32 v5, 0xffff0000, v159
	v_pk_add_f32 v[2:3], v[58:59], v[2:3]
	v_pk_add_f32 v[4:5], v[56:57], v[4:5]
	global_store_dwordx4 v[6:7], v[2:5], off offset:-2048
	v_lshlrev_b32_e32 v244, 16, v160
	v_and_b32_e32 v245, 0xffff0000, v160
	v_lshlrev_b32_e32 v246, 16, v161
	v_and_b32_e32 v247, 0xffff0000, v161
	v_pk_add_f32 v[244:245], v[54:55], v[244:245]
	v_pk_add_f32 v[246:247], v[52:53], v[246:247]
	global_store_dwordx4 v[6:7], v[244:247], off offset:-1024
	v_lshlrev_b32_e32 v120, 16, v162
	v_and_b32_e32 v121, 0xffff0000, v162
	v_lshlrev_b32_e32 v122, 16, v163
	v_and_b32_e32 v123, 0xffff0000, v163
	v_pk_add_f32 v[120:121], v[50:51], v[120:121]
	v_pk_add_f32 v[122:123], v[48:49], v[122:123]
	global_store_dwordx4 v[6:7], v[120:123], off
	v_lshlrev_b32_e32 v2, 16, v164
	v_and_b32_e32 v3, 0xffff0000, v164
	v_lshlrev_b32_e32 v4, 16, v165
	v_and_b32_e32 v5, 0xffff0000, v165
	v_pk_add_f32 v[2:3], v[46:47], v[2:3]
	v_pk_add_f32 v[4:5], v[44:45], v[4:5]
	global_store_dwordx4 v[6:7], v[2:5], off offset:1024
	v_lshlrev_b32_e32 v244, 16, v166
	v_and_b32_e32 v245, 0xffff0000, v166
	v_lshlrev_b32_e32 v246, 16, v167
	v_and_b32_e32 v247, 0xffff0000, v167
	v_pk_add_f32 v[244:245], v[42:43], v[244:245]
	v_pk_add_f32 v[246:247], v[40:41], v[246:247]
	global_store_dwordx4 v[6:7], v[244:247], off offset:2048
	v_lshlrev_b32_e32 v120, 16, v168
	v_and_b32_e32 v121, 0xffff0000, v168
	v_lshlrev_b32_e32 v122, 16, v169
	v_and_b32_e32 v123, 0xffff0000, v169
	v_pk_add_f32 v[120:121], v[38:39], v[120:121]
	v_pk_add_f32 v[122:123], v[36:37], v[122:123]
	global_store_dwordx4 v[6:7], v[120:123], off offset:3072
	v_lshlrev_b32_e32 v2, 16, v170
	v_and_b32_e32 v3, 0xffff0000, v170
	v_lshlrev_b32_e32 v4, 16, v171
	v_and_b32_e32 v5, 0xffff0000, v171
	v_pk_add_f32 v[2:3], v[32:33], v[2:3]
	v_pk_add_f32 v[4:5], v[34:35], v[4:5]
	global_store_dwordx4 v[16:17], v[2:5], off
	v_lshlrev_b32_e32 v244, 16, v172
	v_and_b32_e32 v245, 0xffff0000, v172
	v_lshlrev_b32_e32 v246, 16, v173
	v_and_b32_e32 v247, 0xffff0000, v173
	v_pk_add_f32 v[244:245], v[30:31], v[244:245]
	v_pk_add_f32 v[246:247], v[28:29], v[246:247]
	global_store_dwordx4 v[16:17], v[244:247], off offset:1024
	v_lshlrev_b32_e32 v120, 16, v174
	v_and_b32_e32 v121, 0xffff0000, v174
	v_lshlrev_b32_e32 v122, 16, v175
	v_and_b32_e32 v123, 0xffff0000, v175
	v_pk_add_f32 v[120:121], v[26:27], v[120:121]
	v_pk_add_f32 v[122:123], v[24:25], v[122:123]
	global_store_dwordx4 v[16:17], v[120:123], off offset:2048
	v_lshlrev_b32_e32 v2, 16, v176
	v_and_b32_e32 v3, 0xffff0000, v176
	v_lshlrev_b32_e32 v4, 16, v177
	v_and_b32_e32 v5, 0xffff0000, v177
	v_pk_add_f32 v[2:3], v[20:21], v[2:3]
	v_pk_add_f32 v[4:5], v[22:23], v[4:5]
	global_store_dwordx4 v[16:17], v[2:5], off offset:3072
	s_waitcnt vmcnt(16)
; DI void peer_token(LAS unsigned char* ring, const bf16* x1row, float inv2, const float* nffn, const int* ex, const float* pg, const unsigned char* U6, const unsigned char* V6,
;                    const float* usc, const float* vsc, float* orow, int lane) {
;     ...
; #pragma unroll
;     for (int i = 0; i < 16; ++i) {
;         const v2u aw = *(const v2u*)(x1row + i * 256 + lane * 4);
;         *(f32x4*)(orow + i * 256 + lane * 4) = (f32x4){bflo(aw.x) + ysc * y[2 * i].x, bfhi(aw.x) + ysc * y[2 * i].y, bflo(aw.y) + ysc * y[2 * i + 1].x, bfhi(aw.y) + ysc * y[2 * i + 1].y};
;     }
; __global__ void __launch_bounds__(NTHREADS, 2) fwd(Args args) {
;     ...
;         for (int tb = bid; tb < SEQ / 32; tb += G) {
;             routing_block(lds, QB, skb, experts, pgates, tb);
;             asm volatile("s_waitcnt vmcnt(0)" ::: "memory");
;             __syncthreads();
; #pragma unroll 1
;             for (int j = 0; j < 4; ++j) { const int t = tb * 32 + wave * 4 + j;
;                 peer_token(lds + wave * (4 * RSLOT), XB + (size_t)t * DM, inv2[t], norm_ffn, experts + (size_t)t * 128, pgates + (size_t)t * 128, U8, V8, usc, vsc, out + (size_t)t * DM, lane); }
;             __syncthreads();
;         }
	v_lshlrev_b32_e32 v244, 16, v98
	v_and_b32_e32 v245, 0xffff0000, v98
	v_lshlrev_b32_e32 v246, 16, v99
	v_and_b32_e32 v247, 0xffff0000, v99
	v_pk_add_f32 v[244:245], v[178:179], v[244:245]
	v_pk_add_f32 v[246:247], v[180:181], v[246:247]
	global_store_dwordx4 v[112:113], v[244:247], off
	v_lshlrev_b32_e32 v120, 16, v100
	v_and_b32_e32 v121, 0xffff0000, v100
	v_lshlrev_b32_e32 v122, 16, v101
	v_and_b32_e32 v123, 0xffff0000, v101
	v_pk_add_f32 v[120:121], v[182:183], v[120:121]
	v_pk_add_f32 v[122:123], v[184:185], v[122:123]
	global_store_dwordx4 v[112:113], v[120:123], off offset:1024
	v_lshlrev_b32_e32 v2, 16, v102
	v_and_b32_e32 v3, 0xffff0000, v102
	v_lshlrev_b32_e32 v4, 16, v103
	v_and_b32_e32 v5, 0xffff0000, v103
	v_pk_add_f32 v[2:3], v[186:187], v[2:3]
	v_pk_add_f32 v[4:5], v[188:189], v[4:5]
	global_store_dwordx4 v[112:113], v[2:5], off offset:2048
	v_lshlrev_b32_e32 v244, 16, v104
	v_and_b32_e32 v245, 0xffff0000, v104
	v_lshlrev_b32_e32 v246, 16, v105
	v_and_b32_e32 v247, 0xffff0000, v105
	v_pk_add_f32 v[244:245], v[190:191], v[244:245]
	v_pk_add_f32 v[246:247], v[192:193], v[246:247]
	global_store_dwordx4 v[112:113], v[244:247], off offset:3072
	v_lshlrev_b32_e32 v120, 16, v126
	v_and_b32_e32 v121, 0xffff0000, v126
	v_lshlrev_b32_e32 v122, 16, v127
	v_and_b32_e32 v123, 0xffff0000, v127
	v_pk_add_f32 v[120:121], v[194:195], v[120:121]
	v_pk_add_f32 v[122:123], v[196:197], v[122:123]
	global_store_dwordx4 v[242:243], v[120:123], off offset:-4096
	v_lshlrev_b32_e32 v2, 16, v128
	v_and_b32_e32 v3, 0xffff0000, v128
	v_lshlrev_b32_e32 v4, 16, v129
	v_and_b32_e32 v5, 0xffff0000, v129
	v_pk_add_f32 v[2:3], v[198:199], v[2:3]
	v_pk_add_f32 v[4:5], v[200:201], v[4:5]
	global_store_dwordx4 v[242:243], v[2:5], off offset:-3072
	v_lshlrev_b32_e32 v244, 16, v130
	v_and_b32_e32 v245, 0xffff0000, v130
	v_lshlrev_b32_e32 v246, 16, v131
	v_and_b32_e32 v247, 0xffff0000, v131
	v_pk_add_f32 v[244:245], v[202:203], v[244:245]
	v_pk_add_f32 v[246:247], v[204:205], v[246:247]
	global_store_dwordx4 v[242:243], v[244:247], off offset:-2048
	v_lshlrev_b32_e32 v120, 16, v132
	v_and_b32_e32 v121, 0xffff0000, v132
	v_lshlrev_b32_e32 v122, 16, v133
	v_and_b32_e32 v123, 0xffff0000, v133
	v_pk_add_f32 v[120:121], v[206:207], v[120:121]
	v_pk_add_f32 v[122:123], v[208:209], v[122:123]
	global_store_dwordx4 v[242:243], v[120:123], off offset:-1024
	v_lshlrev_b32_e32 v2, 16, v136
	v_and_b32_e32 v3, 0xffff0000, v136
	v_lshlrev_b32_e32 v4, 16, v137
	v_and_b32_e32 v5, 0xffff0000, v137
	v_pk_add_f32 v[2:3], v[210:211], v[2:3]
	v_pk_add_f32 v[4:5], v[212:213], v[4:5]
	global_store_dwordx4 v[242:243], v[2:5], off
	v_lshlrev_b32_e32 v244, 16, v138
	v_and_b32_e32 v245, 0xffff0000, v138
	v_lshlrev_b32_e32 v246, 16, v139
	v_and_b32_e32 v247, 0xffff0000, v139
	v_pk_add_f32 v[244:245], v[214:215], v[244:245]
	v_pk_add_f32 v[246:247], v[216:217], v[246:247]
	global_store_dwordx4 v[242:243], v[244:247], off offset:1024
	v_lshlrev_b32_e32 v120, 16, v140
	v_and_b32_e32 v121, 0xffff0000, v140
	v_lshlrev_b32_e32 v122, 16, v141
	v_and_b32_e32 v123, 0xffff0000, v141
	v_pk_add_f32 v[120:121], v[218:219], v[120:121]
	v_pk_add_f32 v[122:123], v[220:221], v[122:123]
	global_store_dwordx4 v[242:243], v[120:123], off offset:2048
	v_lshlrev_b32_e32 v2, 16, v142
	v_and_b32_e32 v3, 0xffff0000, v142
	v_lshlrev_b32_e32 v4, 16, v143
	v_and_b32_e32 v5, 0xffff0000, v143
	v_pk_add_f32 v[2:3], v[222:223], v[2:3]
	v_pk_add_f32 v[4:5], v[224:225], v[4:5]
	global_store_dwordx4 v[242:243], v[2:5], off offset:3072
	v_lshlrev_b32_e32 v244, 16, v8
	v_and_b32_e32 v245, 0xffff0000, v8
	v_lshlrev_b32_e32 v246, 16, v9
	v_and_b32_e32 v247, 0xffff0000, v9
	v_pk_add_f32 v[244:245], v[226:227], v[244:245]
	v_pk_add_f32 v[246:247], v[228:229], v[246:247]
	global_store_dwordx4 v[124:125], v[244:247], off
	v_lshlrev_b32_e32 v120, 16, v10
	v_and_b32_e32 v121, 0xffff0000, v10
	v_lshlrev_b32_e32 v122, 16, v11
	v_and_b32_e32 v123, 0xffff0000, v11
	v_pk_add_f32 v[120:121], v[230:231], v[120:121]
	v_pk_add_f32 v[122:123], v[232:233], v[122:123]
	global_store_dwordx4 v[124:125], v[120:123], off offset:1024
	v_lshlrev_b32_e32 v2, 16, v12
	v_and_b32_e32 v3, 0xffff0000, v12
	v_lshlrev_b32_e32 v4, 16, v13
	v_and_b32_e32 v5, 0xffff0000, v13
	v_pk_add_f32 v[2:3], v[234:235], v[2:3]
	v_pk_add_f32 v[4:5], v[236:237], v[4:5]
	global_store_dwordx4 v[124:125], v[2:5], off offset:2048
	v_lshlrev_b32_e32 v244, 16, v14
	v_and_b32_e32 v245, 0xffff0000, v14
	v_lshlrev_b32_e32 v246, 16, v15
	v_and_b32_e32 v247, 0xffff0000, v15
	v_pk_add_f32 v[244:245], v[238:239], v[244:245]
	v_pk_add_f32 v[246:247], v[240:241], v[246:247]
	global_store_dwordx4 v[124:125], v[244:247], off offset:3072
	s_add_i32 s76, s76, 1
	s_cmp_eq_u32 s76, 2
	s_cbranch_scc0 .LBB0_901
	s_add_i32 s2, s2, s3
	s_cmpk_gt_i32 s2, 0xff
	s_barrier
	s_cbranch_scc0 .LBB0_892
